# read-once streaming loads in P0/P4/P8/P13 marked nt, plus earlier edits
# speedup vs baseline: 1.0288x; 1.0129x over previous
.LBB0_32:
	s_load_dwordx2 s[10:11], s[10:11], 0x0
	v_lshlrev_b32_e32 v0, 2, v72
	v_and_b32_e32 v73, 28, v0
	v_mov_b32_e32 v4, 0
	v_or_b32_e32 v0, s14, v73
	v_mov_b32_e32 v6, v4
	v_mov_b32_e32 v7, v4
	v_ashrrev_i32_e32 v74, 3, v72
	v_ashrrev_i32_e32 v1, 31, v0
	v_mov_b32_e32 v5, v4
	v_mov_b64_e32 v[14:15], v[6:7]
	v_mov_b64_e32 v[10:11], v[6:7]
	v_cmp_gt_i32_e32 vcc, s13, v0
	v_add_u32_e32 v30, s12, v74
	s_waitcnt lgkmcnt(0)
	v_lshl_add_u64 v[28:29], v[0:1], 2, s[10:11]
	v_mov_b64_e32 v[12:13], v[4:5]
	v_mov_b64_e32 v[8:9], v[4:5]
	s_and_saveexec_b64 s[10:11], vcc
	s_cbranch_execz .LBB0_34
	v_mad_u64_u32 v[0:1], s[14:15], v30, s13, 0
	v_ashrrev_i32_e32 v3, 31, v30
	v_mov_b32_e32 v2, v1
	v_mad_u64_u32 v[2:3], s[14:15], v3, s13, v[2:3]
	v_mov_b32_e32 v1, v2
	v_add_u32_e32 v2, 8, v30
	v_ashrrev_i32_e32 v9, 31, v2
	v_mad_u64_u32 v[2:3], s[14:15], v2, s13, 0
	v_mov_b32_e32 v8, v3
	v_mad_u64_u32 v[8:9], s[14:15], v9, s13, v[8:9]
	v_lshl_add_u64 v[0:1], v[0:1], 2, v[28:29]
	v_mov_b32_e32 v3, v8
	v_lshl_add_u64 v[2:3], v[2:3], 2, v[28:29]
	global_load_dwordx4 v[12:15], v[0:1], off nt
	global_load_dwordx4 v[8:11], v[2:3], off nt
.LBB0_34:
	s_or_b64 exec, exec, s[10:11]
	v_mov_b64_e32 v[18:19], v[6:7]
	v_mov_b64_e32 v[16:17], v[4:5]
	s_and_saveexec_b64 s[10:11], vcc
	s_cbranch_execz .LBB0_36
	v_add_u32_e32 v0, 16, v30
	v_ashrrev_i32_e32 v3, 31, v0
	v_mad_u64_u32 v[0:1], s[14:15], v0, s13, 0
	v_mov_b32_e32 v2, v1
	v_mad_u64_u32 v[2:3], s[14:15], v3, s13, v[2:3]
	v_mov_b32_e32 v1, v2
	v_add_u32_e32 v2, 24, v30
	v_ashrrev_i32_e32 v5, 31, v2
	v_mad_u64_u32 v[2:3], s[14:15], v2, s13, 0
	v_mov_b32_e32 v4, v3
	v_mad_u64_u32 v[4:5], s[14:15], v5, s13, v[4:5]
	v_lshl_add_u64 v[0:1], v[0:1], 2, v[28:29]
	v_mov_b32_e32 v3, v4
	v_lshl_add_u64 v[2:3], v[2:3], 2, v[28:29]
	global_load_dwordx4 v[4:7], v[0:1], off nt
	global_load_dwordx4 v[16:19], v[2:3], off nt
.LBB0_36:
	s_or_b64 exec, exec, s[10:11]
	v_mov_b32_e32 v1, 0
	v_mov_b32_e32 v2, v1
	v_mov_b32_e32 v3, v1
	v_mov_b32_e32 v0, v1
	v_mov_b64_e32 v[26:27], v[2:3]
	v_mov_b64_e32 v[22:23], v[2:3]
	v_mov_b64_e32 v[24:25], v[0:1]
	v_mov_b64_e32 v[20:21], v[0:1]
	s_and_saveexec_b64 s[10:11], vcc
	s_cbranch_execz .LBB0_38
	v_add_u32_e32 v0, 32, v30
	v_mad_u64_u32 v[2:3], s[14:15], v0, s13, 0
	v_ashrrev_i32_e32 v20, 31, v0
	v_mov_b32_e32 v0, v3
	v_mad_u64_u32 v[20:21], s[14:15], v20, s13, v[0:1]
	v_add_u32_e32 v0, 40, v30
	v_mov_b32_e32 v3, v20
	v_mad_u64_u32 v[20:21], s[14:15], v0, s13, 0
	v_ashrrev_i32_e32 v22, 31, v0
	v_mov_b32_e32 v0, v21
	v_mad_u64_u32 v[22:23], s[14:15], v22, s13, v[0:1]
	v_lshl_add_u64 v[2:3], v[2:3], 2, v[28:29]
	v_mov_b32_e32 v21, v22
	v_lshl_add_u64 v[32:33], v[20:21], 2, v[28:29]
	global_load_dwordx4 v[24:27], v[2:3], off nt
	global_load_dwordx4 v[20:23], v[32:33], off nt
.LBB0_38:
	s_or_b64 exec, exec, s[10:11]
	v_mov_b32_e32 v32, 0
	v_mov_b32_e32 v33, 0
	v_mov_b32_e32 v34, 0
	v_mov_b32_e32 v35, 0
	v_mov_b32_e32 v36, 0
	v_mov_b32_e32 v37, 0
	v_mov_b32_e32 v38, 0
	v_mov_b32_e32 v39, 0
	s_and_saveexec_b64 s[10:11], vcc
	s_cbranch_execz .LBB0_40
	v_add_u32_e32 v0, 48, v30
	v_mad_u64_u32 v[2:3], s[14:15], v0, s13, 0
	v_ashrrev_i32_e32 v31, 31, v0
	v_mov_b32_e32 v0, v3
	v_mad_u64_u32 v[32:33], s[14:15], v31, s13, v[0:1]
	v_add_u32_e32 v0, 56, v30
	v_mad_u64_u32 v[30:31], s[14:15], v0, s13, 0
	v_mov_b32_e32 v3, v32
	v_ashrrev_i32_e32 v32, 31, v0
	v_mov_b32_e32 v0, v31
	v_mad_u64_u32 v[32:33], s[12:13], v32, s13, v[0:1]
	v_lshl_add_u64 v[2:3], v[2:3], 2, v[28:29]
	v_mov_b32_e32 v31, v32
	v_lshl_add_u64 v[28:29], v[30:31], 2, v[28:29]
	global_load_dwordx4 v[36:39], v[2:3], off nt
	global_load_dwordx4 v[32:35], v[28:29], off nt

.LBB0_64:
	s_load_dwordx2 s[34:35], s[34:35], 0x0
	v_or_b32_e32 v30, s28, v73
	v_ashrrev_i32_e32 v31, 31, v30
	v_cmp_gt_i32_e32 vcc, s22, v30
	v_mov_b32_e32 v29, v28
	s_waitcnt lgkmcnt(0)
	v_lshl_add_u64 v[82:83], v[30:31], 2, s[34:35]
	v_mov_b32_e32 v30, v28
	v_mov_b32_e32 v31, v28
	v_mov_b64_e32 v[42:43], v[30:31]
	v_mov_b64_e32 v[46:47], v[30:31]
	v_add_u32_e32 v85, s30, v74
	v_mov_b64_e32 v[40:41], v[28:29]
	v_mov_b64_e32 v[44:45], v[28:29]
	s_and_saveexec_b64 s[28:29], vcc
	s_cbranch_execz .LBB0_66
	v_mad_u64_u32 v[40:41], s[30:31], v85, s22, 0
	v_ashrrev_i32_e32 v43, 31, v85
	v_mov_b32_e32 v42, v41
	v_mad_u64_u32 v[42:43], s[30:31], v43, s22, v[42:43]
	v_mov_b32_e32 v41, v42
	v_add_u32_e32 v42, 8, v85
	v_ashrrev_i32_e32 v45, 31, v42
	v_mad_u64_u32 v[42:43], s[30:31], v42, s22, 0
	v_mov_b32_e32 v44, v43
	v_mad_u64_u32 v[44:45], s[30:31], v45, s22, v[44:45]
	v_mov_b32_e32 v43, v44
	v_lshl_add_u64 v[40:41], v[40:41], 2, v[82:83]
	v_lshl_add_u64 v[44:45], v[42:43], 2, v[82:83]
	global_load_dwordx4 v[40:43], v[40:41], off nt
	s_nop 0
	global_load_dwordx4 v[44:47], v[44:45], off nt
.LBB0_66:
	s_or_b64 exec, exec, s[28:29]
	v_mov_b64_e32 v[50:51], v[30:31]
	v_mov_b64_e32 v[54:55], v[30:31]
	v_mov_b64_e32 v[48:49], v[28:29]
	v_mov_b64_e32 v[52:53], v[28:29]
	s_and_saveexec_b64 s[28:29], vcc
	s_cbranch_execz .LBB0_68
	v_add_u32_e32 v29, 16, v85
	v_mad_u64_u32 v[30:31], s[30:31], v29, s22, 0
	v_ashrrev_i32_e32 v49, 31, v29
	v_mov_b32_e32 v48, v31
	v_mad_u64_u32 v[48:49], s[30:31], v49, s22, v[48:49]
	v_add_u32_e32 v29, 24, v85
	v_mov_b32_e32 v31, v48
	v_mad_u64_u32 v[48:49], s[30:31], v29, s22, 0
	v_ashrrev_i32_e32 v51, 31, v29
	v_mov_b32_e32 v50, v49
	v_mad_u64_u32 v[50:51], s[30:31], v51, s22, v[50:51]
	v_mov_b32_e32 v49, v50
	v_lshl_add_u64 v[30:31], v[30:31], 2, v[82:83]
	v_lshl_add_u64 v[52:53], v[48:49], 2, v[82:83]
	global_load_dwordx4 v[48:51], v[30:31], off nt
	s_nop 0
	global_load_dwordx4 v[52:55], v[52:53], off nt
.LBB0_68:
	s_or_b64 exec, exec, s[28:29]
	v_mov_b32_e32 v30, v28
	v_mov_b32_e32 v31, v28
	v_mov_b32_e32 v29, v28
	v_mov_b64_e32 v[58:59], v[30:31]
	v_mov_b64_e32 v[62:63], v[30:31]
	v_mov_b64_e32 v[56:57], v[28:29]
	v_mov_b64_e32 v[60:61], v[28:29]
	s_and_saveexec_b64 s[28:29], vcc
	s_cbranch_execz .LBB0_70
	v_add_u32_e32 v29, 32, v85
	v_mad_u64_u32 v[30:31], s[30:31], v29, s22, 0
	v_ashrrev_i32_e32 v57, 31, v29
	v_mov_b32_e32 v56, v31
	v_mad_u64_u32 v[56:57], s[30:31], v57, s22, v[56:57]
	v_add_u32_e32 v29, 40, v85
	v_mov_b32_e32 v31, v56
	v_mad_u64_u32 v[56:57], s[30:31], v29, s22, 0
	v_ashrrev_i32_e32 v59, 31, v29
	v_mov_b32_e32 v58, v57
	v_mad_u64_u32 v[58:59], s[30:31], v59, s22, v[58:59]
	v_mov_b32_e32 v57, v58
	v_lshl_add_u64 v[30:31], v[30:31], 2, v[82:83]
	v_lshl_add_u64 v[60:61], v[56:57], 2, v[82:83]
	global_load_dwordx4 v[56:59], v[30:31], off nt
	s_nop 0
	global_load_dwordx4 v[60:63], v[60:61], off nt
.LBB0_70:
	s_or_b64 exec, exec, s[28:29]
	v_mov_b32_e32 v67, 0
	v_mov_b32_e32 v66, 0
	v_mov_b32_e32 v65, 0
	v_mov_b32_e32 v64, 0
	v_mov_b32_e32 v71, 0
	v_mov_b32_e32 v70, 0
	v_mov_b32_e32 v69, 0
	v_mov_b32_e32 v68, 0
	s_and_saveexec_b64 s[28:29], vcc
	s_cbranch_execz .LBB0_41
	v_add_u32_e32 v29, 48, v85
	v_mad_u64_u32 v[30:31], s[30:31], v29, s22, 0
	v_ashrrev_i32_e32 v65, 31, v29
	v_mov_b32_e32 v64, v31
	v_mad_u64_u32 v[64:65], s[30:31], v65, s22, v[64:65]
	v_add_u32_e32 v29, 56, v85
	v_mov_b32_e32 v31, v64
	v_mad_u64_u32 v[64:65], s[30:31], v29, s22, 0
	v_ashrrev_i32_e32 v67, 31, v29
	v_mov_b32_e32 v66, v65
	v_mad_u64_u32 v[66:67], s[30:31], v67, s22, v[66:67]
	v_lshl_add_u64 v[30:31], v[30:31], 2, v[82:83]
	v_mov_b32_e32 v65, v66
	v_lshl_add_u64 v[82:83], v[64:65], 2, v[82:83]
	global_load_dwordx4 v[64:67], v[30:31], off nt
	global_load_dwordx4 v[68:71], v[82:83], off nt
	s_branch .LBB0_41

.LBB0_74:
	v_ashrrev_i32_e32 v4, 11, v0
	v_and_b32_e32 v5, 0x7ff0, v1
	v_add_u32_e32 v4, v5, v4
	v_ashrrev_i32_e32 v5, 31, v4
	v_lshl_add_u64 v[4:5], v[4:5], 2, s[10:11]
	global_load_dword v4, v[4:5], off nt
	v_add_u32_e32 v0, s12, v0
	v_cmp_lt_i32_e32 vcc, s18, v0
	v_add_u32_e32 v1, s13, v1
	s_or_b64 s[16:17], vcc, s[16:17]
	s_waitcnt vmcnt(0)
	global_store_dword v[2:3], v4, off
	v_lshl_add_u64 v[2:3], v[2:3], 0, s[14:15]
	s_andn2_b64 exec, exec, s[16:17]
	s_cbranch_execnz .LBB0_74

.LBB0_77:
	global_load_dwordx4 v[24:27], v[18:19], off offset:-4096 nt
	global_load_dwordx4 v[28:31], v[18:19], off offset:-3072 nt
	global_load_dwordx4 v[32:35], v[18:19], off offset:-2048 nt
	global_load_dwordx4 v[36:39], v[18:19], off offset:-1024 nt
	global_load_dwordx4 v[40:43], v[18:19], off nt
	global_load_dwordx4 v[44:47], v[18:19], off offset:1024 nt
	global_load_dwordx4 v[4:7], v[18:19], off offset:2048 nt
	global_load_dwordx4 v[0:3], v[18:19], off offset:3072 nt
	global_load_dwordx4 v[48:51], v[8:9], off nt
	s_add_i32 s38, s38, s4
	v_lshl_add_u64 v[18:19], v[18:19], 0, s[6:7]
	s_cmpk_lt_i32 s38, 0x4000
	s_waitcnt vmcnt(8)
	v_mul_f32_e32 v52, v25, v25
	v_mul_f32_e32 v53, v27, v27
	s_waitcnt vmcnt(7)
	v_mul_f32_e32 v54, v29, v29
	v_mul_f32_e32 v55, v31, v31
	s_waitcnt vmcnt(6)
	v_mul_f32_e32 v56, v33, v33
	v_mul_f32_e32 v57, v35, v35
	v_fmac_f32_e32 v52, v24, v24
	v_fmac_f32_e32 v53, v26, v26
	v_fmac_f32_e32 v54, v28, v28
	v_fmac_f32_e32 v55, v30, v30
	s_waitcnt vmcnt(5)
	v_mul_f32_e32 v58, v37, v37
	v_mul_f32_e32 v59, v39, v39
	v_fmac_f32_e32 v56, v32, v32
	v_fmac_f32_e32 v57, v34, v34
	v_add_f32_e32 v52, v52, v53
	v_add_f32_e32 v53, v54, v55
	s_waitcnt vmcnt(4)
	v_mul_f32_e32 v60, v41, v41
	v_mul_f32_e32 v61, v43, v43
	v_fmac_f32_e32 v58, v36, v36
	v_fmac_f32_e32 v59, v38, v38
	v_add_f32_e32 v54, v56, v57
	v_add_f32_e32 v52, v52, v53
	s_waitcnt vmcnt(3)
	v_mul_f32_e32 v62, v45, v45
	v_mul_f32_e32 v63, v47, v47
	v_fmac_f32_e32 v60, v40, v40
	v_fmac_f32_e32 v61, v42, v42
	v_add_f32_e32 v55, v58, v59
	v_add_f32_e32 v52, v52, v54
	s_waitcnt vmcnt(2)
	v_mul_f32_e32 v64, v5, v5
	v_mul_f32_e32 v65, v7, v7
	v_fmac_f32_e32 v62, v44, v44
	v_fmac_f32_e32 v63, v46, v46
	v_add_f32_e32 v56, v60, v61
	v_add_f32_e32 v52, v52, v55
	s_waitcnt vmcnt(1)
	v_mul_f32_e32 v66, v1, v1
	v_mul_f32_e32 v67, v3, v3
	v_fmac_f32_e32 v64, v4, v4
	v_fmac_f32_e32 v65, v6, v6
	v_add_f32_e32 v57, v62, v63
	v_add_f32_e32 v52, v52, v56
	v_fmac_f32_e32 v66, v0, v0
	v_fmac_f32_e32 v67, v2, v2
	v_add_f32_e32 v58, v64, v65
	v_add_f32_e32 v52, v52, v57
	v_add_f32_e32 v59, v66, v67
	v_add_f32_e32 v52, v52, v58
	v_add_f32_e32 v52, v52, v59
	ds_swizzle_b32 v53, v52 offset:swizzle(SWAP,1)
	s_waitcnt lgkmcnt(0)
	v_add_f32_e32 v52, v52, v53
	ds_swizzle_b32 v53, v52 offset:swizzle(SWAP,2)
	s_waitcnt lgkmcnt(0)
	v_add_f32_e32 v52, v52, v53
	ds_swizzle_b32 v53, v52 offset:swizzle(SWAP,4)
	s_waitcnt lgkmcnt(0)
	v_add_f32_e32 v52, v52, v53
	ds_swizzle_b32 v53, v52 offset:swizzle(SWAP,8)
	s_waitcnt lgkmcnt(0)
	v_add_f32_e32 v52, v52, v53
	ds_swizzle_b32 v53, v52 offset:swizzle(SWAP,16)
	s_waitcnt lgkmcnt(0)
	v_add_f32_e32 v52, v52, v53
	v_mov_b32_e32 v53, v52
	s_nop 1
	v_permlane32_swap_b32_e32 v52, v53
	v_add_f32_e32 v52, v52, v53
	v_fmamk_f32 v52, v52, 0x3a000000, v22
	v_mul_f32_e32 v53, 0x4f800000, v52
	v_cmp_gt_f32_e32 vcc, s5, v52
	s_nop 1
	v_cndmask_b32_e32 v52, v52, v53, vcc
	v_sqrt_f32_e32 v53, v52
	s_nop 0
	v_add_u32_e32 v54, -1, v53
	v_add_u32_e32 v55, 1, v53
	v_fma_f32 v56, -v54, v53, v52
	v_fma_f32 v57, -v55, v53, v52
	v_cmp_ge_f32_e64 s[2:3], 0, v56
	s_nop 1
	v_cndmask_b32_e64 v53, v53, v54, s[2:3]
	v_cmp_lt_f32_e64 s[2:3], 0, v57
	s_nop 1
	v_cndmask_b32_e64 v53, v53, v55, s[2:3]
	v_mul_f32_e32 v54, 0x37800000, v53
	v_cndmask_b32_e32 v53, v53, v54, vcc
	v_cmp_class_f32_e32 vcc, v52, v23
	s_nop 1
	v_cndmask_b32_e32 v52, v53, v52, vcc
	v_div_scale_f32 v53, s[2:3], v52, v52, 1.0
	v_rcp_f32_e32 v55, v53
	v_div_scale_f32 v54, vcc, 1.0, v52, 1.0
	v_fma_f32 v56, -v53, v55, 1.0
	v_fmac_f32_e32 v55, v56, v55
	v_mul_f32_e32 v56, v54, v55
	v_fma_f32 v57, -v53, v56, v54
	v_fmac_f32_e32 v56, v57, v55
	v_fma_f32 v53, -v53, v56, v54
	v_div_fmas_f32 v53, v53, v55, v56
	v_div_fixup_f32 v52, v53, v52, 1.0
	v_pk_mul_f32 v[24:25], v[24:25], v[52:53] op_sel_hi:[1,0]
	v_pk_mul_f32 v[26:27], v[26:27], v[52:53] op_sel_hi:[1,0]
	s_waitcnt vmcnt(0)
	v_pk_mul_f32 v[24:25], v[48:49], v[24:25]
	v_pk_mul_f32 v[26:27], v[50:51], v[26:27]
	v_cvt_pk_bf16_f32 v24, v24, v25
	v_cvt_pk_bf16_f32 v25, v26, v27
	global_store_dwordx2 v[20:21], v[24:25], off offset:-2048
	global_load_dwordx4 v[24:27], v[8:9], off offset:1024 nt
	v_pk_mul_f32 v[28:29], v[28:29], v[52:53] op_sel_hi:[1,0]
	v_pk_mul_f32 v[30:31], v[30:31], v[52:53] op_sel_hi:[1,0]
	v_pk_mul_f32 v[4:5], v[4:5], v[52:53] op_sel_hi:[1,0]
	v_pk_mul_f32 v[6:7], v[6:7], v[52:53] op_sel_hi:[1,0]
	v_pk_mul_f32 v[0:1], v[0:1], v[52:53] op_sel_hi:[1,0]
	v_pk_mul_f32 v[2:3], v[2:3], v[52:53] op_sel_hi:[1,0]
	s_waitcnt vmcnt(0)
	v_pk_mul_f32 v[24:25], v[24:25], v[28:29]
	v_pk_mul_f32 v[26:27], v[26:27], v[30:31]
	v_cvt_pk_bf16_f32 v24, v24, v25
	v_cvt_pk_bf16_f32 v25, v26, v27
	global_store_dwordx2 v[20:21], v[24:25], off offset:-1536
	global_load_dwordx4 v[24:27], v[8:9], off offset:2048 nt
	v_pk_mul_f32 v[28:29], v[32:33], v[52:53] op_sel_hi:[1,0]
	v_pk_mul_f32 v[30:31], v[34:35], v[52:53] op_sel_hi:[1,0]
	s_waitcnt vmcnt(0)
	v_pk_mul_f32 v[24:25], v[24:25], v[28:29]
	v_pk_mul_f32 v[26:27], v[26:27], v[30:31]
	v_cvt_pk_bf16_f32 v24, v24, v25
	v_cvt_pk_bf16_f32 v25, v26, v27
	global_store_dwordx2 v[20:21], v[24:25], off offset:-1024
	global_load_dwordx4 v[24:27], v[8:9], off offset:3072 nt
	v_pk_mul_f32 v[28:29], v[36:37], v[52:53] op_sel_hi:[1,0]
	v_pk_mul_f32 v[30:31], v[38:39], v[52:53] op_sel_hi:[1,0]
	s_waitcnt vmcnt(0)
	v_pk_mul_f32 v[24:25], v[28:29], v[24:25]
	v_pk_mul_f32 v[26:27], v[30:31], v[26:27]
	v_cvt_pk_bf16_f32 v24, v24, v25
	v_cvt_pk_bf16_f32 v25, v26, v27
	global_store_dwordx2 v[20:21], v[24:25], off offset:-512
	global_load_dwordx4 v[24:27], v[10:11], off nt
	v_pk_mul_f32 v[28:29], v[40:41], v[52:53] op_sel_hi:[1,0]
	v_pk_mul_f32 v[30:31], v[42:43], v[52:53] op_sel_hi:[1,0]
	s_waitcnt vmcnt(0)
	v_pk_mul_f32 v[24:25], v[28:29], v[24:25]
	v_pk_mul_f32 v[26:27], v[30:31], v[26:27]
	v_cvt_pk_bf16_f32 v24, v24, v25
	v_cvt_pk_bf16_f32 v25, v26, v27
	global_store_dwordx2 v[20:21], v[24:25], off
	global_load_dwordx4 v[24:27], v[12:13], off nt
	v_pk_mul_f32 v[28:29], v[44:45], v[52:53] op_sel_hi:[1,0]
	v_pk_mul_f32 v[30:31], v[46:47], v[52:53] op_sel_hi:[1,0]
	s_waitcnt vmcnt(0)
	v_pk_mul_f32 v[24:25], v[28:29], v[24:25]
	v_pk_mul_f32 v[26:27], v[30:31], v[26:27]
	v_cvt_pk_bf16_f32 v24, v24, v25
	v_cvt_pk_bf16_f32 v25, v26, v27
	global_store_dwordx2 v[20:21], v[24:25], off offset:512
	global_load_dwordx4 v[24:27], v[14:15], off nt
	s_waitcnt vmcnt(0)
	v_pk_mul_f32 v[4:5], v[4:5], v[24:25]
	v_pk_mul_f32 v[6:7], v[6:7], v[26:27]
	v_cvt_pk_bf16_f32 v4, v4, v5
	v_cvt_pk_bf16_f32 v5, v6, v7
	global_store_dwordx2 v[20:21], v[4:5], off offset:1024
	global_load_dwordx4 v[4:7], v[16:17], off nt
	s_waitcnt vmcnt(0)
	v_pk_mul_f32 v[0:1], v[0:1], v[4:5]
	v_pk_mul_f32 v[2:3], v[2:3], v[6:7]
	v_cvt_pk_bf16_f32 v0, v0, v1
	v_cvt_pk_bf16_f32 v1, v2, v3
	global_store_dwordx2 v[20:21], v[0:1], off offset:1536
	v_lshl_add_u64 v[20:21], v[20:21], 0, s[8:9]
	s_cbranch_scc1 .LBB0_77

.LBB0_647:
	s_or_b64 exec, exec, s[4:5]
	s_mov_b64 s[2:3], s[0:1]
	v_mbcnt_lo_u32_b32 v0, -1, 0
	v_mbcnt_hi_u32_b32 v0, -1, v0
	s_lshl_b32 s4, s33, 4
	s_lshl_b32 s5, s63, 1
	s_add_i32 s42, s4, s5
	s_cmpk_gt_i32 s42, 0x3fff
	s_cbranch_scc1 .LBB0_650
	s_load_dwordx2 s[4:5], s[2:3], 0x88
	s_load_dwordx2 s[44:45], s[2:3], 0xf0
	v_lshlrev_b32_e32 v2, 1, v0
	v_ashrrev_i32_e32 v3, 31, v2
	v_lshlrev_b64 v[6:7], 2, v[2:3]
	s_waitcnt lgkmcnt(0)
	v_lshl_add_u64 v[0:1], s[4:5], 0, v[6:7]
	global_load_dwordx2 v[0:1], v[0:1], off nt
	s_ashr_i32 s43, s42, 31
	s_lshl_b32 s46, s62, 4
	s_lshl_b64 s[2:3], s[42:43], 12
	v_lshlrev_b64 v[4:5], 1, v[2:3]
	v_mov_b32_e32 v8, 0x3600
	v_lshl_add_u64 v[2:3], s[2:3], 0, v[4:5]
	s_ashr_i32 s47, s46, 31
	v_mad_i64_i32 v[4:5], s[2:3], s42, v8, v[4:5]
	v_mov_b32_e32 v8, 0xc00
	s_lshl_b64 s[48:49], s[46:47], 12
	s_mul_i32 s50, s62, 0x36000
	s_mul_hi_i32 s51, s46, 0x3600
	v_mad_i64_i32 v[6:7], s[2:3], s42, v8, v[6:7]
	s_mul_i32 s52, s62, 0xc000
	s_mul_hi_i32 s53, s46, 0xc00
	s_mov_b32 s43, 0x14606000
	s_mov_b32 s47, 0x36801000
	s_mov_b32 s54, 0x39801000
	v_mov_b32_e32 v60, 0x358637bd
	s_mov_b32 s55, 0xf800000
	v_mov_b32_e32 v61, 0x260
	s_mov_b32 s56, 0x22000000
	s_mov_b32 s57, 0x22001000
.LBB0_649:
	v_lshl_add_u64 v[8:9], s[44:45], 0, v[4:5]
	v_add_co_u32_e64 v18, s[2:3], s43, v8
	v_lshl_add_u64 v[10:11], s[44:45], 0, v[6:7]
	s_nop 0
	v_addc_co_u32_e64 v19, s[2:3], 0, v9, s[2:3]
	v_add_co_u32_e32 v16, vcc, 0x36800000, v10
	v_add_co_u32_e64 v20, s[2:3], s47, v10
	s_nop 0
	v_addc_co_u32_e32 v17, vcc, 0, v11, vcc
	v_addc_co_u32_e64 v21, s[2:3], 0, v11, s[2:3]
	v_add_co_u32_e64 v22, s[2:3], s54, v10
	v_add_co_u32_e32 v10, vcc, 0x39800000, v10
	s_nop 0
	v_addc_co_u32_e64 v23, s[2:3], 0, v11, s[2:3]
	global_load_dword v71, v[18:19], off offset:2048 nt
	global_load_dwordx2 v[24:25], v[22:23], off nt
	global_load_dwordx2 v[26:27], v[20:21], off offset:512 nt
	global_load_dwordx2 v[28:29], v[20:21], off nt
	global_load_dword v73, v[18:19], off offset:2304 nt
	global_load_dwordx2 v[30:31], v[22:23], off offset:512 nt
	global_load_dwordx2 v[32:33], v[22:23], off offset:1024 nt
	global_load_dword v75, v[18:19], off offset:2560 nt
	global_load_dwordx2 v[34:35], v[20:21], off offset:1024 nt
	global_load_dwordx2 v[36:37], v[20:21], off offset:1536 nt
	global_load_dword v77, v[18:19], off offset:2816 nt
	global_load_dwordx2 v[38:39], v[22:23], off offset:1536 nt
	v_addc_co_u32_e32 v11, vcc, 0, v11, vcc
	v_add_co_u32_e32 v8, vcc, 0x14603000, v8
	global_load_dwordx2 v[20:21], v[16:17], off nt
	global_load_dwordx2 v[22:23], v[16:17], off offset:512 nt
	global_load_dwordx2 v[40:41], v[16:17], off offset:1024 nt
	global_load_dwordx2 v[42:43], v[16:17], off offset:1536 nt
	global_load_dwordx2 v[44:45], v[16:17], off offset:2048 nt
	global_load_dwordx2 v[46:47], v[16:17], off offset:2560 nt
	global_load_dwordx2 v[48:49], v[16:17], off offset:3072 nt
	global_load_dwordx2 v[50:51], v[16:17], off offset:3584 nt
	global_load_dwordx2 v[52:53], v[10:11], off nt
	global_load_dwordx2 v[54:55], v[10:11], off offset:512 nt
	global_load_dwordx2 v[56:57], v[10:11], off offset:1024 nt
	global_load_dwordx2 v[58:59], v[10:11], off offset:1536 nt
	global_load_dwordx2 v[62:63], v[10:11], off offset:2048 nt
	global_load_dwordx2 v[64:65], v[10:11], off offset:2560 nt
	global_load_dwordx2 v[66:67], v[10:11], off offset:3072 nt
	global_load_dwordx2 v[68:69], v[10:11], off offset:3584 nt
	v_addc_co_u32_e32 v9, vcc, 0, v9, vcc
	global_load_dword v82, v[8:9], off nt
	global_load_dword v83, v[8:9], off offset:256 nt
	global_load_dword v84, v[8:9], off offset:512 nt
	global_load_dword v85, v[8:9], off offset:768 nt
	global_load_dword v86, v[8:9], off offset:1024 nt
	global_load_dword v87, v[8:9], off offset:1280 nt
	global_load_dword v88, v[18:19], off offset:1536 nt
	global_load_dword v89, v[18:19], off offset:1792 nt
	v_lshl_add_u64 v[12:13], s[44:45], 0, v[2:3]
	v_add_co_u32_e64 v14, s[2:3], s56, v12
	s_add_i32 s42, s42, s46
	s_nop 0
	v_addc_co_u32_e64 v15, s[2:3], 0, v13, s[2:3]
	v_add_co_u32_e64 v12, s[2:3], s57, v12
	v_lshl_add_u64 v[2:3], v[2:3], 0, s[48:49]
	s_nop 0
	v_addc_co_u32_e64 v13, s[2:3], 0, v13, s[2:3]
	v_lshl_add_u64 v[4:5], v[4:5], 0, s[50:51]
	v_lshl_add_u64 v[6:7], v[6:7], 0, s[52:53]
	s_cmpk_lt_i32 s42, 0x4000
	s_waitcnt vmcnt(35)
	v_lshlrev_b32_e32 v70, 16, v71
	v_and_b32_e32 v71, 0xffff0000, v71
	v_mul_f32_e32 v90, 0xbfb8aa3b, v70
	s_waitcnt vmcnt(32)
	v_pk_add_f32 v[18:19], v[28:29], v[24:25]
	s_waitcnt vmcnt(31)
	v_lshlrev_b32_e32 v72, 16, v73
	s_waitcnt vmcnt(30)
	v_pk_add_f32 v[16:17], v[26:27], v[30:31]
	v_and_b32_e32 v73, 0xffff0000, v73
	s_waitcnt vmcnt(28)
	v_lshlrev_b32_e32 v74, 16, v75
	s_waitcnt vmcnt(27)
	v_pk_add_f32 v[10:11], v[34:35], v[32:33]
	s_waitcnt vmcnt(15)
	v_pk_add_f32 v[34:35], v[20:21], v[52:53]
	v_lshlrev_b32_e32 v76, 16, v77
	v_pk_add_f32 v[8:9], v[36:37], v[38:39]
	v_pk_mul_f32 v[36:37], v[18:19], v[18:19]
	v_pk_mul_f32 v[38:39], v[16:17], v[16:17]
	v_pk_mul_f32 v[78:79], v[10:11], v[10:11]
	v_pk_mul_f32 v[80:81], v[8:9], v[8:9]
	s_waitcnt vmcnt(14)
	v_pk_add_f32 v[32:33], v[22:23], v[54:55]
	s_waitcnt vmcnt(12)
	v_pk_add_f32 v[28:29], v[42:43], v[58:59]
	s_waitcnt vmcnt(11)
	v_pk_add_f32 v[26:27], v[44:45], v[62:63]
	v_add_f32_e32 v98, v36, v37
	v_and_b32_e32 v75, 0xffff0000, v75
	v_and_b32_e32 v77, 0xffff0000, v77
	v_mul_f32_e32 v92, 0xbfb8aa3b, v72
	v_mul_f32_e32 v96, 0xbfb8aa3b, v76
	v_pk_add_f32 v[30:31], v[40:41], v[56:57]
	s_waitcnt vmcnt(10)
	v_pk_add_f32 v[24:25], v[46:47], v[64:65]
	s_waitcnt vmcnt(9)
	v_pk_add_f32 v[22:23], v[48:49], v[66:67]
	s_waitcnt vmcnt(8)
	v_pk_add_f32 v[20:21], v[50:51], v[68:69]
	v_add_f32_e32 v99, v38, v39
	v_add_f32_e32 v78, v78, v79
	v_add_f32_e32 v80, v80, v81
	s_waitcnt vmcnt(7)
	v_lshlrev_b32_e32 v44, 16, v82
	v_and_b32_e32 v45, 0xffff0000, v82
	v_pk_mul_f32 v[36:37], v[34:35], v[34:35]
	s_waitcnt vmcnt(6)
	v_and_b32_e32 v47, 0xffff0000, v83
	v_pk_mul_f32 v[38:39], v[32:33], v[32:33]
	s_waitcnt vmcnt(5)
	v_and_b32_e32 v49, 0xffff0000, v84
	s_waitcnt vmcnt(4)
	v_lshlrev_b32_e32 v50, 16, v85
	v_and_b32_e32 v51, 0xffff0000, v85
	v_pk_mul_f32 v[42:43], v[28:29], v[28:29]
	s_waitcnt vmcnt(3)
	v_lshlrev_b32_e32 v62, 16, v86
	v_and_b32_e32 v63, 0xffff0000, v86
	v_pk_mul_f32 v[52:53], v[26:27], v[26:27]
	ds_swizzle_b32 v82, v98 offset:swizzle(SWAP,1)
	v_mul_f32_e32 v93, 0xbfb8aa3b, v73
	v_mul_f32_e32 v94, 0xbfb8aa3b, v74
	v_mul_f32_e32 v95, 0xbfb8aa3b, v75
	v_mul_f32_e32 v97, 0xbfb8aa3b, v77
	v_exp_f32_e32 v92, v92
	v_exp_f32_e32 v81, v96
	v_lshlrev_b32_e32 v46, 16, v83
	v_lshlrev_b32_e32 v48, 16, v84
	v_pk_mul_f32 v[40:41], v[30:31], v[30:31]
	s_waitcnt vmcnt(2)
	v_lshlrev_b32_e32 v64, 16, v87
	v_and_b32_e32 v65, 0xffff0000, v87
	v_pk_mul_f32 v[54:55], v[24:25], v[24:25]
	s_waitcnt vmcnt(1)
	v_lshlrev_b32_e32 v66, 16, v88
	v_and_b32_e32 v67, 0xffff0000, v88
	v_pk_mul_f32 v[56:57], v[22:23], v[22:23]
	s_waitcnt vmcnt(0)
	v_lshlrev_b32_e32 v68, 16, v89
	v_and_b32_e32 v69, 0xffff0000, v89
	v_pk_mul_f32 v[58:59], v[20:21], v[20:21]
	ds_swizzle_b32 v83, v99 offset:swizzle(SWAP,1)
	ds_swizzle_b32 v84, v78 offset:swizzle(SWAP,1)
	ds_swizzle_b32 v85, v80 offset:swizzle(SWAP,1)
	v_add_f32_e32 v86, v36, v37
	v_mul_f32_e32 v37, 0xbfb8aa3b, v45
	v_add_f32_e32 v87, v38, v39
	v_mul_f32_e32 v39, 0xbfb8aa3b, v47
	v_mul_f32_e32 v88, 0xbfb8aa3b, v49
	v_add_f32_e32 v42, v42, v43
	v_mul_f32_e32 v43, 0xbfb8aa3b, v50
	v_mul_f32_e32 v89, 0xbfb8aa3b, v51
	v_add_f32_e32 v96, v52, v53
	v_mul_f32_e32 v52, 0xbfb8aa3b, v62
	v_mul_f32_e32 v53, 0xbfb8aa3b, v63
	v_mul_f32_e32 v91, 0xbfb8aa3b, v71
	v_exp_f32_e32 v93, v93
	v_exp_f32_e32 v79, v94
	v_exp_f32_e32 v94, v95
	v_exp_f32_e32 v95, v97
	v_mul_f32_e32 v36, 0xbfb8aa3b, v44
	v_mul_f32_e32 v38, 0xbfb8aa3b, v46
	v_add_f32_e32 v40, v40, v41
	v_mul_f32_e32 v41, 0xbfb8aa3b, v48
	v_add_f32_e32 v97, v54, v55
	v_mul_f32_e32 v54, 0xbfb8aa3b, v64
	v_mul_f32_e32 v55, 0xbfb8aa3b, v65
	v_add_f32_e32 v100, v56, v57
	v_mul_f32_e32 v56, 0xbfb8aa3b, v66
	v_mul_f32_e32 v57, 0xbfb8aa3b, v67
	v_add_f32_e32 v58, v58, v59
	v_mul_f32_e32 v101, 0xbfb8aa3b, v69
	ds_swizzle_b32 v102, v86 offset:swizzle(SWAP,1)
	v_exp_f32_e32 v104, v37
	v_exp_f32_e32 v107, v39
	v_exp_f32_e32 v88, v88
	v_exp_f32_e32 v43, v43
	v_exp_f32_e32 v89, v89
	ds_swizzle_b32 v110, v96 offset:swizzle(SWAP,1)
	v_exp_f32_e32 v111, v52
	v_exp_f32_e32 v112, v53
	v_exp_f32_e32 v90, v90
	v_exp_f32_e32 v91, v91
	v_mul_f32_e32 v59, 0xbfb8aa3b, v68
	v_exp_f32_e32 v103, v36
	ds_swizzle_b32 v105, v87 offset:swizzle(SWAP,1)
	v_exp_f32_e32 v106, v38
	ds_swizzle_b32 v108, v40 offset:swizzle(SWAP,1)
	v_exp_f32_e32 v41, v41
	ds_swizzle_b32 v109, v42 offset:swizzle(SWAP,1)
	ds_swizzle_b32 v113, v97 offset:swizzle(SWAP,1)
	v_exp_f32_e32 v114, v54
	v_exp_f32_e32 v115, v55
	ds_swizzle_b32 v116, v100 offset:swizzle(SWAP,1)
	v_exp_f32_e32 v56, v56
	v_exp_f32_e32 v57, v57
	ds_swizzle_b32 v117, v58 offset:swizzle(SWAP,1)
	v_exp_f32_e32 v101, v101
	v_exp_f32_e32 v59, v59
	v_add_f32_e32 v38, 1.0, v92
	s_waitcnt lgkmcnt(11)
	v_add_f32_e32 v92, v98, v82
	v_add_f32_e32 v39, 1.0, v93
	v_add_f32_e32 v52, 1.0, v79
	v_add_f32_e32 v53, 1.0, v94
	v_add_f32_e32 v54, 1.0, v81
	v_add_f32_e32 v55, 1.0, v95
	s_waitcnt lgkmcnt(10)
	v_add_f32_e32 v93, v99, v83
	s_waitcnt lgkmcnt(9)
	v_add_f32_e32 v94, v78, v84
	s_waitcnt lgkmcnt(8)
	v_add_f32_e32 v95, v80, v85
	v_add_f32_e32 v79, 1.0, v104
	v_add_f32_e32 v81, 1.0, v107
	v_add_f32_e32 v82, 1.0, v88
	v_add_f32_e32 v43, 1.0, v43
	v_add_f32_e32 v83, 1.0, v89
	v_add_f32_e32 v84, 1.0, v111
	v_add_f32_e32 v85, 1.0, v112
	ds_swizzle_b32 v99, v92 offset:swizzle(SWAP,2)
	v_add_f32_e32 v36, 1.0, v90
	v_add_f32_e32 v37, 1.0, v91
	v_rcp_f32_e32 v38, v38
	v_rcp_f32_e32 v39, v39
	v_rcp_f32_e32 v52, v52
	v_rcp_f32_e32 v53, v53
	v_add_f32_e32 v78, 1.0, v103
	v_add_f32_e32 v80, 1.0, v106
	v_add_f32_e32 v41, 1.0, v41
	v_add_f32_e32 v88, 1.0, v114
	v_add_f32_e32 v89, 1.0, v115
	v_add_f32_e32 v90, 1.0, v56
	v_add_f32_e32 v91, 1.0, v57
	v_add_f32_e32 v98, 1.0, v101
	ds_swizzle_b32 v101, v93 offset:swizzle(SWAP,2)
	ds_swizzle_b32 v103, v94 offset:swizzle(SWAP,2)
	ds_swizzle_b32 v104, v95 offset:swizzle(SWAP,2)
	s_waitcnt lgkmcnt(11)
	v_add_f32_e32 v102, v86, v102
	v_rcp_f32_e32 v57, v79
	v_rcp_f32_e32 v79, v81
	v_rcp_f32_e32 v81, v82
	v_rcp_f32_e32 v82, v43
	v_rcp_f32_e32 v83, v83
	s_waitcnt lgkmcnt(10)
	v_add_f32_e32 v96, v96, v110
	v_rcp_f32_e32 v84, v84
	v_rcp_f32_e32 v85, v85
	v_rcp_f32_e32 v36, v36
	v_rcp_f32_e32 v37, v37
	v_rcp_f32_e32 v54, v54
	v_rcp_f32_e32 v55, v55
	v_add_f32_e32 v59, 1.0, v59
	v_rcp_f32_e32 v56, v78
	s_waitcnt lgkmcnt(9)
	v_add_f32_e32 v105, v87, v105
	v_rcp_f32_e32 v78, v80
	s_waitcnt lgkmcnt(8)
	v_add_f32_e32 v106, v40, v108
	v_rcp_f32_e32 v80, v41
	s_waitcnt lgkmcnt(7)
	v_add_f32_e32 v107, v42, v109
	s_waitcnt lgkmcnt(6)
	v_add_f32_e32 v97, v97, v113
	v_rcp_f32_e32 v86, v88
	v_rcp_f32_e32 v87, v89
	s_waitcnt lgkmcnt(5)
	v_add_f32_e32 v100, v100, v116
	v_rcp_f32_e32 v88, v90
	v_rcp_f32_e32 v89, v91
	s_waitcnt lgkmcnt(4)
	v_add_f32_e32 v108, v58, v117
	v_rcp_f32_e32 v91, v98
	ds_swizzle_b32 v98, v102 offset:swizzle(SWAP,2)
	ds_swizzle_b32 v112, v96 offset:swizzle(SWAP,2)
	v_rcp_f32_e32 v90, v59
	ds_swizzle_b32 v109, v105 offset:swizzle(SWAP,2)
	ds_swizzle_b32 v110, v106 offset:swizzle(SWAP,2)
	ds_swizzle_b32 v111, v107 offset:swizzle(SWAP,2)
	ds_swizzle_b32 v113, v97 offset:swizzle(SWAP,2)
	ds_swizzle_b32 v114, v100 offset:swizzle(SWAP,2)
	ds_swizzle_b32 v115, v108 offset:swizzle(SWAP,2)
	v_pk_mul_f32 v[40:41], v[38:39], v[72:73]
	v_pk_mul_f32 v[38:39], v[52:53], v[74:75]
	v_pk_mul_f32 v[52:53], v[82:83], v[50:51]
	v_pk_mul_f32 v[50:51], v[84:85], v[62:63]
	s_waitcnt lgkmcnt(11)
	v_add_f32_e32 v62, v92, v99
	v_pk_mul_f32 v[42:43], v[36:37], v[70:71]
	v_pk_mul_f32 v[36:37], v[54:55], v[76:77]
	v_pk_mul_f32 v[58:59], v[56:57], v[44:45]
	v_pk_mul_f32 v[56:57], v[78:79], v[46:47]
	v_pk_mul_f32 v[54:55], v[80:81], v[48:49]
	v_pk_mul_f32 v[48:49], v[86:87], v[64:65]
	v_pk_mul_f32 v[46:47], v[88:89], v[66:67]
	s_waitcnt lgkmcnt(10)
	v_add_f32_e32 v63, v93, v101
	s_waitcnt lgkmcnt(9)
	v_add_f32_e32 v64, v94, v103
	s_waitcnt lgkmcnt(8)
	v_add_f32_e32 v65, v95, v104
	ds_swizzle_b32 v66, v62 offset:swizzle(SWAP,4)
	v_pk_mul_f32 v[44:45], v[90:91], v[68:69]
	ds_swizzle_b32 v67, v63 offset:swizzle(SWAP,4)
	ds_swizzle_b32 v68, v64 offset:swizzle(SWAP,4)
	ds_swizzle_b32 v69, v65 offset:swizzle(SWAP,4)
	s_waitcnt lgkmcnt(11)
	v_add_f32_e32 v70, v102, v98
	s_waitcnt lgkmcnt(10)
	v_add_f32_e32 v74, v96, v112
	s_waitcnt lgkmcnt(9)
	v_add_f32_e32 v71, v105, v109
	s_waitcnt lgkmcnt(8)
	v_add_f32_e32 v72, v106, v110
	s_waitcnt lgkmcnt(7)
	v_add_f32_e32 v73, v107, v111
	s_waitcnt lgkmcnt(6)
	v_add_f32_e32 v75, v97, v113
	s_waitcnt lgkmcnt(5)
	v_add_f32_e32 v76, v100, v114
	s_waitcnt lgkmcnt(4)
	v_add_f32_e32 v77, v108, v115
	ds_swizzle_b32 v78, v70 offset:swizzle(SWAP,4)
	ds_swizzle_b32 v82, v74 offset:swizzle(SWAP,4)
	ds_swizzle_b32 v79, v71 offset:swizzle(SWAP,4)
	ds_swizzle_b32 v80, v72 offset:swizzle(SWAP,4)
	ds_swizzle_b32 v81, v73 offset:swizzle(SWAP,4)
	ds_swizzle_b32 v83, v75 offset:swizzle(SWAP,4)
	ds_swizzle_b32 v84, v76 offset:swizzle(SWAP,4)
	ds_swizzle_b32 v85, v77 offset:swizzle(SWAP,4)
	s_waitcnt lgkmcnt(11)
	v_add_f32_e32 v62, v62, v66
	s_waitcnt lgkmcnt(10)
	v_add_f32_e32 v63, v63, v67
	s_waitcnt lgkmcnt(9)
	v_add_f32_e32 v64, v64, v68
	s_waitcnt lgkmcnt(8)
	v_add_f32_e32 v65, v65, v69
	ds_swizzle_b32 v66, v62 offset:swizzle(SWAP,8)
	ds_swizzle_b32 v67, v63 offset:swizzle(SWAP,8)
	ds_swizzle_b32 v68, v64 offset:swizzle(SWAP,8)
	ds_swizzle_b32 v69, v65 offset:swizzle(SWAP,8)
	s_waitcnt lgkmcnt(11)
	v_add_f32_e32 v70, v70, v78
	s_waitcnt lgkmcnt(10)
	v_add_f32_e32 v74, v74, v82
	s_waitcnt lgkmcnt(9)
	v_add_f32_e32 v71, v71, v79
	s_waitcnt lgkmcnt(8)
	v_add_f32_e32 v72, v72, v80
	s_waitcnt lgkmcnt(7)
	v_add_f32_e32 v73, v73, v81
	s_waitcnt lgkmcnt(6)
	v_add_f32_e32 v75, v75, v83
	s_waitcnt lgkmcnt(5)
	v_add_f32_e32 v76, v76, v84
	s_waitcnt lgkmcnt(4)
	v_add_f32_e32 v77, v77, v85
	ds_swizzle_b32 v78, v70 offset:swizzle(SWAP,8)
	ds_swizzle_b32 v82, v74 offset:swizzle(SWAP,8)
	ds_swizzle_b32 v79, v71 offset:swizzle(SWAP,8)
	ds_swizzle_b32 v80, v72 offset:swizzle(SWAP,8)
	ds_swizzle_b32 v81, v73 offset:swizzle(SWAP,8)
	ds_swizzle_b32 v83, v75 offset:swizzle(SWAP,8)
	ds_swizzle_b32 v84, v76 offset:swizzle(SWAP,8)
	ds_swizzle_b32 v85, v77 offset:swizzle(SWAP,8)
	s_waitcnt lgkmcnt(11)
	v_add_f32_e32 v62, v62, v66
	s_waitcnt lgkmcnt(10)
	v_add_f32_e32 v63, v63, v67
	s_waitcnt lgkmcnt(9)
	v_add_f32_e32 v64, v64, v68
	s_waitcnt lgkmcnt(8)
	v_add_f32_e32 v65, v65, v69
	ds_swizzle_b32 v66, v62 offset:swizzle(SWAP,16)
	ds_swizzle_b32 v67, v63 offset:swizzle(SWAP,16)
	ds_swizzle_b32 v68, v64 offset:swizzle(SWAP,16)
	ds_swizzle_b32 v69, v65 offset:swizzle(SWAP,16)
	s_waitcnt lgkmcnt(11)
	v_add_f32_e32 v70, v70, v78
	s_waitcnt lgkmcnt(10)
	v_add_f32_e32 v74, v74, v82
	s_waitcnt lgkmcnt(9)
	v_add_f32_e32 v71, v71, v79
	s_waitcnt lgkmcnt(8)
	v_add_f32_e32 v72, v72, v80
	s_waitcnt lgkmcnt(7)
	v_add_f32_e32 v73, v73, v81
	s_waitcnt lgkmcnt(6)
	v_add_f32_e32 v75, v75, v83
	s_waitcnt lgkmcnt(5)
	v_add_f32_e32 v76, v76, v84
	s_waitcnt lgkmcnt(4)
	v_add_f32_e32 v77, v77, v85
	ds_swizzle_b32 v78, v70 offset:swizzle(SWAP,16)
	ds_swizzle_b32 v82, v74 offset:swizzle(SWAP,16)
	ds_swizzle_b32 v79, v71 offset:swizzle(SWAP,16)
	ds_swizzle_b32 v80, v72 offset:swizzle(SWAP,16)
	ds_swizzle_b32 v81, v73 offset:swizzle(SWAP,16)
	ds_swizzle_b32 v83, v75 offset:swizzle(SWAP,16)
	ds_swizzle_b32 v84, v76 offset:swizzle(SWAP,16)
	ds_swizzle_b32 v85, v77 offset:swizzle(SWAP,16)
	s_waitcnt lgkmcnt(11)
	v_add_f32_e32 v62, v62, v66
	s_waitcnt lgkmcnt(10)
	v_add_f32_e32 v63, v63, v67
	s_waitcnt lgkmcnt(9)
	v_add_f32_e32 v64, v64, v68
	s_waitcnt lgkmcnt(8)
	v_add_f32_e32 v65, v65, v69
	v_mov_b32_e32 v66, v62
	v_mov_b32_e32 v67, v63
	v_mov_b32_e32 v68, v64
	v_mov_b32_e32 v69, v65
	s_waitcnt lgkmcnt(7)
	v_add_f32_e32 v70, v70, v78
	s_waitcnt lgkmcnt(6)
	v_add_f32_e32 v74, v74, v82
	v_permlane32_swap_b32_e32 v62, v66
	s_waitcnt lgkmcnt(5)
	v_add_f32_e32 v71, v71, v79
	s_waitcnt lgkmcnt(4)
	v_add_f32_e32 v72, v72, v80
	s_waitcnt lgkmcnt(3)
	v_add_f32_e32 v73, v73, v81
	s_waitcnt lgkmcnt(2)
	v_add_f32_e32 v75, v75, v83
	s_waitcnt lgkmcnt(1)
	v_add_f32_e32 v76, v76, v84
	s_waitcnt lgkmcnt(0)
	v_add_f32_e32 v77, v77, v85
	v_permlane32_swap_b32_e32 v63, v67
	v_permlane32_swap_b32_e32 v64, v68
	v_permlane32_swap_b32_e32 v65, v69
	v_mov_b32_e32 v78, v70
	v_mov_b32_e32 v82, v74
	v_add_f32_e32 v62, v62, v66
	v_mov_b32_e32 v79, v71
	v_mov_b32_e32 v80, v72
	v_mov_b32_e32 v81, v73
	v_mov_b32_e32 v83, v75
	v_mov_b32_e32 v84, v76
	v_mov_b32_e32 v85, v77
	v_add_f32_e32 v63, v63, v67
	v_add_f32_e32 v64, v64, v68
	v_add_f32_e32 v65, v65, v69
	v_permlane32_swap_b32_e32 v70, v78
	v_permlane32_swap_b32_e32 v74, v82
	v_fmamk_f32 v62, v62, 0x3c000000, v60
	v_permlane32_swap_b32_e32 v71, v79
	v_permlane32_swap_b32_e32 v72, v80
	v_permlane32_swap_b32_e32 v73, v81
	v_permlane32_swap_b32_e32 v75, v83
	v_permlane32_swap_b32_e32 v76, v84
	v_permlane32_swap_b32_e32 v77, v85
	v_fmamk_f32 v63, v63, 0x3c000000, v60
	v_fmamk_f32 v64, v64, 0x3c000000, v60
	v_fmamk_f32 v65, v65, 0x3c000000, v60
	v_add_f32_e32 v66, v70, v78
	v_add_f32_e32 v70, v74, v82
	v_mul_f32_e32 v74, 0x4f800000, v62
	v_cmp_gt_f32_e64 s[14:15], s55, v62
	v_add_f32_e32 v67, v71, v79
	v_add_f32_e32 v68, v72, v80
	v_add_f32_e32 v69, v73, v81
	v_add_f32_e32 v71, v75, v83
	v_add_f32_e32 v72, v76, v84
	v_add_f32_e32 v73, v77, v85
	v_mul_f32_e32 v75, 0x4f800000, v63
	v_cmp_gt_f32_e64 s[16:17], s55, v63
	v_mul_f32_e32 v76, 0x4f800000, v64
	v_cmp_gt_f32_e64 s[18:19], s55, v64
	v_mul_f32_e32 v77, 0x4f800000, v65
	v_cmp_gt_f32_e64 s[20:21], s55, v65
	v_fmamk_f32 v66, v66, 0x3c000000, v60
	v_cndmask_b32_e64 v62, v62, v74, s[14:15]
	v_fmamk_f32 v67, v67, 0x3c000000, v60
	v_fmamk_f32 v68, v68, 0x3c000000, v60
	v_fmamk_f32 v69, v69, 0x3c000000, v60
	v_fmamk_f32 v70, v70, 0x3c000000, v60
	v_fmamk_f32 v71, v71, 0x3c000000, v60
	v_fmamk_f32 v72, v72, 0x3c000000, v60
	v_fmamk_f32 v73, v73, 0x3c000000, v60
	v_cndmask_b32_e64 v63, v63, v75, s[16:17]
	v_cndmask_b32_e64 v64, v64, v76, s[18:19]
	v_cndmask_b32_e64 v65, v65, v77, s[20:21]
	v_mul_f32_e32 v74, 0x4f800000, v66
	v_sqrt_f32_e32 v82, v62
	v_cmp_gt_f32_e64 s[22:23], s55, v66
	v_mul_f32_e32 v75, 0x4f800000, v67
	v_cmp_gt_f32_e32 vcc, s55, v67
	v_mul_f32_e32 v76, 0x4f800000, v68
	v_cmp_gt_f32_e64 s[2:3], s55, v68
	v_mul_f32_e32 v77, 0x4f800000, v69
	v_cmp_gt_f32_e64 s[4:5], s55, v69
	v_mul_f32_e32 v78, 0x4f800000, v70
	v_cmp_gt_f32_e64 s[6:7], s55, v70
	v_mul_f32_e32 v79, 0x4f800000, v71
	v_cmp_gt_f32_e64 s[8:9], s55, v71
	v_mul_f32_e32 v80, 0x4f800000, v72
	v_cmp_gt_f32_e64 s[10:11], s55, v72
	v_mul_f32_e32 v81, 0x4f800000, v73
	v_cmp_gt_f32_e64 s[12:13], s55, v73
	v_sqrt_f32_e32 v83, v63
	v_sqrt_f32_e32 v84, v64
	v_sqrt_f32_e32 v85, v65
	v_cndmask_b32_e64 v66, v66, v74, s[22:23]
	v_cndmask_b32_e32 v67, v67, v75, vcc
	v_cndmask_b32_e64 v68, v68, v76, s[2:3]
	v_cndmask_b32_e64 v69, v69, v77, s[4:5]
	v_cndmask_b32_e64 v70, v70, v78, s[6:7]
	v_cndmask_b32_e64 v71, v71, v79, s[8:9]
	v_cndmask_b32_e64 v72, v72, v80, s[10:11]
	v_cndmask_b32_e64 v73, v73, v81, s[12:13]
	v_sqrt_f32_e32 v74, v66
	v_sqrt_f32_e32 v75, v67
	v_sqrt_f32_e32 v76, v68
	v_sqrt_f32_e32 v77, v69
	v_sqrt_f32_e32 v78, v70
	v_sqrt_f32_e32 v79, v71
	v_sqrt_f32_e32 v80, v72
	v_sqrt_f32_e32 v81, v73
	v_add_u32_e32 v86, -1, v82
	v_add_u32_e32 v87, 1, v82
	v_add_u32_e32 v88, -1, v83
	v_add_u32_e32 v90, -1, v84
	v_add_u32_e32 v92, -1, v85
	v_fma_f32 v94, -v86, v82, v62
	v_add_u32_e32 v89, 1, v83
	v_add_u32_e32 v91, 1, v84
	v_add_u32_e32 v93, 1, v85
	v_fma_f32 v95, -v87, v82, v62
	v_fma_f32 v96, -v88, v83, v63
	v_fma_f32 v98, -v90, v84, v64
	v_fma_f32 v100, -v92, v85, v65
	v_add_u32_e32 v102, -1, v74
	v_cmp_ge_f32_e64 s[24:25], 0, v94
	v_fma_f32 v97, -v89, v83, v63
	v_fma_f32 v99, -v91, v84, v64
	v_fma_f32 v101, -v93, v85, v65
	v_add_u32_e32 v103, 1, v74
	v_add_u32_e32 v104, -1, v75
	v_add_u32_e32 v106, -1, v76
	v_add_u32_e32 v108, -1, v77
	v_add_u32_e32 v110, -1, v78
	v_add_u32_e32 v112, -1, v79
	v_add_u32_e32 v114, -1, v80
	v_add_u32_e32 v116, -1, v81
	v_cndmask_b32_e64 v82, v82, v86, s[24:25]
	v_cmp_lt_f32_e64 s[24:25], 0, v95
	v_cmp_ge_f32_e64 s[26:27], 0, v96
	v_cmp_ge_f32_e64 s[28:29], 0, v98
	v_cmp_ge_f32_e64 s[30:31], 0, v100
	v_fma_f32 v86, -v102, v74, v66
	v_add_u32_e32 v105, 1, v75
	v_add_u32_e32 v107, 1, v76
	v_add_u32_e32 v109, 1, v77
	v_add_u32_e32 v111, 1, v78
	v_add_u32_e32 v113, 1, v79
	v_add_u32_e32 v115, 1, v80
	v_add_u32_e32 v117, 1, v81
	v_cndmask_b32_e64 v83, v83, v88, s[26:27]
	v_cmp_lt_f32_e64 s[26:27], 0, v97
	v_cndmask_b32_e64 v84, v84, v90, s[28:29]
	v_cmp_lt_f32_e64 s[28:29], 0, v99
	v_cndmask_b32_e64 v85, v85, v92, s[30:31]
	v_cmp_lt_f32_e64 s[30:31], 0, v101
	v_fma_f32 v88, -v103, v74, v66
	v_fma_f32 v90, -v104, v75, v67
	v_fma_f32 v94, -v106, v76, v68
	v_fma_f32 v96, -v108, v77, v69
	v_fma_f32 v98, -v110, v78, v70
	v_fma_f32 v100, -v112, v79, v71
	v_fma_f32 v118, -v114, v80, v72
	v_fma_f32 v120, -v116, v81, v73
	v_cndmask_b32_e64 v82, v82, v87, s[24:25]
	v_cmp_ge_f32_e64 s[24:25], 0, v86
	v_fma_f32 v92, -v105, v75, v67
	v_fma_f32 v95, -v107, v76, v68
	v_fma_f32 v97, -v109, v77, v69
	v_fma_f32 v99, -v111, v78, v70
	v_fma_f32 v101, -v113, v79, v71
	v_fma_f32 v119, -v115, v80, v72
	v_fma_f32 v121, -v117, v81, v73
	v_cndmask_b32_e64 v83, v83, v89, s[26:27]
	v_cndmask_b32_e64 v84, v84, v91, s[28:29]
	v_cndmask_b32_e64 v85, v85, v93, s[30:31]
	v_cndmask_b32_e64 v74, v74, v102, s[24:25]
	v_cmp_ge_f32_e64 s[24:25], 0, v90
	v_cmp_ge_f32_e64 s[26:27], 0, v94
	v_cmp_ge_f32_e64 s[28:29], 0, v96
	v_cmp_ge_f32_e64 s[30:31], 0, v98
	v_cmp_ge_f32_e64 s[34:35], 0, v100
	v_cmp_ge_f32_e64 s[36:37], 0, v118
	v_cmp_ge_f32_e64 s[38:39], 0, v120
	v_cmp_lt_f32_e64 s[40:41], 0, v88
	v_cndmask_b32_e64 v75, v75, v104, s[24:25]
	v_cmp_lt_f32_e64 s[24:25], 0, v92
	v_cndmask_b32_e64 v76, v76, v106, s[26:27]
	v_cmp_lt_f32_e64 s[26:27], 0, v95
	v_cndmask_b32_e64 v77, v77, v108, s[28:29]
	v_cmp_lt_f32_e64 s[28:29], 0, v97
	v_cndmask_b32_e64 v78, v78, v110, s[30:31]
	v_cmp_lt_f32_e64 s[30:31], 0, v99
	v_cndmask_b32_e64 v79, v79, v112, s[34:35]
	v_cmp_lt_f32_e64 s[34:35], 0, v101
	v_cndmask_b32_e64 v80, v80, v114, s[36:37]
	v_cmp_lt_f32_e64 s[36:37], 0, v119
	v_cndmask_b32_e64 v81, v81, v116, s[38:39]
	v_cmp_lt_f32_e64 s[38:39], 0, v121
	v_mul_f32_e32 v86, 0x37800000, v82
	v_cndmask_b32_e64 v74, v74, v103, s[40:41]
	v_mul_f32_e32 v87, 0x37800000, v83
	v_mul_f32_e32 v89, 0x37800000, v84
	v_mul_f32_e32 v90, 0x37800000, v85
	v_cndmask_b32_e64 v75, v75, v105, s[24:25]
	v_cndmask_b32_e64 v76, v76, v107, s[26:27]
	v_cndmask_b32_e64 v77, v77, v109, s[28:29]
	v_cndmask_b32_e64 v78, v78, v111, s[30:31]
	v_cndmask_b32_e64 v79, v79, v113, s[34:35]
	v_cndmask_b32_e64 v80, v80, v115, s[36:37]
	v_cndmask_b32_e64 v81, v81, v117, s[38:39]
	v_cndmask_b32_e64 v82, v82, v86, s[14:15]
	v_cmp_class_f32_e64 s[14:15], v62, v61
	v_mul_f32_e32 v86, 0x37800000, v74
	v_cndmask_b32_e64 v83, v83, v87, s[16:17]
	v_cmp_class_f32_e64 s[16:17], v63, v61
	v_cndmask_b32_e64 v84, v84, v89, s[18:19]
	v_cmp_class_f32_e64 s[18:19], v64, v61
	v_cndmask_b32_e64 v85, v85, v90, s[20:21]
	v_cmp_class_f32_e64 s[20:21], v65, v61
	v_mul_f32_e32 v87, 0x37800000, v75
	v_mul_f32_e32 v88, 0x37800000, v76
	v_mul_f32_e32 v89, 0x37800000, v77
	v_mul_f32_e32 v90, 0x37800000, v78
	v_mul_f32_e32 v91, 0x37800000, v79
	v_mul_f32_e32 v92, 0x37800000, v80
	v_mul_f32_e32 v93, 0x37800000, v81
	v_cndmask_b32_e64 v82, v82, v62, s[14:15]
	v_cndmask_b32_e64 v62, v74, v86, s[22:23]
	v_cmp_class_f32_e64 s[22:23], v66, v61
	v_cndmask_b32_e64 v63, v83, v63, s[16:17]
	v_cndmask_b32_e64 v64, v84, v64, s[18:19]
	v_cndmask_b32_e64 v65, v85, v65, s[20:21]
	v_cndmask_b32_e32 v74, v75, v87, vcc
	v_cmp_class_f32_e32 vcc, v67, v61
	v_cndmask_b32_e64 v75, v76, v88, s[2:3]
	v_cmp_class_f32_e64 s[14:15], v68, v61
	v_cndmask_b32_e64 v76, v77, v89, s[4:5]
	v_cmp_class_f32_e64 s[16:17], v69, v61
	v_cndmask_b32_e64 v77, v78, v90, s[6:7]
	v_cmp_class_f32_e64 s[18:19], v70, v61
	v_cndmask_b32_e64 v78, v79, v91, s[8:9]
	v_cmp_class_f32_e64 s[20:21], v71, v61
	v_cndmask_b32_e64 v79, v80, v92, s[10:11]
	v_cmp_class_f32_e64 s[10:11], v72, v61
	v_cndmask_b32_e64 v80, v81, v93, s[12:13]
	v_cmp_class_f32_e64 s[12:13], v73, v61
	v_div_scale_f32 v81, s[2:3], v82, v82, 1.0
	v_cndmask_b32_e64 v62, v62, v66, s[22:23]
	v_div_scale_f32 v84, s[2:3], v63, v63, 1.0
	v_cndmask_b32_e32 v66, v74, v67, vcc
	v_cndmask_b32_e64 v67, v75, v68, s[14:15]
	v_cndmask_b32_e64 v68, v76, v69, s[16:17]
	v_cndmask_b32_e64 v69, v77, v70, s[18:19]
	v_cndmask_b32_e64 v70, v78, v71, s[20:21]
	v_cndmask_b32_e64 v71, v79, v72, s[10:11]
	v_cndmask_b32_e64 v72, v80, v73, s[12:13]
	v_rcp_f32_e32 v73, v81
	v_div_scale_f32 v77, s[10:11], v62, v62, 1.0
	v_div_scale_f32 v86, s[2:3], v64, v64, 1.0
	v_rcp_f32_e32 v74, v84
	v_div_scale_f32 v79, s[10:11], v66, v66, 1.0
	v_div_scale_f32 v94, s[10:11], v69, v69, 1.0
	v_rcp_f32_e32 v102, v77
	v_div_scale_f32 v88, s[2:3], v65, v65, 1.0
	v_rcp_f32_e32 v75, v86
	v_div_scale_f32 v90, s[10:11], v67, v67, 1.0
	v_div_scale_f32 v96, s[10:11], v70, v70, 1.0
	v_rcp_f32_e32 v103, v79
	v_rcp_f32_e32 v106, v94
	v_rcp_f32_e32 v76, v88
	v_div_scale_f32 v92, s[10:11], v68, v68, 1.0
	v_div_scale_f32 v98, s[10:11], v71, v71, 1.0
	v_rcp_f32_e32 v104, v90
	v_rcp_f32_e32 v107, v96
	v_div_scale_f32 v100, s[10:11], v72, v72, 1.0
	v_rcp_f32_e32 v105, v92
	v_rcp_f32_e32 v108, v98
	v_fma_f32 v110, -v81, v73, 1.0
	v_div_scale_f32 v83, s[8:9], 1.0, v82, 1.0
	v_rcp_f32_e32 v109, v100
	v_fma_f32 v111, -v84, v74, 1.0
	v_fmac_f32_e32 v73, v110, v73
	v_fma_f32 v110, -v77, v102, 1.0
	v_div_scale_f32 v85, s[6:7], 1.0, v63, 1.0
	v_div_scale_f32 v78, vcc, 1.0, v62, 1.0
	v_fma_f32 v112, -v86, v75, 1.0
	v_fmac_f32_e32 v74, v111, v74
	v_fma_f32 v111, -v79, v103, 1.0
	v_fma_f32 v114, -v94, v106, 1.0
	v_mul_f32_e32 v118, v83, v73
	v_fmac_f32_e32 v102, v110, v102
	v_div_scale_f32 v87, s[4:5], 1.0, v64, 1.0
	v_div_scale_f32 v80, s[20:21], 1.0, v66, 1.0
	v_fma_f32 v113, -v88, v76, 1.0
	v_fmac_f32_e32 v75, v112, v75
	v_fma_f32 v112, -v90, v104, 1.0
	v_fma_f32 v115, -v96, v107, 1.0
	v_mul_f32_e32 v119, v85, v74
	v_fmac_f32_e32 v103, v111, v103
	v_fmac_f32_e32 v106, v114, v106
	v_fma_f32 v110, -v81, v118, v83
	v_mul_f32_e32 v114, v78, v102
	v_div_scale_f32 v89, s[2:3], 1.0, v65, 1.0
	v_div_scale_f32 v91, s[22:23], 1.0, v67, 1.0
	v_fmac_f32_e32 v76, v113, v76
	v_fma_f32 v113, -v92, v105, 1.0
	v_fma_f32 v116, -v98, v108, 1.0
	v_mul_f32_e32 v120, v87, v75
	v_fmac_f32_e32 v104, v112, v104
	v_fmac_f32_e32 v107, v115, v107
	v_fma_f32 v111, -v84, v119, v85
	v_mul_f32_e32 v115, v80, v103
	v_fmac_f32_e32 v118, v110, v73
	v_fma_f32 v110, -v77, v114, v78
	v_div_scale_f32 v93, s[18:19], 1.0, v68, 1.0
	v_fma_f32 v117, -v100, v109, 1.0
	v_mul_f32_e32 v121, v89, v76
	v_fmac_f32_e32 v105, v113, v105
	v_fmac_f32_e32 v108, v116, v108
	v_fma_f32 v112, -v86, v120, v87
	v_mul_f32_e32 v116, v91, v104
	v_fmac_f32_e32 v119, v111, v74
	v_fma_f32 v111, -v79, v115, v80
	v_fmac_f32_e32 v114, v110, v102
	v_div_scale_f32 v95, s[16:17], 1.0, v69, 1.0
	v_fmac_f32_e32 v109, v117, v109
	v_fma_f32 v113, -v88, v121, v89
	v_mul_f32_e32 v117, v93, v105
	v_fmac_f32_e32 v120, v112, v75
	v_fma_f32 v112, -v90, v116, v91
	v_fmac_f32_e32 v115, v111, v103
	v_fma_f32 v77, -v77, v114, v78
	v_div_scale_f32 v97, s[14:15], 1.0, v70, 1.0
	v_mul_f32_e32 v122, v95, v106
	v_fmac_f32_e32 v121, v113, v76
	v_fma_f32 v113, -v92, v117, v93
	v_fmac_f32_e32 v116, v112, v104
	v_fma_f32 v78, -v79, v115, v80
	v_div_fmas_f32 v77, v77, v102, v114
	s_mov_b64 vcc, s[20:21]
	v_div_scale_f32 v99, s[12:13], 1.0, v71, 1.0
	v_mul_f32_e32 v123, v97, v107
	v_fma_f32 v126, -v94, v122, v95
	v_fmac_f32_e32 v117, v113, v105
	v_fma_f32 v79, -v90, v116, v91
	v_div_fixup_f32 v62, v77, v62, 1.0
	v_div_fmas_f32 v77, v78, v103, v115
	s_mov_b64 vcc, s[22:23]
	v_div_scale_f32 v101, s[10:11], 1.0, v72, 1.0
	v_mul_f32_e32 v124, v99, v108
	v_fma_f32 v127, -v96, v123, v97
	v_fmac_f32_e32 v122, v126, v106
	v_fma_f32 v80, -v92, v117, v93
	v_pk_mul_f32 v[34:35], v[34:35], v[62:63] op_sel_hi:[1,0]
	v_div_fixup_f32 v62, v77, v66, 1.0
	v_div_fmas_f32 v66, v79, v104, v116
	s_mov_b64 vcc, s[18:19]
	v_mul_f32_e32 v125, v101, v109
	v_fma_f32 v128, -v98, v124, v99
	v_fma_f32 v81, -v81, v118, v83
	v_fma_f32 v83, -v84, v119, v85
	v_fma_f32 v84, -v86, v120, v87
	v_fmac_f32_e32 v123, v127, v107
	v_fma_f32 v86, -v94, v122, v95
	v_pk_mul_f32 v[34:35], v[0:1], v[34:35]
	v_pk_mul_f32 v[32:33], v[32:33], v[62:63] op_sel_hi:[1,0]
	v_div_fixup_f32 v62, v66, v67, 1.0
	v_div_fmas_f32 v66, v80, v105, v117
	s_mov_b64 vcc, s[16:17]
	v_fma_f32 v129, -v100, v125, v101
	v_fmac_f32_e32 v124, v128, v108
	v_fma_f32 v87, -v96, v123, v97
	v_pk_mul_f32 v[34:35], v[58:59], v[34:35]
	v_pk_mul_f32 v[32:33], v[0:1], v[32:33]
	v_pk_mul_f32 v[30:31], v[30:31], v[62:63] op_sel_hi:[1,0]
	v_div_fixup_f32 v58, v66, v68, 1.0
	v_div_fmas_f32 v59, v86, v106, v122
	s_mov_b64 vcc, s[14:15]
	v_fma_f32 v85, -v88, v121, v89
	v_fmac_f32_e32 v125, v129, v109
	v_fma_f32 v88, -v98, v124, v99
	v_cvt_pk_bf16_f32 v35, v34, v35
	v_pk_mul_f32 v[32:33], v[56:57], v[32:33]
	v_pk_mul_f32 v[30:31], v[0:1], v[30:31]
	v_pk_mul_f32 v[28:29], v[28:29], v[58:59] op_sel_hi:[1,0]
	v_div_fixup_f32 v34, v59, v69, 1.0
	v_div_fmas_f32 v56, v87, v107, v123
	s_mov_b64 vcc, s[12:13]
	v_fma_f32 v89, -v100, v125, v101
	v_cvt_pk_bf16_f32 v33, v32, v33
	v_pk_mul_f32 v[30:31], v[54:55], v[30:31]
	v_pk_mul_f32 v[28:29], v[0:1], v[28:29]
	v_pk_mul_f32 v[26:27], v[26:27], v[34:35] op_sel_hi:[1,0]
	v_div_fixup_f32 v32, v56, v70, 1.0
	v_div_fmas_f32 v34, v88, v108, v124
	s_mov_b64 vcc, s[10:11]
	v_cvt_pk_bf16_f32 v31, v30, v31
	v_pk_mul_f32 v[28:29], v[52:53], v[28:29]
	v_pk_mul_f32 v[26:27], v[0:1], v[26:27]
	v_pk_mul_f32 v[24:25], v[24:25], v[32:33] op_sel_hi:[1,0]
	v_div_fixup_f32 v30, v34, v71, 1.0
	v_div_fmas_f32 v32, v89, v109, v125
	s_mov_b64 vcc, s[8:9]
	v_cvt_pk_bf16_f32 v29, v28, v29
	v_pk_mul_f32 v[26:27], v[50:51], v[26:27]
	v_pk_mul_f32 v[24:25], v[0:1], v[24:25]
	v_pk_mul_f32 v[22:23], v[22:23], v[30:31] op_sel_hi:[1,0]
	v_div_fixup_f32 v28, v32, v72, 1.0
	v_div_fmas_f32 v30, v81, v73, v118
	v_cvt_pk_bf16_f32 v27, v26, v27
	v_pk_mul_f32 v[24:25], v[48:49], v[24:25]
	v_pk_mul_f32 v[22:23], v[0:1], v[22:23]
	v_pk_mul_f32 v[20:21], v[20:21], v[28:29] op_sel_hi:[1,0]
	v_div_fixup_f32 v26, v30, v82, 1.0
	s_mov_b64 vcc, s[6:7]
	v_div_fmas_f32 v28, v83, v74, v119
	v_cvt_pk_bf16_f32 v25, v24, v25
	v_pk_mul_f32 v[22:23], v[46:47], v[22:23]
	v_pk_mul_f32 v[20:21], v[0:1], v[20:21]
	v_pk_mul_f32 v[18:19], v[18:19], v[26:27] op_sel_hi:[1,0]
	s_mov_b64 vcc, s[4:5]
	global_store_dword v[14:15], v35, off offset:2560
	global_store_dword v[14:15], v33, off offset:2816
	global_store_dword v[14:15], v31, off offset:3072
	global_store_dword v[14:15], v29, off offset:3328
	global_store_dword v[14:15], v27, off offset:3584
	v_div_fmas_f32 v26, v84, v75, v120
	global_store_dword v[14:15], v25, off offset:3840
	v_cvt_pk_bf16_f32 v22, v22, v23
	v_pk_mul_f32 v[14:15], v[44:45], v[20:21]
	v_pk_mul_f32 v[18:19], v[0:1], v[18:19]
	s_mov_b64 vcc, s[2:3]
	v_div_fmas_f32 v21, v85, v76, v121
	global_store_dword v[12:13], v22, off offset:2560
	v_cvt_pk_bf16_f32 v22, v14, v15
	v_pk_mul_f32 v[14:15], v[42:43], v[18:19]
	v_div_fixup_f32 v24, v28, v63, 1.0
	v_div_fixup_f32 v20, v26, v64, 1.0
	v_div_fixup_f32 v18, v21, v65, 1.0
	v_cvt_pk_bf16_f32 v19, v14, v15
	v_pk_mul_f32 v[16:17], v[16:17], v[24:25] op_sel_hi:[1,0]
	v_pk_mul_f32 v[10:11], v[10:11], v[20:21] op_sel_hi:[1,0]
	v_pk_mul_f32 v[8:9], v[8:9], v[18:19] op_sel_hi:[1,0]
	v_pk_mul_f32 v[16:17], v[0:1], v[16:17]
	v_pk_mul_f32 v[10:11], v[0:1], v[10:11]
	v_pk_mul_f32 v[8:9], v[0:1], v[8:9]
	v_pk_mul_f32 v[14:15], v[40:41], v[16:17]
	v_pk_mul_f32 v[10:11], v[38:39], v[10:11]
	v_pk_mul_f32 v[8:9], v[36:37], v[8:9]
	v_cvt_pk_bf16_f32 v14, v14, v15
	v_cvt_pk_bf16_f32 v10, v10, v11
	v_cvt_pk_bf16_f32 v8, v8, v9
	global_store_dword v[12:13], v22, off offset:2816
	global_store_dword v[12:13], v19, off offset:3072
	global_store_dword v[12:13], v14, off offset:3328
	global_store_dword v[12:13], v10, off offset:3584
	global_store_dword v[12:13], v8, off offset:3840
	s_cbranch_scc1 .LBB0_649

.LBB0_949:
	v_ashrrev_i32_e32 v3, 31, v2
	v_lshl_add_u64 v[6:7], v[2:3], 2, s[6:7]
	global_load_dwordx4 v[6:9], v[6:7], off nt
	v_add_u32_e32 v1, 0x200, v1
	v_cmp_lt_i32_e32 vcc, s10, v1
	v_add_u32_e32 v2, 0x800, v2
	s_or_b64 s[8:9], vcc, s[8:9]
	s_waitcnt vmcnt(0)
	ds_write_b128 v4, v[6:9]
	v_add_u32_e32 v4, 0x2000, v4
	s_andn2_b64 exec, exec, s[8:9]
	s_cbranch_execnz .LBB0_949

.LBB0_953:
	v_add_co_u32_e64 v16, s[12:13], s21, v78
	v_add_co_u32_e32 v28, vcc, 0xffffd000, v78
	s_nop 0
	v_addc_co_u32_e64 v17, s[12:13], -1, v79, s[12:13]
	v_add_co_u32_e64 v30, s[12:13], s23, v78
	global_load_dwordx4 v[0:3], v[16:17], off offset:-3072 nt
	global_load_dwordx4 v[4:7], v[16:17], off offset:-2048 nt
	global_load_dwordx4 v[12:15], v[16:17], off offset:-1024 nt
	global_load_dwordx4 v[8:11], v[16:17], off nt
	v_addc_co_u32_e64 v31, s[12:13], -1, v79, s[12:13]
	global_load_dwordx4 v[16:19], v[30:31], off offset:-3072 nt
	global_load_dwordx4 v[20:23], v[30:31], off offset:-2048 nt
	global_load_dwordx4 v[24:27], v[30:31], off offset:-1024 nt
	v_addc_co_u32_e32 v29, vcc, -1, v79, vcc
	global_load_dwordx4 v[60:63], v[28:29], off offset:-3072 nt
	global_load_dwordx4 v[56:59], v[28:29], off offset:-2048 nt
	global_load_dwordx4 v[44:47], v[28:29], off offset:-1024 nt
	s_nop 0
	global_load_dwordx4 v[28:31], v[28:29], off nt
	s_nop 0
	global_load_dwordx4 v[36:39], v[78:79], off offset:-4096 nt
	global_load_dwordx4 v[40:43], v[78:79], off offset:-3072 nt
	global_load_dwordx4 v[48:51], v[78:79], off offset:-2048 nt
	global_load_dwordx4 v[52:55], v[78:79], off offset:-1024 nt
	global_load_dwordx4 v[32:35], v[78:79], off nt
	global_load_dwordx4 v[176:179], v[66:67], off nt
	global_load_dwordx4 v[180:183], v[68:69], off nt
	global_load_dwordx4 v[184:187], v[70:71], off nt
	global_load_dwordx4 v[188:191], v[72:73], off nt
	global_load_dwordx4 v[172:175], v[64:65], off offset:3072 nt
	s_waitcnt vmcnt(20)
	v_mul_f32_e32 v80, v1, v1
	v_mul_f32_e32 v81, v3, v3
	s_waitcnt vmcnt(19)
	v_mul_f32_e32 v82, v5, v5
	v_mul_f32_e32 v83, v7, v7
	s_waitcnt vmcnt(18)
	v_mul_f32_e32 v84, v13, v13
	v_mul_f32_e32 v85, v15, v15
	s_waitcnt vmcnt(17)
	v_mul_f32_e32 v86, v9, v9
	v_mul_f32_e32 v87, v11, v11
	s_waitcnt vmcnt(16)
	v_mul_f32_e32 v88, v17, v17
	v_mul_f32_e32 v89, v19, v19
	s_waitcnt vmcnt(15)
	v_mul_f32_e32 v90, v21, v21
	v_mul_f32_e32 v91, v23, v23
	s_waitcnt vmcnt(13)
	v_mul_f32_e32 v94, v61, v61
	v_mul_f32_e32 v95, v63, v63
	s_waitcnt vmcnt(12)
	v_mul_f32_e32 v164, v57, v57
	v_mul_f32_e32 v165, v59, v59
	s_waitcnt vmcnt(11)
	v_mul_f32_e32 v166, v45, v45
	v_mul_f32_e32 v167, v47, v47
	v_fmac_f32_e32 v80, v0, v0
	v_fmac_f32_e32 v81, v2, v2
	v_fmac_f32_e32 v82, v4, v4
	v_fmac_f32_e32 v83, v6, v6
	v_fmac_f32_e32 v84, v12, v12
	v_fmac_f32_e32 v85, v14, v14
	v_fmac_f32_e32 v86, v8, v8
	v_fmac_f32_e32 v87, v10, v10
	v_fmac_f32_e32 v88, v16, v16
	v_fmac_f32_e32 v89, v18, v18
	v_fmac_f32_e32 v90, v20, v20
	v_fmac_f32_e32 v91, v22, v22
	v_fmac_f32_e32 v94, v60, v60
	v_fmac_f32_e32 v95, v62, v62
	v_fmac_f32_e32 v164, v56, v56
	v_fmac_f32_e32 v165, v58, v58
	s_waitcnt vmcnt(10)
	v_mul_f32_e32 v168, v29, v29
	v_mul_f32_e32 v169, v31, v31
	v_fmac_f32_e32 v166, v44, v44
	v_fmac_f32_e32 v167, v46, v46
	v_add_f32_e32 v80, v80, v81
	v_add_f32_e32 v81, v82, v83
	v_add_f32_e32 v82, v84, v85
	v_add_f32_e32 v83, v86, v87
	v_add_f32_e32 v84, v88, v89
	v_add_f32_e32 v85, v90, v91
	v_add_f32_e32 v87, v94, v95
	v_add_f32_e32 v88, v164, v165
	v_fmac_f32_e32 v168, v28, v28
	v_fmac_f32_e32 v169, v30, v30
	v_add_f32_e32 v89, v166, v167
	v_add_f32_e32 v84, v84, v85
	v_add_f32_e32 v85, v87, v88
	v_add_f32_e32 v90, v168, v169
	v_add_f32_e32 v85, v85, v89
	v_add_f32_e32 v85, v85, v90
	v_add_f32_e32 v80, v85, v80
	v_add_f32_e32 v80, v80, v81
	v_add_f32_e32 v80, v80, v82
	v_add_f32_e32 v80, v80, v83
	s_waitcnt vmcnt(9)
	v_mul_f32_e32 v82, v37, v37
	v_mul_f32_e32 v83, v39, v39
	v_fmac_f32_e32 v82, v36, v36
	v_fmac_f32_e32 v83, v38, v38
	v_add_f32_e32 v82, v82, v83
	ds_swizzle_b32 v83, v80 offset:swizzle(SWAP,1)
	v_mul_f32_e32 v92, v25, v25
	v_mul_f32_e32 v93, v27, v27
	v_fmac_f32_e32 v92, v24, v24
	v_fmac_f32_e32 v93, v26, v26
	s_waitcnt lgkmcnt(0)
	v_add_f32_e32 v80, v80, v83
	ds_swizzle_b32 v83, v80 offset:swizzle(SWAP,2)
	v_add_f32_e32 v86, v92, v93
	v_add_f32_e32 v81, v84, v86
	v_add_f32_e32 v81, v81, v82
	s_waitcnt vmcnt(8)
	v_mul_f32_e32 v82, v41, v41
	s_waitcnt lgkmcnt(0)
	v_add_f32_e32 v80, v80, v83
	ds_swizzle_b32 v83, v80 offset:swizzle(SWAP,4)
	v_mul_f32_e32 v84, v43, v43
	v_fmac_f32_e32 v82, v40, v40
	v_fmac_f32_e32 v84, v42, v42
	v_add_f32_e32 v82, v82, v84
	s_waitcnt lgkmcnt(0)
	v_add_f32_e32 v80, v80, v83
	ds_swizzle_b32 v83, v80 offset:swizzle(SWAP,8)
	v_add_f32_e32 v81, v81, v82
	s_waitcnt vmcnt(7)
	v_mul_f32_e32 v82, v49, v49
	v_mul_f32_e32 v84, v51, v51
	v_fmac_f32_e32 v82, v48, v48
	s_waitcnt lgkmcnt(0)
	v_add_f32_e32 v80, v80, v83
	ds_swizzle_b32 v83, v80 offset:swizzle(SWAP,16)
	v_fmac_f32_e32 v84, v50, v50
	v_add_f32_e32 v82, v82, v84
	v_add_f32_e32 v81, v81, v82
	s_waitcnt vmcnt(6)
	v_mul_f32_e32 v82, v53, v53
	s_waitcnt lgkmcnt(0)
	v_add_f32_e32 v80, v80, v83
	v_mul_f32_e32 v84, v55, v55
	v_mov_b32_e32 v83, v80
	v_fmac_f32_e32 v82, v52, v52
	v_fmac_f32_e32 v84, v54, v54
	v_permlane32_swap_b32_e32 v80, v83
	v_add_f32_e32 v82, v82, v84
	v_add_f32_e32 v80, v80, v83
	v_add_f32_e32 v81, v81, v82
	s_waitcnt vmcnt(5)
	v_mul_f32_e32 v82, v33, v33
	v_mul_f32_e32 v84, v35, v35
	v_fmamk_f32 v80, v80, 0x3a000000, v161
	v_fmac_f32_e32 v82, v32, v32
	v_mul_f32_e32 v83, 0x4f800000, v80
	v_cmp_gt_f32_e32 vcc, s28, v80
	v_fmac_f32_e32 v84, v34, v34
	global_load_dwordx4 v[164:167], v[64:65], off offset:1024 nt
	v_cndmask_b32_e32 v85, v80, v83, vcc
	v_add_f32_e32 v80, v82, v84
	v_add_f32_e32 v84, v81, v80
	global_load_dwordx4 v[80:83], v[64:65], off nt
	global_load_dwordx4 v[168:171], v[64:65], off offset:2048 nt
	ds_swizzle_b32 v89, v84 offset:swizzle(SWAP,1)
	v_sqrt_f32_e32 v86, v85
	s_waitcnt lgkmcnt(0)
	v_add_f32_e32 v84, v84, v89
	v_add_u32_e32 v87, -1, v86
	v_fma_f32 v88, -v87, v86, v85
	ds_swizzle_b32 v89, v84 offset:swizzle(SWAP,2)
	v_cmp_ge_f32_e64 s[12:13], 0, v88
	v_add_u32_e32 v88, 1, v86
	s_waitcnt lgkmcnt(0)
	v_add_f32_e32 v84, v84, v89
	v_cndmask_b32_e64 v87, v86, v87, s[12:13]
	v_fma_f32 v86, -v88, v86, v85
	v_cmp_lt_f32_e64 s[12:13], 0, v86
	s_nop 1
	v_cndmask_b32_e64 v86, v87, v88, s[12:13]
	v_mul_f32_e32 v87, 0x37800000, v86
	v_cndmask_b32_e32 v86, v86, v87, vcc
	ds_swizzle_b32 v87, v84 offset:swizzle(SWAP,4)
	v_cmp_class_f32_e32 vcc, v85, v162
	s_waitcnt lgkmcnt(0)
	v_add_f32_e32 v84, v84, v87
	ds_swizzle_b32 v87, v84 offset:swizzle(SWAP,8)
	v_cndmask_b32_e32 v85, v86, v85, vcc
	v_div_scale_f32 v86, s[12:13], v85, v85, 1.0
	v_rcp_f32_e32 v88, v86
	s_waitcnt lgkmcnt(0)
	v_add_f32_e32 v84, v84, v87
	ds_swizzle_b32 v87, v84 offset:swizzle(SWAP,16)
	v_fma_f32 v89, -v86, v88, 1.0
	v_fmac_f32_e32 v88, v89, v88
	v_div_scale_f32 v89, vcc, 1.0, v85, 1.0
	s_waitcnt lgkmcnt(0)
	v_add_f32_e32 v84, v84, v87
	v_mov_b32_e32 v87, v84
	s_nop 1
	v_permlane32_swap_b32_e32 v84, v87
	v_add_f32_e32 v84, v84, v87
	v_fmamk_f32 v84, v84, 0x3a000000, v161
	v_mul_f32_e32 v87, 0x4f800000, v84
	v_cmp_gt_f32_e64 s[12:13], s28, v84
	v_mul_f32_e32 v90, v89, v88
	v_fma_f32 v91, -v86, v90, v89
	v_cndmask_b32_e64 v84, v84, v87, s[12:13]
	v_sqrt_f32_e32 v87, v84
	v_fmac_f32_e32 v90, v91, v88
	v_fma_f32 v86, -v86, v90, v89
	v_div_fmas_f32 v86, v86, v88, v90
	v_add_u32_e32 v89, -1, v87
	v_fma_f32 v91, -v89, v87, v84
	v_cmp_ge_f32_e64 s[14:15], 0, v91
	v_add_u32_e32 v91, 1, v87
	v_div_fixup_f32 v192, v86, v85, 1.0
	v_cndmask_b32_e64 v89, v87, v89, s[14:15]
	v_fma_f32 v87, -v91, v87, v84
	v_cmp_lt_f32_e64 s[14:15], 0, v87
	v_pk_mul_f32 v[60:61], v[60:61], v[192:193] op_sel_hi:[1,0]
	v_pk_mul_f32 v[62:63], v[62:63], v[192:193] op_sel_hi:[1,0]
	v_cndmask_b32_e64 v87, v89, v91, s[14:15]
	v_mul_f32_e32 v89, 0x37800000, v87
	v_cndmask_b32_e64 v87, v87, v89, s[12:13]
	v_cmp_class_f32_e64 s[12:13], v84, v162
	v_pk_mul_f32 v[0:1], v[0:1], v[192:193] op_sel_hi:[1,0]
	v_pk_mul_f32 v[2:3], v[2:3], v[192:193] op_sel_hi:[1,0]
	v_cndmask_b32_e64 v84, v87, v84, s[12:13]
	v_div_scale_f32 v87, s[12:13], v84, v84, 1.0
	v_rcp_f32_e32 v89, v87
	s_waitcnt vmcnt(1)
	v_pk_mul_f32 v[92:93], v[80:81], v[60:61]
	v_fma_f32 v85, -v87, v89, 1.0
	v_fmac_f32_e32 v89, v85, v89
	v_div_scale_f32 v85, vcc, 1.0, v84, 1.0
	v_mul_f32_e32 v86, v85, v89
	v_fma_f32 v88, -v87, v86, v85
	v_fmac_f32_e32 v86, v88, v89
	v_fma_f32 v85, -v87, v86, v85
	v_div_fmas_f32 v85, v85, v89, v86
	v_div_fixup_f32 v194, v85, v84, 1.0
	v_pk_mul_f32 v[16:17], v[16:17], v[194:195] op_sel_hi:[1,0]
	v_pk_mul_f32 v[18:19], v[18:19], v[194:195] op_sel_hi:[1,0]
	v_pk_mul_f32 v[94:95], v[80:81], v[16:17]
	v_pk_mul_f32 v[16:17], v[56:57], v[192:193] op_sel_hi:[1,0]
	v_pk_mul_f32 v[88:89], v[82:83], v[18:19]
	v_pk_mul_f32 v[18:19], v[58:59], v[192:193] op_sel_hi:[1,0]
	v_pk_mul_f32 v[86:87], v[164:165], v[16:17]
	v_pk_mul_f32 v[16:17], v[20:21], v[194:195] op_sel_hi:[1,0]
	v_pk_mul_f32 v[80:81], v[166:167], v[18:19]
	v_pk_mul_f32 v[18:19], v[22:23], v[194:195] op_sel_hi:[1,0]
	v_pk_mul_f32 v[90:91], v[164:165], v[16:17]
	v_pk_mul_f32 v[16:17], v[44:45], v[192:193] op_sel_hi:[1,0]
	v_pk_mul_f32 v[84:85], v[82:83], v[62:63]
	v_pk_mul_f32 v[82:83], v[166:167], v[18:19]
	v_pk_mul_f32 v[18:19], v[46:47], v[192:193] op_sel_hi:[1,0]
	s_waitcnt vmcnt(0)
	v_pk_mul_f32 v[60:61], v[168:169], v[16:17]
	v_pk_mul_f32 v[16:17], v[24:25], v[194:195] op_sel_hi:[1,0]
	v_pk_mul_f32 v[46:47], v[170:171], v[18:19]
	v_pk_mul_f32 v[18:19], v[26:27], v[194:195] op_sel_hi:[1,0]
	v_pk_mul_f32 v[62:63], v[168:169], v[16:17]
	v_pk_mul_f32 v[16:17], v[28:29], v[192:193] op_sel_hi:[1,0]
	v_pk_mul_f32 v[28:29], v[0:1], v[176:177]
	v_pk_mul_f32 v[0:1], v[40:41], v[194:195] op_sel_hi:[1,0]
	v_pk_mul_f32 v[58:59], v[170:171], v[18:19]
	v_pk_mul_f32 v[18:19], v[30:31], v[192:193] op_sel_hi:[1,0]
	v_pk_mul_f32 v[30:31], v[176:177], v[0:1]
	v_pk_mul_f32 v[0:1], v[4:5], v[192:193] op_sel_hi:[1,0]
	v_pk_mul_f32 v[20:21], v[2:3], v[178:179]
	v_pk_mul_f32 v[2:3], v[42:43], v[194:195] op_sel_hi:[1,0]
	v_pk_mul_f32 v[22:23], v[0:1], v[180:181]
	v_pk_mul_f32 v[0:1], v[48:49], v[194:195] op_sel_hi:[1,0]
	v_pk_mul_f32 v[56:57], v[172:173], v[16:17]
	v_pk_mul_f32 v[16:17], v[36:37], v[194:195] op_sel_hi:[1,0]
	v_pk_mul_f32 v[24:25], v[178:179], v[2:3]
	v_pk_mul_f32 v[2:3], v[6:7], v[192:193] op_sel_hi:[1,0]
	v_pk_mul_f32 v[26:27], v[180:181], v[0:1]
	v_pk_mul_f32 v[0:1], v[12:13], v[192:193] op_sel_hi:[1,0]
	v_pk_mul_f32 v[44:45], v[174:175], v[18:19]
	v_pk_mul_f32 v[18:19], v[38:39], v[194:195] op_sel_hi:[1,0]
	v_pk_mul_f32 v[38:39], v[172:173], v[16:17]
	v_pk_mul_f32 v[16:17], v[2:3], v[182:183]
	v_pk_mul_f32 v[2:3], v[50:51], v[194:195] op_sel_hi:[1,0]
	v_pk_mul_f32 v[12:13], v[0:1], v[184:185]
	v_pk_mul_f32 v[0:1], v[52:53], v[194:195] op_sel_hi:[1,0]
	v_pk_mul_f32 v[36:37], v[174:175], v[18:19]
	v_pk_mul_f32 v[18:19], v[182:183], v[2:3]
	v_pk_mul_f32 v[2:3], v[14:15], v[192:193] op_sel_hi:[1,0]
	v_pk_mul_f32 v[14:15], v[184:185], v[0:1]
	v_pk_mul_f32 v[0:1], v[10:11], v[192:193] op_sel_hi:[1,0]
	v_pk_mul_f32 v[10:11], v[32:33], v[194:195] op_sel_hi:[1,0]
	v_lshl_add_u64 v[32:33], s[18:19], 0, v[76:77]
	v_add_co_u32_e32 v40, vcc, s29, v32
	v_pk_mul_f32 v[4:5], v[54:55], v[194:195] op_sel_hi:[1,0]
	s_nop 0
	v_addc_co_u32_e32 v41, vcc, 0, v33, vcc
	v_pk_mul_f32 v[6:7], v[186:187], v[4:5]
	v_pk_mul_f32 v[4:5], v[8:9], v[192:193] op_sel_hi:[1,0]
	v_add_co_u32_e32 v32, vcc, s30, v32
	v_pk_mul_f32 v[8:9], v[4:5], v[188:189]
	v_pk_mul_f32 v[4:5], v[34:35], v[194:195] op_sel_hi:[1,0]
	v_cvt_pk_bf16_f32 v34, v92, v93
	v_cvt_pk_bf16_f32 v35, v84, v85
	v_addc_co_u32_e32 v33, vcc, 0, v33, vcc
	global_store_dwordx2 v[32:33], v[34:35], off offset:-4096
	v_cvt_pk_bf16_f32 v34, v86, v87
	v_cvt_pk_bf16_f32 v35, v80, v81
	global_store_dwordx2 v[40:41], v[34:35], off offset:512
	v_cvt_pk_bf16_f32 v34, v60, v61
	v_cvt_pk_bf16_f32 v35, v46, v47
	global_store_dwordx2 v[40:41], v[34:35], off offset:1024
	v_cvt_pk_bf16_f32 v34, v56, v57
	v_cvt_pk_bf16_f32 v35, v44, v45
	global_store_dwordx2 v[40:41], v[34:35], off offset:1536
	v_cvt_pk_bf16_f32 v34, v28, v29
	v_cvt_pk_bf16_f32 v35, v20, v21
	v_pk_mul_f32 v[2:3], v[2:3], v[186:187]
	global_store_dwordx2 v[40:41], v[34:35], off offset:2048
	v_cvt_pk_bf16_f32 v34, v22, v23
	v_cvt_pk_bf16_f32 v35, v16, v17
	v_pk_mul_f32 v[0:1], v[0:1], v[190:191]
	global_store_dwordx2 v[40:41], v[34:35], off offset:2560
	v_cvt_pk_bf16_f32 v34, v12, v13
	v_cvt_pk_bf16_f32 v35, v2, v3
	global_store_dwordx2 v[40:41], v[34:35], off offset:3072
	v_cvt_pk_bf16_f32 v34, v8, v9
	v_cvt_pk_bf16_f32 v35, v0, v1
	global_store_dwordx2 v[40:41], v[34:35], off offset:3584
	v_cvt_pk_bf16_f32 v34, v94, v95
	v_cvt_pk_bf16_f32 v35, v88, v89
	global_store_dwordx2 v[32:33], v[34:35], off
	v_cvt_pk_bf16_f32 v34, v90, v91
	v_cvt_pk_bf16_f32 v35, v82, v83
	global_store_dwordx2 v[32:33], v[34:35], off offset:512
	v_cvt_pk_bf16_f32 v34, v62, v63
	v_cvt_pk_bf16_f32 v35, v58, v59
	global_store_dwordx2 v[32:33], v[34:35], off offset:1024
	v_cvt_pk_bf16_f32 v34, v38, v39
	v_cvt_pk_bf16_f32 v35, v36, v37
	ds_read_b128 v[40:43], v96
	ds_read_b128 v[48:51], v96 offset:1024
	global_store_dwordx2 v[32:33], v[34:35], off offset:1536
	v_cvt_pk_bf16_f32 v34, v30, v31
	v_cvt_pk_bf16_f32 v35, v24, v25
	global_store_dwordx2 v[32:33], v[34:35], off offset:2048
	v_cvt_pk_bf16_f32 v34, v26, v27
	v_cvt_pk_bf16_f32 v35, v18, v19
	v_pk_mul_f32 v[4:5], v[190:191], v[4:5]
	v_pk_mul_f32 v[10:11], v[188:189], v[10:11]
	global_store_dwordx2 v[32:33], v[34:35], off offset:2560
	v_cvt_pk_bf16_f32 v34, v14, v15
	v_cvt_pk_bf16_f32 v35, v6, v7
	global_store_dwordx2 v[32:33], v[34:35], off offset:3072
	v_cvt_pk_bf16_f32 v34, v10, v11
	v_cvt_pk_bf16_f32 v35, v4, v5
	global_store_dwordx2 v[32:33], v[34:35], off offset:3584
	s_waitcnt lgkmcnt(1)
	v_fma_f32 v33, v92, v40, 0
	v_fma_f32 v32, v94, v40, 0
	v_fmac_f32_e32 v33, v93, v41
	v_fmac_f32_e32 v32, v95, v41
	v_fmac_f32_e32 v33, v84, v42
	v_fmac_f32_e32 v32, v88, v42
	v_fmac_f32_e32 v33, v85, v43
	v_fmac_f32_e32 v32, v89, v43
	ds_read_b128 v[40:43], v96 offset:2048
	s_waitcnt lgkmcnt(1)
	v_fmac_f32_e32 v33, v86, v48
	v_fmac_f32_e32 v32, v90, v48
	v_fmac_f32_e32 v33, v87, v49
	v_fmac_f32_e32 v32, v91, v49
	v_fmac_f32_e32 v33, v80, v50
	v_fmac_f32_e32 v32, v82, v50
	v_fmac_f32_e32 v33, v81, v51
	v_fmac_f32_e32 v32, v83, v51
	ds_read_b128 v[48:51], v96 offset:3072
	s_waitcnt lgkmcnt(1)
	v_fmac_f32_e32 v33, v60, v40
	v_fmac_f32_e32 v32, v62, v40
	v_fmac_f32_e32 v33, v61, v41
	v_fmac_f32_e32 v32, v63, v41
	v_fmac_f32_e32 v33, v46, v42
	v_fmac_f32_e32 v32, v58, v42
	v_fmac_f32_e32 v33, v47, v43
	v_fmac_f32_e32 v32, v59, v43
	ds_read_b128 v[40:43], v96 offset:4096
	s_waitcnt lgkmcnt(1)
	v_fmac_f32_e32 v33, v56, v48
	v_fmac_f32_e32 v32, v38, v48
	v_fmac_f32_e32 v33, v57, v49
	v_fmac_f32_e32 v32, v39, v49
	v_fmac_f32_e32 v33, v44, v50
	v_fmac_f32_e32 v32, v36, v50
	v_fmac_f32_e32 v33, v45, v51
	v_fmac_f32_e32 v32, v37, v51
	ds_read_b128 v[48:51], v96 offset:5120
	s_waitcnt lgkmcnt(1)
	v_fmac_f32_e32 v33, v28, v40
	v_fmac_f32_e32 v32, v30, v40
	v_fmac_f32_e32 v33, v29, v41
	v_fmac_f32_e32 v32, v31, v41
	v_fmac_f32_e32 v33, v20, v42
	v_fmac_f32_e32 v32, v24, v42
	v_fmac_f32_e32 v33, v21, v43
	v_fmac_f32_e32 v32, v25, v43
	ds_read_b128 v[40:43], v96 offset:6144
	s_waitcnt lgkmcnt(1)
	v_fmac_f32_e32 v33, v22, v48
	v_fmac_f32_e32 v32, v26, v48
	v_fmac_f32_e32 v33, v23, v49
	v_fmac_f32_e32 v32, v27, v49
	v_fmac_f32_e32 v33, v16, v50
	v_fmac_f32_e32 v32, v18, v50
	v_fmac_f32_e32 v33, v17, v51
	v_fmac_f32_e32 v32, v19, v51
	ds_read_b128 v[48:51], v96 offset:7168
	s_waitcnt lgkmcnt(1)
	v_fmac_f32_e32 v33, v12, v40
	v_fmac_f32_e32 v32, v14, v40
	v_fmac_f32_e32 v33, v13, v41
	v_fmac_f32_e32 v32, v15, v41
	v_fmac_f32_e32 v33, v2, v42
	v_fmac_f32_e32 v32, v6, v42
	v_fmac_f32_e32 v33, v3, v43
	v_fmac_f32_e32 v32, v7, v43
	s_waitcnt lgkmcnt(0)
	v_fmac_f32_e32 v33, v8, v48
	v_fmac_f32_e32 v32, v10, v48
	v_fmac_f32_e32 v33, v9, v49
	v_fmac_f32_e32 v32, v11, v49
	v_fmac_f32_e32 v33, v0, v50
	v_fmac_f32_e32 v32, v4, v50
	v_fmac_f32_e32 v33, v1, v51
	v_fmac_f32_e32 v32, v5, v51
	ds_read_b128 v[40:43], v96 offset:8192
	ds_read_b128 v[48:51], v96 offset:9216
	s_waitcnt lgkmcnt(1)
	v_fma_f32 v35, v92, v40, 0
	v_fma_f32 v34, v94, v40, 0
	v_fmac_f32_e32 v35, v93, v41
	v_fmac_f32_e32 v34, v95, v41
	v_fmac_f32_e32 v35, v84, v42
	v_fmac_f32_e32 v34, v88, v42
	v_fmac_f32_e32 v35, v85, v43
	v_fmac_f32_e32 v34, v89, v43
	ds_read_b128 v[40:43], v96 offset:10240
	s_waitcnt lgkmcnt(1)
	v_fmac_f32_e32 v35, v86, v48
	v_fmac_f32_e32 v34, v90, v48
	v_fmac_f32_e32 v35, v87, v49
	v_fmac_f32_e32 v34, v91, v49
	v_fmac_f32_e32 v35, v80, v50
	v_fmac_f32_e32 v34, v82, v50
	v_fmac_f32_e32 v35, v81, v51
	v_fmac_f32_e32 v34, v83, v51
	ds_read_b128 v[48:51], v96 offset:11264
	s_waitcnt lgkmcnt(1)
	v_fmac_f32_e32 v35, v60, v40
	v_fmac_f32_e32 v34, v62, v40
	v_fmac_f32_e32 v35, v61, v41
	v_fmac_f32_e32 v34, v63, v41
	v_fmac_f32_e32 v35, v46, v42
	v_fmac_f32_e32 v34, v58, v42
	v_fmac_f32_e32 v35, v47, v43
	v_fmac_f32_e32 v34, v59, v43
	ds_read_b128 v[40:43], v96 offset:12288
	s_waitcnt lgkmcnt(1)
	v_fmac_f32_e32 v35, v56, v48
	v_fmac_f32_e32 v34, v38, v48
	v_fmac_f32_e32 v35, v57, v49
	v_fmac_f32_e32 v34, v39, v49
	v_fmac_f32_e32 v35, v44, v50
	v_fmac_f32_e32 v34, v36, v50
	v_fmac_f32_e32 v35, v45, v51
	v_fmac_f32_e32 v34, v37, v51
	ds_read_b128 v[48:51], v96 offset:13312
	s_waitcnt lgkmcnt(1)
	v_fmac_f32_e32 v35, v28, v40
	v_fmac_f32_e32 v34, v30, v40
	v_fmac_f32_e32 v35, v29, v41
	v_fmac_f32_e32 v34, v31, v41
	v_fmac_f32_e32 v35, v20, v42
	v_fmac_f32_e32 v34, v24, v42
	v_fmac_f32_e32 v35, v21, v43
	v_fmac_f32_e32 v34, v25, v43
	ds_read_b128 v[40:43], v96 offset:14336
	s_waitcnt lgkmcnt(1)
	v_fmac_f32_e32 v35, v22, v48
	v_fmac_f32_e32 v34, v26, v48
	v_fmac_f32_e32 v35, v23, v49
	v_fmac_f32_e32 v34, v27, v49
	v_fmac_f32_e32 v35, v16, v50
	v_fmac_f32_e32 v34, v18, v50
	v_fmac_f32_e32 v35, v17, v51
	v_fmac_f32_e32 v34, v19, v51
	ds_read_b128 v[48:51], v96 offset:15360
	s_waitcnt lgkmcnt(1)
	v_fmac_f32_e32 v35, v12, v40
	v_fmac_f32_e32 v34, v14, v40
	v_fmac_f32_e32 v35, v13, v41
	v_fmac_f32_e32 v34, v15, v41
	v_fmac_f32_e32 v35, v2, v42
	v_fmac_f32_e32 v34, v6, v42
	v_fmac_f32_e32 v35, v3, v43
	v_fmac_f32_e32 v34, v7, v43
	s_waitcnt lgkmcnt(0)
	v_fmac_f32_e32 v35, v8, v48
	v_fmac_f32_e32 v34, v10, v48
	v_fmac_f32_e32 v35, v9, v49
	v_fmac_f32_e32 v34, v11, v49
	v_fmac_f32_e32 v35, v0, v50
	v_fmac_f32_e32 v34, v4, v50
	v_fmac_f32_e32 v35, v1, v51
	v_fmac_f32_e32 v34, v5, v51
	ds_read_b128 v[48:51], v96 offset:16384
	ds_read_b128 v[52:55], v96 offset:17408
	s_waitcnt lgkmcnt(1)
	v_fma_f32 v41, v92, v48, 0
	v_fma_f32 v40, v94, v48, 0
	v_fmac_f32_e32 v41, v93, v49
	v_fmac_f32_e32 v40, v95, v49
	v_fmac_f32_e32 v41, v84, v50
	v_fmac_f32_e32 v40, v88, v50
	v_fmac_f32_e32 v41, v85, v51
	v_fmac_f32_e32 v40, v89, v51
	ds_read_b128 v[48:51], v96 offset:18432
	s_waitcnt lgkmcnt(1)
	v_fmac_f32_e32 v41, v86, v52
	v_fmac_f32_e32 v40, v90, v52
	v_fmac_f32_e32 v41, v87, v53
	v_fmac_f32_e32 v40, v91, v53
	v_fmac_f32_e32 v41, v80, v54
	v_fmac_f32_e32 v40, v82, v54
	v_fmac_f32_e32 v41, v81, v55
	v_fmac_f32_e32 v40, v83, v55
	ds_read_b128 v[52:55], v96 offset:19456
	s_waitcnt lgkmcnt(1)
	v_fmac_f32_e32 v41, v60, v48
	v_fmac_f32_e32 v40, v62, v48
	v_fmac_f32_e32 v41, v61, v49
	v_fmac_f32_e32 v40, v63, v49
	v_fmac_f32_e32 v41, v46, v50
	v_fmac_f32_e32 v40, v58, v50
	v_fmac_f32_e32 v41, v47, v51
	v_fmac_f32_e32 v40, v59, v51
	ds_read_b128 v[48:51], v96 offset:20480
	s_waitcnt lgkmcnt(1)
	v_fmac_f32_e32 v41, v56, v52
	v_fmac_f32_e32 v40, v38, v52
	v_fmac_f32_e32 v41, v57, v53
	v_fmac_f32_e32 v40, v39, v53
	v_fmac_f32_e32 v41, v44, v54
	v_fmac_f32_e32 v40, v36, v54
	v_fmac_f32_e32 v41, v45, v55
	v_fmac_f32_e32 v40, v37, v55
	ds_read_b128 v[52:55], v96 offset:21504
	s_waitcnt lgkmcnt(1)
	v_fmac_f32_e32 v41, v28, v48
	v_fmac_f32_e32 v40, v30, v48
	v_fmac_f32_e32 v41, v29, v49
	v_fmac_f32_e32 v40, v31, v49
	v_fmac_f32_e32 v41, v20, v50
	v_fmac_f32_e32 v40, v24, v50
	v_fmac_f32_e32 v41, v21, v51
	v_fmac_f32_e32 v40, v25, v51
	ds_read_b128 v[48:51], v96 offset:22528
	s_waitcnt lgkmcnt(1)
	v_fmac_f32_e32 v41, v22, v52
	v_fmac_f32_e32 v40, v26, v52
	v_fmac_f32_e32 v41, v23, v53
	v_fmac_f32_e32 v40, v27, v53
	v_fmac_f32_e32 v41, v16, v54
	v_fmac_f32_e32 v40, v18, v54
	v_fmac_f32_e32 v41, v17, v55
	v_fmac_f32_e32 v40, v19, v55
	ds_read_b128 v[52:55], v96 offset:23552
	s_waitcnt lgkmcnt(1)
	v_fmac_f32_e32 v41, v12, v48
	v_fmac_f32_e32 v40, v14, v48
	v_fmac_f32_e32 v41, v13, v49
	v_fmac_f32_e32 v40, v15, v49
	v_fmac_f32_e32 v41, v2, v50
	v_fmac_f32_e32 v40, v6, v50
	v_fmac_f32_e32 v41, v3, v51
	v_fmac_f32_e32 v40, v7, v51
	s_waitcnt lgkmcnt(0)
	v_fmac_f32_e32 v41, v8, v52
	v_fmac_f32_e32 v40, v10, v52
	v_fmac_f32_e32 v41, v9, v53
	v_fmac_f32_e32 v40, v11, v53
	v_fmac_f32_e32 v41, v0, v54
	v_fmac_f32_e32 v40, v4, v54
	v_fmac_f32_e32 v41, v1, v55
	v_fmac_f32_e32 v40, v5, v55
	ds_read_b128 v[48:51], v96 offset:24576
	ds_read_b128 v[52:55], v96 offset:25600
	s_waitcnt lgkmcnt(1)
	v_fma_f32 v43, v92, v48, 0
	v_fma_f32 v42, v94, v48, 0
	v_fmac_f32_e32 v43, v93, v49
	v_fmac_f32_e32 v42, v95, v49
	v_fmac_f32_e32 v43, v84, v50
	v_fmac_f32_e32 v42, v88, v50
	v_fmac_f32_e32 v43, v85, v51
	v_fmac_f32_e32 v42, v89, v51
	ds_read_b128 v[48:51], v96 offset:26624
	s_waitcnt lgkmcnt(1)
	v_fmac_f32_e32 v43, v86, v52
	v_fmac_f32_e32 v42, v90, v52
	v_fmac_f32_e32 v43, v87, v53
	v_fmac_f32_e32 v42, v91, v53
	v_fmac_f32_e32 v43, v80, v54
	v_fmac_f32_e32 v42, v82, v54
	v_fmac_f32_e32 v43, v81, v55
	v_fmac_f32_e32 v42, v83, v55
	ds_read_b128 v[52:55], v96 offset:27648
	s_waitcnt lgkmcnt(1)
	v_fmac_f32_e32 v43, v60, v48
	v_fmac_f32_e32 v42, v62, v48
	v_fmac_f32_e32 v43, v61, v49
	v_fmac_f32_e32 v42, v63, v49
	v_fmac_f32_e32 v43, v46, v50
	v_fmac_f32_e32 v42, v58, v50
	v_fmac_f32_e32 v43, v47, v51
	v_fmac_f32_e32 v42, v59, v51
	ds_read_b128 v[48:51], v96 offset:28672
	s_waitcnt lgkmcnt(1)
	v_fmac_f32_e32 v43, v56, v52
	v_fmac_f32_e32 v42, v38, v52
	v_fmac_f32_e32 v43, v57, v53
	v_fmac_f32_e32 v42, v39, v53
	v_fmac_f32_e32 v43, v44, v54
	v_fmac_f32_e32 v42, v36, v54
	v_fmac_f32_e32 v43, v45, v55
	v_fmac_f32_e32 v42, v37, v55
	ds_read_b128 v[52:55], v96 offset:29696
	s_waitcnt lgkmcnt(1)
	v_fmac_f32_e32 v43, v28, v48
	v_fmac_f32_e32 v42, v30, v48
	v_fmac_f32_e32 v43, v29, v49
	v_fmac_f32_e32 v42, v31, v49
	v_fmac_f32_e32 v43, v20, v50
	v_fmac_f32_e32 v42, v24, v50
	v_fmac_f32_e32 v43, v21, v51
	v_fmac_f32_e32 v42, v25, v51
	ds_read_b128 v[48:51], v96 offset:30720
	s_waitcnt lgkmcnt(1)
	v_fmac_f32_e32 v43, v22, v52
	v_fmac_f32_e32 v42, v26, v52
	v_fmac_f32_e32 v43, v23, v53
	v_fmac_f32_e32 v42, v27, v53
	v_fmac_f32_e32 v43, v16, v54
	v_fmac_f32_e32 v42, v18, v54
	v_fmac_f32_e32 v43, v17, v55
	v_fmac_f32_e32 v42, v19, v55
	ds_read_b128 v[52:55], v96 offset:31744
	s_waitcnt lgkmcnt(1)
	v_fmac_f32_e32 v43, v12, v48
	v_fmac_f32_e32 v42, v14, v48
	v_fmac_f32_e32 v43, v13, v49
	v_fmac_f32_e32 v42, v15, v49
	v_fmac_f32_e32 v43, v2, v50
	v_fmac_f32_e32 v42, v6, v50
	v_fmac_f32_e32 v43, v3, v51
	v_fmac_f32_e32 v42, v7, v51
	s_waitcnt lgkmcnt(0)
	v_fmac_f32_e32 v43, v8, v52
	v_fmac_f32_e32 v42, v10, v52
	v_fmac_f32_e32 v43, v9, v53
	v_fmac_f32_e32 v42, v11, v53
	v_fmac_f32_e32 v43, v0, v54
	v_fmac_f32_e32 v42, v4, v54
	v_fmac_f32_e32 v43, v1, v55
	v_fmac_f32_e32 v42, v5, v55
	ds_read_b128 v[50:53], v96 offset:32768
	ds_read_b128 v[164:167], v96 offset:33792
	s_waitcnt lgkmcnt(1)
	v_fma_f32 v49, v92, v50, 0
	v_fma_f32 v48, v94, v50, 0
	v_fmac_f32_e32 v49, v93, v51
	v_fmac_f32_e32 v48, v95, v51
	v_fmac_f32_e32 v49, v84, v52
	v_fmac_f32_e32 v48, v88, v52
	v_fmac_f32_e32 v49, v85, v53
	v_fmac_f32_e32 v48, v89, v53
	ds_read_b128 v[50:53], v96 offset:34816
	s_waitcnt lgkmcnt(1)
	v_fmac_f32_e32 v49, v86, v164
	v_fmac_f32_e32 v48, v90, v164
	v_fmac_f32_e32 v49, v87, v165
	v_fmac_f32_e32 v48, v91, v165
	v_fmac_f32_e32 v49, v80, v166
	v_fmac_f32_e32 v48, v82, v166
	v_fmac_f32_e32 v49, v81, v167
	v_fmac_f32_e32 v48, v83, v167
	ds_read_b128 v[164:167], v96 offset:35840
	s_waitcnt lgkmcnt(1)
	v_fmac_f32_e32 v49, v60, v50
	v_fmac_f32_e32 v48, v62, v50
	v_fmac_f32_e32 v49, v61, v51
	v_fmac_f32_e32 v48, v63, v51
	v_fmac_f32_e32 v49, v46, v52
	v_fmac_f32_e32 v48, v58, v52
	v_fmac_f32_e32 v49, v47, v53
	v_fmac_f32_e32 v48, v59, v53
	ds_read_b128 v[50:53], v96 offset:36864
	s_waitcnt lgkmcnt(1)
	v_fmac_f32_e32 v49, v56, v164
	v_fmac_f32_e32 v48, v38, v164
	v_fmac_f32_e32 v49, v57, v165
	v_fmac_f32_e32 v48, v39, v165
	v_fmac_f32_e32 v49, v44, v166
	v_fmac_f32_e32 v48, v36, v166
	v_fmac_f32_e32 v49, v45, v167
	v_fmac_f32_e32 v48, v37, v167
	ds_read_b128 v[164:167], v96 offset:37888
	s_waitcnt lgkmcnt(1)
	v_fmac_f32_e32 v49, v28, v50
	v_fmac_f32_e32 v48, v30, v50
	v_fmac_f32_e32 v49, v29, v51
	v_fmac_f32_e32 v48, v31, v51
	v_fmac_f32_e32 v49, v20, v52
	v_fmac_f32_e32 v48, v24, v52
	v_fmac_f32_e32 v49, v21, v53
	v_fmac_f32_e32 v48, v25, v53
	ds_read_b128 v[50:53], v96 offset:38912
	s_waitcnt lgkmcnt(1)
	v_fmac_f32_e32 v49, v22, v164
	v_fmac_f32_e32 v48, v26, v164
	v_fmac_f32_e32 v49, v23, v165
	v_fmac_f32_e32 v48, v27, v165
	v_fmac_f32_e32 v49, v16, v166
	v_fmac_f32_e32 v48, v18, v166
	v_fmac_f32_e32 v49, v17, v167
	v_fmac_f32_e32 v48, v19, v167
	ds_read_b128 v[164:167], v96 offset:39936
	s_waitcnt lgkmcnt(1)
	v_fmac_f32_e32 v49, v12, v50
	v_fmac_f32_e32 v48, v14, v50
	v_fmac_f32_e32 v49, v13, v51
	v_fmac_f32_e32 v48, v15, v51
	v_fmac_f32_e32 v49, v2, v52
	v_fmac_f32_e32 v48, v6, v52
	v_fmac_f32_e32 v49, v3, v53
	v_fmac_f32_e32 v48, v7, v53
	s_waitcnt lgkmcnt(0)
	v_fmac_f32_e32 v49, v8, v164
	v_fmac_f32_e32 v48, v10, v164
	v_fmac_f32_e32 v49, v9, v165
	v_fmac_f32_e32 v48, v11, v165
	v_fmac_f32_e32 v49, v0, v166
	v_fmac_f32_e32 v48, v4, v166
	v_fmac_f32_e32 v49, v1, v167
	v_fmac_f32_e32 v48, v5, v167
	ds_read_b128 v[52:55], v96 offset:40960
	ds_read_b128 v[164:167], v96 offset:41984
	s_waitcnt lgkmcnt(1)
	v_fma_f32 v51, v92, v52, 0
	v_fma_f32 v50, v94, v52, 0
	v_fmac_f32_e32 v51, v93, v53
	v_fmac_f32_e32 v50, v95, v53
	v_fmac_f32_e32 v51, v84, v54
	v_fmac_f32_e32 v50, v88, v54
	v_fmac_f32_e32 v51, v85, v55
	v_fmac_f32_e32 v50, v89, v55
	ds_read_b128 v[52:55], v96 offset:43008
	s_waitcnt lgkmcnt(1)
	v_fmac_f32_e32 v51, v86, v164
	v_fmac_f32_e32 v50, v90, v164
	v_fmac_f32_e32 v51, v87, v165
	v_fmac_f32_e32 v50, v91, v165
	v_fmac_f32_e32 v51, v80, v166
	v_fmac_f32_e32 v50, v82, v166
	v_fmac_f32_e32 v51, v81, v167
	v_fmac_f32_e32 v50, v83, v167
	ds_read_b128 v[164:167], v96 offset:44032
	s_waitcnt lgkmcnt(1)
	v_fmac_f32_e32 v51, v60, v52
	v_fmac_f32_e32 v50, v62, v52
	v_fmac_f32_e32 v51, v61, v53
	v_fmac_f32_e32 v50, v63, v53
	v_fmac_f32_e32 v51, v46, v54
	v_fmac_f32_e32 v50, v58, v54
	v_fmac_f32_e32 v51, v47, v55
	v_fmac_f32_e32 v50, v59, v55
	ds_read_b128 v[52:55], v96 offset:45056
	s_waitcnt lgkmcnt(1)
	v_fmac_f32_e32 v51, v56, v164
	v_fmac_f32_e32 v50, v38, v164
	v_fmac_f32_e32 v51, v57, v165
	v_fmac_f32_e32 v50, v39, v165
	v_fmac_f32_e32 v51, v44, v166
	v_fmac_f32_e32 v50, v36, v166
	v_fmac_f32_e32 v51, v45, v167
	v_fmac_f32_e32 v50, v37, v167
	ds_read_b128 v[164:167], v96 offset:46080
	s_waitcnt lgkmcnt(1)
	v_fmac_f32_e32 v51, v28, v52
	v_fmac_f32_e32 v50, v30, v52
	v_fmac_f32_e32 v51, v29, v53
	v_fmac_f32_e32 v50, v31, v53
	v_fmac_f32_e32 v51, v20, v54
	v_fmac_f32_e32 v50, v24, v54
	v_fmac_f32_e32 v51, v21, v55
	v_fmac_f32_e32 v50, v25, v55
	ds_read_b128 v[52:55], v96 offset:47104
	s_waitcnt lgkmcnt(1)
	v_fmac_f32_e32 v51, v22, v164
	v_fmac_f32_e32 v50, v26, v164
	v_fmac_f32_e32 v51, v23, v165
	v_fmac_f32_e32 v50, v27, v165
	v_fmac_f32_e32 v51, v16, v166
	v_fmac_f32_e32 v50, v18, v166
	v_fmac_f32_e32 v51, v17, v167
	v_fmac_f32_e32 v50, v19, v167
	ds_read_b128 v[164:167], v96 offset:48128
	s_waitcnt lgkmcnt(1)
	v_fmac_f32_e32 v51, v12, v52
	v_fmac_f32_e32 v50, v14, v52
	v_fmac_f32_e32 v51, v13, v53
	v_fmac_f32_e32 v50, v15, v53
	v_fmac_f32_e32 v51, v2, v54
	v_fmac_f32_e32 v50, v6, v54
	v_fmac_f32_e32 v51, v3, v55
	v_fmac_f32_e32 v50, v7, v55
	s_waitcnt lgkmcnt(0)
	v_fmac_f32_e32 v51, v8, v164
	v_fmac_f32_e32 v50, v10, v164
	v_fmac_f32_e32 v51, v9, v165
	v_fmac_f32_e32 v50, v11, v165
	v_fmac_f32_e32 v51, v0, v166
	v_fmac_f32_e32 v50, v4, v166
	v_fmac_f32_e32 v51, v1, v167
	v_fmac_f32_e32 v50, v5, v167
	ds_read_b128 v[164:167], v96 offset:49152
	ds_read_b128 v[168:171], v96 offset:50176
	s_waitcnt lgkmcnt(1)
	v_fma_f32 v53, v92, v164, 0
	v_fma_f32 v52, v94, v164, 0
	v_fmac_f32_e32 v53, v93, v165
	v_fmac_f32_e32 v52, v95, v165
	v_fmac_f32_e32 v53, v84, v166
	v_fmac_f32_e32 v52, v88, v166
	v_fmac_f32_e32 v53, v85, v167
	v_fmac_f32_e32 v52, v89, v167
	ds_read_b128 v[164:167], v96 offset:51200
	s_waitcnt lgkmcnt(1)
	v_fmac_f32_e32 v53, v86, v168
	v_fmac_f32_e32 v52, v90, v168
	v_fmac_f32_e32 v53, v87, v169
	v_fmac_f32_e32 v52, v91, v169
	v_fmac_f32_e32 v53, v80, v170
	v_fmac_f32_e32 v52, v82, v170
	v_fmac_f32_e32 v53, v81, v171
	v_fmac_f32_e32 v52, v83, v171
	ds_read_b128 v[168:171], v96 offset:52224
	s_waitcnt lgkmcnt(1)
	v_fmac_f32_e32 v53, v60, v164
	v_fmac_f32_e32 v52, v62, v164
	v_fmac_f32_e32 v53, v61, v165
	v_fmac_f32_e32 v52, v63, v165
	v_fmac_f32_e32 v53, v46, v166
	v_fmac_f32_e32 v52, v58, v166
	v_fmac_f32_e32 v53, v47, v167
	v_fmac_f32_e32 v52, v59, v167
	ds_read_b128 v[164:167], v96 offset:53248
	s_waitcnt lgkmcnt(1)
	v_fmac_f32_e32 v53, v56, v168
	v_fmac_f32_e32 v52, v38, v168
	v_fmac_f32_e32 v53, v57, v169
	v_fmac_f32_e32 v52, v39, v169
	v_fmac_f32_e32 v53, v44, v170
	v_fmac_f32_e32 v52, v36, v170
	v_fmac_f32_e32 v53, v45, v171
	v_fmac_f32_e32 v52, v37, v171
	ds_read_b128 v[168:171], v96 offset:54272
	s_waitcnt lgkmcnt(1)
	v_fmac_f32_e32 v53, v28, v164
	v_fmac_f32_e32 v52, v30, v164
	v_fmac_f32_e32 v53, v29, v165
	v_fmac_f32_e32 v52, v31, v165
	v_fmac_f32_e32 v53, v20, v166
	v_fmac_f32_e32 v52, v24, v166
	v_fmac_f32_e32 v53, v21, v167
	v_fmac_f32_e32 v52, v25, v167
	ds_read_b128 v[164:167], v96 offset:55296
	s_waitcnt lgkmcnt(1)
	v_fmac_f32_e32 v53, v22, v168
	v_fmac_f32_e32 v52, v26, v168
	v_fmac_f32_e32 v53, v23, v169
	v_fmac_f32_e32 v52, v27, v169
	v_fmac_f32_e32 v53, v16, v170
	v_fmac_f32_e32 v52, v18, v170
	v_fmac_f32_e32 v53, v17, v171
	v_fmac_f32_e32 v52, v19, v171
	ds_read_b128 v[168:171], v96 offset:56320
	s_waitcnt lgkmcnt(1)
	v_fmac_f32_e32 v53, v12, v164
	v_fmac_f32_e32 v52, v14, v164
	v_fmac_f32_e32 v53, v13, v165
	v_fmac_f32_e32 v52, v15, v165
	v_fmac_f32_e32 v53, v2, v166
	v_fmac_f32_e32 v52, v6, v166
	v_fmac_f32_e32 v53, v3, v167
	v_fmac_f32_e32 v52, v7, v167
	s_waitcnt lgkmcnt(0)
	v_fmac_f32_e32 v53, v8, v168
	v_fmac_f32_e32 v52, v10, v168
	v_fmac_f32_e32 v53, v9, v169
	v_fmac_f32_e32 v52, v11, v169
	v_fmac_f32_e32 v53, v0, v170
	v_fmac_f32_e32 v52, v4, v170
	v_fmac_f32_e32 v53, v1, v171
	v_fmac_f32_e32 v52, v5, v171
	ds_read_b128 v[164:167], v96 offset:57344
	ds_read_b128 v[168:171], v96 offset:58368
	s_waitcnt lgkmcnt(1)
	v_fma_f32 v55, v92, v164, 0
	v_fma_f32 v54, v94, v164, 0
	v_fmac_f32_e32 v55, v93, v165
	v_fmac_f32_e32 v54, v95, v165
	v_fmac_f32_e32 v55, v84, v166
	v_fmac_f32_e32 v54, v88, v166
	v_fmac_f32_e32 v55, v85, v167
	v_fmac_f32_e32 v54, v89, v167
	ds_read_b128 v[164:167], v96 offset:59392
	s_waitcnt lgkmcnt(1)
	v_fmac_f32_e32 v55, v86, v168
	v_fmac_f32_e32 v54, v90, v168
	v_fmac_f32_e32 v55, v87, v169
	v_fmac_f32_e32 v54, v91, v169
	v_fmac_f32_e32 v55, v80, v170
	v_fmac_f32_e32 v54, v82, v170
	v_fmac_f32_e32 v55, v81, v171
	v_fmac_f32_e32 v54, v83, v171
	ds_read_b128 v[168:171], v96 offset:60416
	s_waitcnt lgkmcnt(1)
	v_fmac_f32_e32 v55, v60, v164
	v_fmac_f32_e32 v54, v62, v164
	v_fmac_f32_e32 v55, v61, v165
	v_fmac_f32_e32 v54, v63, v165
	v_fmac_f32_e32 v55, v46, v166
	v_fmac_f32_e32 v54, v58, v166
	v_fmac_f32_e32 v55, v47, v167
	v_fmac_f32_e32 v54, v59, v167
	ds_read_b128 v[164:167], v96 offset:61440
	s_waitcnt lgkmcnt(1)
	v_fmac_f32_e32 v55, v56, v168
	v_fmac_f32_e32 v54, v38, v168
	v_fmac_f32_e32 v55, v57, v169
	v_fmac_f32_e32 v54, v39, v169
	v_fmac_f32_e32 v55, v44, v170
	v_fmac_f32_e32 v54, v36, v170
	v_fmac_f32_e32 v55, v45, v171
	v_fmac_f32_e32 v54, v37, v171
	ds_read_b128 v[168:171], v96 offset:62464
	s_waitcnt lgkmcnt(1)
	v_fmac_f32_e32 v55, v28, v164
	v_fmac_f32_e32 v54, v30, v164
	v_fmac_f32_e32 v55, v29, v165
	v_fmac_f32_e32 v54, v31, v165
	v_fmac_f32_e32 v55, v20, v166
	v_fmac_f32_e32 v54, v24, v166
	v_fmac_f32_e32 v55, v21, v167
	v_fmac_f32_e32 v54, v25, v167
	ds_read_b128 v[164:167], v96 offset:63488
	s_waitcnt lgkmcnt(1)
	v_fmac_f32_e32 v55, v22, v168
	v_fmac_f32_e32 v54, v26, v168
	v_fmac_f32_e32 v55, v23, v169
	v_fmac_f32_e32 v54, v27, v169
	v_fmac_f32_e32 v55, v16, v170
	v_fmac_f32_e32 v54, v18, v170
	v_fmac_f32_e32 v55, v17, v171
	v_fmac_f32_e32 v54, v19, v171
	ds_read_b128 v[168:171], v96 offset:64512
	s_waitcnt lgkmcnt(1)
	v_fmac_f32_e32 v55, v12, v164
	v_fmac_f32_e32 v54, v14, v164
	v_fmac_f32_e32 v55, v13, v165
	v_fmac_f32_e32 v54, v15, v165
	v_fmac_f32_e32 v55, v2, v166
	v_fmac_f32_e32 v54, v6, v166
	v_fmac_f32_e32 v55, v3, v167
	v_fmac_f32_e32 v54, v7, v167
	s_waitcnt lgkmcnt(0)
	v_fmac_f32_e32 v55, v8, v168
	v_fmac_f32_e32 v54, v10, v168
	v_fmac_f32_e32 v55, v9, v169
	v_fmac_f32_e32 v54, v11, v169
	v_fmac_f32_e32 v55, v0, v170
	v_fmac_f32_e32 v54, v4, v170
	v_fmac_f32_e32 v55, v1, v171
	v_fmac_f32_e32 v54, v5, v171
	ds_read_b128 v[166:169], v97
	ds_read_b128 v[170:173], v98
	s_waitcnt lgkmcnt(1)
	v_fma_f32 v165, v92, v166, 0
	v_fma_f32 v164, v94, v166, 0
	v_fmac_f32_e32 v165, v93, v167
	v_fmac_f32_e32 v164, v95, v167
	v_fmac_f32_e32 v165, v84, v168
	v_fmac_f32_e32 v164, v88, v168
	v_fmac_f32_e32 v165, v85, v169
	v_fmac_f32_e32 v164, v89, v169
	ds_read_b128 v[166:169], v99
	s_waitcnt lgkmcnt(1)
	v_fmac_f32_e32 v165, v86, v170
	v_fmac_f32_e32 v164, v90, v170
	v_fmac_f32_e32 v165, v87, v171
	v_fmac_f32_e32 v164, v91, v171
	v_fmac_f32_e32 v165, v80, v172
	v_fmac_f32_e32 v164, v82, v172
	v_fmac_f32_e32 v165, v81, v173
	v_fmac_f32_e32 v164, v83, v173
	ds_read_b128 v[170:173], v100
	s_waitcnt lgkmcnt(1)
	v_fmac_f32_e32 v165, v60, v166
	v_fmac_f32_e32 v164, v62, v166
	v_fmac_f32_e32 v165, v61, v167
	v_fmac_f32_e32 v164, v63, v167
	v_fmac_f32_e32 v165, v46, v168
	v_fmac_f32_e32 v164, v58, v168
	v_fmac_f32_e32 v165, v47, v169
	v_fmac_f32_e32 v164, v59, v169
	ds_read_b128 v[166:169], v101
	s_waitcnt lgkmcnt(1)
	v_fmac_f32_e32 v165, v56, v170
	v_fmac_f32_e32 v164, v38, v170
	v_fmac_f32_e32 v165, v57, v171
	v_fmac_f32_e32 v164, v39, v171
	v_fmac_f32_e32 v165, v44, v172
	v_fmac_f32_e32 v164, v36, v172
	v_fmac_f32_e32 v165, v45, v173
	v_fmac_f32_e32 v164, v37, v173
	ds_read_b128 v[170:173], v102
	s_waitcnt lgkmcnt(1)
	v_fmac_f32_e32 v165, v28, v166
	v_fmac_f32_e32 v164, v30, v166
	v_fmac_f32_e32 v165, v29, v167
	v_fmac_f32_e32 v164, v31, v167
	v_fmac_f32_e32 v165, v20, v168
	v_fmac_f32_e32 v164, v24, v168
	v_fmac_f32_e32 v165, v21, v169
	v_fmac_f32_e32 v164, v25, v169
	ds_read_b128 v[166:169], v103
	s_waitcnt lgkmcnt(1)
	v_fmac_f32_e32 v165, v22, v170
	v_fmac_f32_e32 v164, v26, v170
	v_fmac_f32_e32 v165, v23, v171
	v_fmac_f32_e32 v164, v27, v171
	v_fmac_f32_e32 v165, v16, v172
	v_fmac_f32_e32 v164, v18, v172
	v_fmac_f32_e32 v165, v17, v173
	v_fmac_f32_e32 v164, v19, v173
	ds_read_b128 v[170:173], v104
	s_waitcnt lgkmcnt(1)
	v_fmac_f32_e32 v165, v12, v166
	v_fmac_f32_e32 v164, v14, v166
	v_fmac_f32_e32 v165, v13, v167
	v_fmac_f32_e32 v164, v15, v167
	v_fmac_f32_e32 v165, v2, v168
	v_fmac_f32_e32 v164, v6, v168
	v_fmac_f32_e32 v165, v3, v169
	v_fmac_f32_e32 v164, v7, v169
	s_waitcnt lgkmcnt(0)
	v_fmac_f32_e32 v165, v8, v170
	v_fmac_f32_e32 v164, v10, v170
	v_fmac_f32_e32 v165, v9, v171
	v_fmac_f32_e32 v164, v11, v171
	v_fmac_f32_e32 v165, v0, v172
	v_fmac_f32_e32 v164, v4, v172
	v_fmac_f32_e32 v165, v1, v173
	v_fmac_f32_e32 v164, v5, v173
	ds_read_b128 v[168:171], v105
	ds_read_b128 v[172:175], v106
	s_waitcnt lgkmcnt(1)
	v_fma_f32 v167, v92, v168, 0
	v_fma_f32 v166, v94, v168, 0
	v_fmac_f32_e32 v167, v93, v169
	v_fmac_f32_e32 v166, v95, v169
	v_fmac_f32_e32 v167, v84, v170
	v_fmac_f32_e32 v166, v88, v170
	v_fmac_f32_e32 v167, v85, v171
	v_fmac_f32_e32 v166, v89, v171
	ds_read_b128 v[168:171], v107
	s_waitcnt lgkmcnt(1)
	v_fmac_f32_e32 v167, v86, v172
	v_fmac_f32_e32 v166, v90, v172
	v_fmac_f32_e32 v167, v87, v173
	v_fmac_f32_e32 v166, v91, v173
	v_fmac_f32_e32 v167, v80, v174
	v_fmac_f32_e32 v166, v82, v174
	v_fmac_f32_e32 v167, v81, v175
	v_fmac_f32_e32 v166, v83, v175
	ds_read_b128 v[172:175], v108
	s_waitcnt lgkmcnt(1)
	v_fmac_f32_e32 v167, v60, v168
	v_fmac_f32_e32 v166, v62, v168
	v_fmac_f32_e32 v167, v61, v169
	v_fmac_f32_e32 v166, v63, v169
	v_fmac_f32_e32 v167, v46, v170
	v_fmac_f32_e32 v166, v58, v170
	v_fmac_f32_e32 v167, v47, v171
	v_fmac_f32_e32 v166, v59, v171
	ds_read_b128 v[168:171], v109
	s_waitcnt lgkmcnt(1)
	v_fmac_f32_e32 v167, v56, v172
	v_fmac_f32_e32 v166, v38, v172
	v_fmac_f32_e32 v167, v57, v173
	v_fmac_f32_e32 v166, v39, v173
	v_fmac_f32_e32 v167, v44, v174
	v_fmac_f32_e32 v166, v36, v174
	v_fmac_f32_e32 v167, v45, v175
	v_fmac_f32_e32 v166, v37, v175
	ds_read_b128 v[172:175], v110
	s_waitcnt lgkmcnt(1)
	v_fmac_f32_e32 v167, v28, v168
	v_fmac_f32_e32 v166, v30, v168
	v_fmac_f32_e32 v167, v29, v169
	v_fmac_f32_e32 v166, v31, v169
	v_fmac_f32_e32 v167, v20, v170
	v_fmac_f32_e32 v166, v24, v170
	v_fmac_f32_e32 v167, v21, v171
	v_fmac_f32_e32 v166, v25, v171
	ds_read_b128 v[168:171], v111
	s_waitcnt lgkmcnt(1)
	v_fmac_f32_e32 v167, v22, v172
	v_fmac_f32_e32 v166, v26, v172
	v_fmac_f32_e32 v167, v23, v173
	v_fmac_f32_e32 v166, v27, v173
	v_fmac_f32_e32 v167, v16, v174
	v_fmac_f32_e32 v166, v18, v174
	v_fmac_f32_e32 v167, v17, v175
	v_fmac_f32_e32 v166, v19, v175
	ds_read_b128 v[172:175], v112
	s_waitcnt lgkmcnt(1)
	v_fmac_f32_e32 v167, v12, v168
	v_fmac_f32_e32 v166, v14, v168
	v_fmac_f32_e32 v167, v13, v169
	v_fmac_f32_e32 v166, v15, v169
	v_fmac_f32_e32 v167, v2, v170
	v_fmac_f32_e32 v166, v6, v170
	v_fmac_f32_e32 v167, v3, v171
	v_fmac_f32_e32 v166, v7, v171
	s_waitcnt lgkmcnt(0)
	v_fmac_f32_e32 v167, v8, v172
	v_fmac_f32_e32 v166, v10, v172
	v_fmac_f32_e32 v167, v9, v173
	v_fmac_f32_e32 v166, v11, v173
	v_fmac_f32_e32 v167, v0, v174
	v_fmac_f32_e32 v166, v4, v174
	v_fmac_f32_e32 v167, v1, v175
	v_fmac_f32_e32 v166, v5, v175
	ds_read_b128 v[170:173], v113
	ds_read_b128 v[174:177], v114
	s_waitcnt lgkmcnt(1)
	v_fma_f32 v169, v92, v170, 0
	v_fma_f32 v168, v94, v170, 0
	v_fmac_f32_e32 v169, v93, v171
	v_fmac_f32_e32 v168, v95, v171
	v_fmac_f32_e32 v169, v84, v172
	v_fmac_f32_e32 v168, v88, v172
	v_fmac_f32_e32 v169, v85, v173
	v_fmac_f32_e32 v168, v89, v173
	ds_read_b128 v[170:173], v115
	s_waitcnt lgkmcnt(1)
	v_fmac_f32_e32 v169, v86, v174
	v_fmac_f32_e32 v168, v90, v174
	v_fmac_f32_e32 v169, v87, v175
	v_fmac_f32_e32 v168, v91, v175
	v_fmac_f32_e32 v169, v80, v176
	v_fmac_f32_e32 v168, v82, v176
	v_fmac_f32_e32 v169, v81, v177
	v_fmac_f32_e32 v168, v83, v177
	ds_read_b128 v[174:177], v116
	s_waitcnt lgkmcnt(1)
	v_fmac_f32_e32 v169, v60, v170
	v_fmac_f32_e32 v168, v62, v170
	v_fmac_f32_e32 v169, v61, v171
	v_fmac_f32_e32 v168, v63, v171
	v_fmac_f32_e32 v169, v46, v172
	v_fmac_f32_e32 v168, v58, v172
	v_fmac_f32_e32 v169, v47, v173
	v_fmac_f32_e32 v168, v59, v173
	ds_read_b128 v[170:173], v117
	s_waitcnt lgkmcnt(1)
	v_fmac_f32_e32 v169, v56, v174
	v_fmac_f32_e32 v168, v38, v174
	v_fmac_f32_e32 v169, v57, v175
	v_fmac_f32_e32 v168, v39, v175
	v_fmac_f32_e32 v169, v44, v176
	v_fmac_f32_e32 v168, v36, v176
	v_fmac_f32_e32 v169, v45, v177
	v_fmac_f32_e32 v168, v37, v177
	ds_read_b128 v[174:177], v118
	s_waitcnt lgkmcnt(1)
	v_fmac_f32_e32 v169, v28, v170
	v_fmac_f32_e32 v168, v30, v170
	v_fmac_f32_e32 v169, v29, v171
	v_fmac_f32_e32 v168, v31, v171
	v_fmac_f32_e32 v169, v20, v172
	v_fmac_f32_e32 v168, v24, v172
	v_fmac_f32_e32 v169, v21, v173
	v_fmac_f32_e32 v168, v25, v173
	ds_read_b128 v[170:173], v119
	s_waitcnt lgkmcnt(1)
	v_fmac_f32_e32 v169, v22, v174
	v_fmac_f32_e32 v168, v26, v174
	v_fmac_f32_e32 v169, v23, v175
	v_fmac_f32_e32 v168, v27, v175
	v_fmac_f32_e32 v169, v16, v176
	v_fmac_f32_e32 v168, v18, v176
	v_fmac_f32_e32 v169, v17, v177
	v_fmac_f32_e32 v168, v19, v177
	ds_read_b128 v[174:177], v120
	s_waitcnt lgkmcnt(1)
	v_fmac_f32_e32 v169, v12, v170
	v_fmac_f32_e32 v168, v14, v170
	v_fmac_f32_e32 v169, v13, v171
	v_fmac_f32_e32 v168, v15, v171
	v_fmac_f32_e32 v169, v2, v172
	v_fmac_f32_e32 v168, v6, v172
	v_fmac_f32_e32 v169, v3, v173
	v_fmac_f32_e32 v168, v7, v173
	s_waitcnt lgkmcnt(0)
	v_fmac_f32_e32 v169, v8, v174
	v_fmac_f32_e32 v168, v10, v174
	v_fmac_f32_e32 v169, v9, v175
	v_fmac_f32_e32 v168, v11, v175
	v_fmac_f32_e32 v169, v0, v176
	v_fmac_f32_e32 v168, v4, v176
	v_fmac_f32_e32 v169, v1, v177
	v_fmac_f32_e32 v168, v5, v177
	ds_read_b128 v[172:175], v121
	ds_read_b128 v[176:179], v122
	s_waitcnt lgkmcnt(1)
	v_fma_f32 v171, v92, v172, 0
	v_fma_f32 v170, v94, v172, 0
	v_fmac_f32_e32 v171, v93, v173
	v_fmac_f32_e32 v170, v95, v173
	v_fmac_f32_e32 v171, v84, v174
	v_fmac_f32_e32 v170, v88, v174
	v_fmac_f32_e32 v171, v85, v175
	v_fmac_f32_e32 v170, v89, v175
	ds_read_b128 v[172:175], v123
	s_waitcnt lgkmcnt(1)
	v_fmac_f32_e32 v171, v86, v176
	v_fmac_f32_e32 v170, v90, v176
	v_fmac_f32_e32 v171, v87, v177
	v_fmac_f32_e32 v170, v91, v177
	v_fmac_f32_e32 v171, v80, v178
	v_fmac_f32_e32 v170, v82, v178
	v_fmac_f32_e32 v171, v81, v179
	v_fmac_f32_e32 v170, v83, v179
	ds_read_b128 v[176:179], v124
	s_waitcnt lgkmcnt(1)
	v_fmac_f32_e32 v171, v60, v172
	v_fmac_f32_e32 v170, v62, v172
	v_fmac_f32_e32 v171, v61, v173
	v_fmac_f32_e32 v170, v63, v173
	v_fmac_f32_e32 v171, v46, v174
	v_fmac_f32_e32 v170, v58, v174
	v_fmac_f32_e32 v171, v47, v175
	v_fmac_f32_e32 v170, v59, v175
	ds_read_b128 v[172:175], v125
	s_waitcnt lgkmcnt(1)
	v_fmac_f32_e32 v171, v56, v176
	v_fmac_f32_e32 v170, v38, v176
	v_fmac_f32_e32 v171, v57, v177
	v_fmac_f32_e32 v170, v39, v177
	v_fmac_f32_e32 v171, v44, v178
	v_fmac_f32_e32 v170, v36, v178
	v_fmac_f32_e32 v171, v45, v179
	v_fmac_f32_e32 v170, v37, v179
	ds_read_b128 v[176:179], v126
	s_waitcnt lgkmcnt(1)
	v_fmac_f32_e32 v171, v28, v172
	v_fmac_f32_e32 v170, v30, v172
	v_fmac_f32_e32 v171, v29, v173
	v_fmac_f32_e32 v170, v31, v173
	v_fmac_f32_e32 v171, v20, v174
	v_fmac_f32_e32 v170, v24, v174
	v_fmac_f32_e32 v171, v21, v175
	v_fmac_f32_e32 v170, v25, v175
	ds_read_b128 v[172:175], v127
	s_waitcnt lgkmcnt(1)
	v_fmac_f32_e32 v171, v22, v176
	v_fmac_f32_e32 v170, v26, v176
	v_fmac_f32_e32 v171, v23, v177
	v_fmac_f32_e32 v170, v27, v177
	v_fmac_f32_e32 v171, v16, v178
	v_fmac_f32_e32 v170, v18, v178
	v_fmac_f32_e32 v171, v17, v179
	v_fmac_f32_e32 v170, v19, v179
	ds_read_b128 v[176:179], v128
	s_waitcnt lgkmcnt(1)
	v_fmac_f32_e32 v171, v12, v172
	v_fmac_f32_e32 v170, v14, v172
	v_fmac_f32_e32 v171, v13, v173
	v_fmac_f32_e32 v170, v15, v173
	v_fmac_f32_e32 v171, v2, v174
	v_fmac_f32_e32 v170, v6, v174
	v_fmac_f32_e32 v171, v3, v175
	v_fmac_f32_e32 v170, v7, v175
	s_waitcnt lgkmcnt(0)
	v_fmac_f32_e32 v171, v8, v176
	v_fmac_f32_e32 v170, v10, v176
	v_fmac_f32_e32 v171, v9, v177
	v_fmac_f32_e32 v170, v11, v177
	v_fmac_f32_e32 v171, v0, v178
	v_fmac_f32_e32 v170, v4, v178
	v_fmac_f32_e32 v171, v1, v179
	v_fmac_f32_e32 v170, v5, v179
	ds_read_b128 v[174:177], v129
	ds_read_b128 v[178:181], v130
	s_waitcnt lgkmcnt(1)
	v_fma_f32 v173, v92, v174, 0
	v_fma_f32 v172, v94, v174, 0
	v_fmac_f32_e32 v173, v93, v175
	v_fmac_f32_e32 v172, v95, v175
	v_fmac_f32_e32 v173, v84, v176
	v_fmac_f32_e32 v172, v88, v176
	v_fmac_f32_e32 v173, v85, v177
	v_fmac_f32_e32 v172, v89, v177
	ds_read_b128 v[174:177], v131
	s_waitcnt lgkmcnt(1)
	v_fmac_f32_e32 v173, v86, v178
	v_fmac_f32_e32 v172, v90, v178
	v_fmac_f32_e32 v173, v87, v179
	v_fmac_f32_e32 v172, v91, v179
	v_fmac_f32_e32 v173, v80, v180
	v_fmac_f32_e32 v172, v82, v180
	v_fmac_f32_e32 v173, v81, v181
	v_fmac_f32_e32 v172, v83, v181
	ds_read_b128 v[178:181], v132
	s_waitcnt lgkmcnt(1)
	v_fmac_f32_e32 v173, v60, v174
	v_fmac_f32_e32 v172, v62, v174
	v_fmac_f32_e32 v173, v61, v175
	v_fmac_f32_e32 v172, v63, v175
	v_fmac_f32_e32 v173, v46, v176
	v_fmac_f32_e32 v172, v58, v176
	v_fmac_f32_e32 v173, v47, v177
	v_fmac_f32_e32 v172, v59, v177
	ds_read_b128 v[174:177], v133
	s_waitcnt lgkmcnt(1)
	v_fmac_f32_e32 v173, v56, v178
	v_fmac_f32_e32 v172, v38, v178
	v_fmac_f32_e32 v173, v57, v179
	v_fmac_f32_e32 v172, v39, v179
	v_fmac_f32_e32 v173, v44, v180
	v_fmac_f32_e32 v172, v36, v180
	v_fmac_f32_e32 v173, v45, v181
	v_fmac_f32_e32 v172, v37, v181
	ds_read_b128 v[178:181], v134
	s_waitcnt lgkmcnt(1)
	v_fmac_f32_e32 v173, v28, v174
	v_fmac_f32_e32 v172, v30, v174
	v_fmac_f32_e32 v173, v29, v175
	v_fmac_f32_e32 v172, v31, v175
	v_fmac_f32_e32 v173, v20, v176
	v_fmac_f32_e32 v172, v24, v176
	v_fmac_f32_e32 v173, v21, v177
	v_fmac_f32_e32 v172, v25, v177
	ds_read_b128 v[174:177], v135
	s_waitcnt lgkmcnt(1)
	v_fmac_f32_e32 v173, v22, v178
	v_fmac_f32_e32 v172, v26, v178
	v_fmac_f32_e32 v173, v23, v179
	v_fmac_f32_e32 v172, v27, v179
	v_fmac_f32_e32 v173, v16, v180
	v_fmac_f32_e32 v172, v18, v180
	v_fmac_f32_e32 v173, v17, v181
	v_fmac_f32_e32 v172, v19, v181
	ds_read_b128 v[178:181], v136
	s_waitcnt lgkmcnt(1)
	v_fmac_f32_e32 v173, v12, v174
	v_fmac_f32_e32 v172, v14, v174
	v_fmac_f32_e32 v173, v13, v175
	v_fmac_f32_e32 v172, v15, v175
	v_fmac_f32_e32 v173, v2, v176
	v_fmac_f32_e32 v172, v6, v176
	v_fmac_f32_e32 v173, v3, v177
	v_fmac_f32_e32 v172, v7, v177
	s_waitcnt lgkmcnt(0)
	v_fmac_f32_e32 v173, v8, v178
	v_fmac_f32_e32 v172, v10, v178
	v_fmac_f32_e32 v173, v9, v179
	v_fmac_f32_e32 v172, v11, v179
	v_fmac_f32_e32 v173, v0, v180
	v_fmac_f32_e32 v172, v4, v180
	v_fmac_f32_e32 v173, v1, v181
	v_fmac_f32_e32 v172, v5, v181
	ds_read_b128 v[176:179], v137
	ds_read_b128 v[180:183], v138
	s_waitcnt lgkmcnt(1)
	v_fma_f32 v175, v92, v176, 0
	v_fma_f32 v174, v94, v176, 0
	v_fmac_f32_e32 v175, v93, v177
	v_fmac_f32_e32 v174, v95, v177
	v_fmac_f32_e32 v175, v84, v178
	v_fmac_f32_e32 v174, v88, v178
	v_fmac_f32_e32 v175, v85, v179
	v_fmac_f32_e32 v174, v89, v179
	ds_read_b128 v[176:179], v139
	s_waitcnt lgkmcnt(1)
	v_fmac_f32_e32 v175, v86, v180
	v_fmac_f32_e32 v174, v90, v180
	v_fmac_f32_e32 v175, v87, v181
	v_fmac_f32_e32 v174, v91, v181
	v_fmac_f32_e32 v175, v80, v182
	v_fmac_f32_e32 v174, v82, v182
	v_fmac_f32_e32 v175, v81, v183
	v_fmac_f32_e32 v174, v83, v183
	ds_read_b128 v[180:183], v140
	s_waitcnt lgkmcnt(1)
	v_fmac_f32_e32 v175, v60, v176
	v_fmac_f32_e32 v174, v62, v176
	v_fmac_f32_e32 v175, v61, v177
	v_fmac_f32_e32 v174, v63, v177
	v_fmac_f32_e32 v175, v46, v178
	v_fmac_f32_e32 v174, v58, v178
	v_fmac_f32_e32 v175, v47, v179
	v_fmac_f32_e32 v174, v59, v179
	ds_read_b128 v[176:179], v141
	s_waitcnt lgkmcnt(1)
	v_fmac_f32_e32 v175, v56, v180
	v_fmac_f32_e32 v174, v38, v180
	v_fmac_f32_e32 v175, v57, v181
	v_fmac_f32_e32 v174, v39, v181
	v_fmac_f32_e32 v175, v44, v182
	v_fmac_f32_e32 v174, v36, v182
	v_fmac_f32_e32 v175, v45, v183
	v_fmac_f32_e32 v174, v37, v183
	ds_read_b128 v[180:183], v142
	s_waitcnt lgkmcnt(1)
	v_fmac_f32_e32 v175, v28, v176
	v_fmac_f32_e32 v174, v30, v176
	v_fmac_f32_e32 v175, v29, v177
	v_fmac_f32_e32 v174, v31, v177
	v_fmac_f32_e32 v175, v20, v178
	v_fmac_f32_e32 v174, v24, v178
	v_fmac_f32_e32 v175, v21, v179
	v_fmac_f32_e32 v174, v25, v179
	ds_read_b128 v[176:179], v143
	s_waitcnt lgkmcnt(1)
	v_fmac_f32_e32 v175, v22, v180
	v_fmac_f32_e32 v174, v26, v180
	v_fmac_f32_e32 v175, v23, v181
	v_fmac_f32_e32 v174, v27, v181
	v_fmac_f32_e32 v175, v16, v182
	v_fmac_f32_e32 v174, v18, v182
	v_fmac_f32_e32 v175, v17, v183
	v_fmac_f32_e32 v174, v19, v183
	ds_read_b128 v[180:183], v144
	s_waitcnt lgkmcnt(1)
	v_fmac_f32_e32 v175, v12, v176
	v_fmac_f32_e32 v174, v14, v176
	v_fmac_f32_e32 v175, v13, v177
	v_fmac_f32_e32 v174, v15, v177
	v_fmac_f32_e32 v175, v2, v178
	v_fmac_f32_e32 v174, v6, v178
	v_fmac_f32_e32 v175, v3, v179
	v_fmac_f32_e32 v174, v7, v179
	s_waitcnt lgkmcnt(0)
	v_fmac_f32_e32 v175, v8, v180
	v_fmac_f32_e32 v174, v10, v180
	v_fmac_f32_e32 v175, v9, v181
	v_fmac_f32_e32 v174, v11, v181
	v_fmac_f32_e32 v175, v0, v182
	v_fmac_f32_e32 v174, v4, v182
	v_fmac_f32_e32 v175, v1, v183
	v_fmac_f32_e32 v174, v5, v183
	ds_read_b128 v[176:179], v145
	ds_read_b128 v[180:183], v146
	s_waitcnt lgkmcnt(1)
	v_fma_f32 v184, v92, v176, 0
	v_fma_f32 v185, v94, v176, 0
	v_fmac_f32_e32 v184, v93, v177
	v_fmac_f32_e32 v185, v95, v177
	v_fmac_f32_e32 v184, v84, v178
	v_fmac_f32_e32 v185, v88, v178
	v_fmac_f32_e32 v184, v85, v179
	v_fmac_f32_e32 v185, v89, v179
	ds_read_b128 v[176:179], v147
	s_waitcnt lgkmcnt(1)
	v_fmac_f32_e32 v184, v86, v180
	v_fmac_f32_e32 v185, v90, v180
	v_fmac_f32_e32 v184, v87, v181
	v_fmac_f32_e32 v185, v91, v181
	v_fmac_f32_e32 v184, v80, v182
	v_fmac_f32_e32 v185, v82, v182
	v_fmac_f32_e32 v184, v81, v183
	v_fmac_f32_e32 v185, v83, v183
	ds_read_b128 v[180:183], v148
	s_waitcnt lgkmcnt(1)
	v_fmac_f32_e32 v184, v60, v176
	v_fmac_f32_e32 v185, v62, v176
	v_fmac_f32_e32 v184, v61, v177
	v_fmac_f32_e32 v185, v63, v177
	v_fmac_f32_e32 v184, v46, v178
	v_fmac_f32_e32 v185, v58, v178
	v_fmac_f32_e32 v184, v47, v179
	v_fmac_f32_e32 v185, v59, v179
	ds_read_b128 v[176:179], v149
	s_waitcnt lgkmcnt(1)
	v_fmac_f32_e32 v184, v56, v180
	v_fmac_f32_e32 v185, v38, v180
	v_fmac_f32_e32 v184, v57, v181
	v_fmac_f32_e32 v185, v39, v181
	v_fmac_f32_e32 v184, v44, v182
	v_fmac_f32_e32 v185, v36, v182
	v_fmac_f32_e32 v184, v45, v183
	v_fmac_f32_e32 v185, v37, v183
	ds_read_b128 v[180:183], v150
	s_waitcnt lgkmcnt(1)
	v_fmac_f32_e32 v184, v28, v176
	v_fmac_f32_e32 v185, v30, v176
	v_fmac_f32_e32 v184, v29, v177
	v_fmac_f32_e32 v185, v31, v177
	v_fmac_f32_e32 v184, v20, v178
	v_fmac_f32_e32 v185, v24, v178
	v_fmac_f32_e32 v184, v21, v179
	v_fmac_f32_e32 v185, v25, v179
	ds_read_b128 v[176:179], v151
	s_waitcnt lgkmcnt(1)
	v_fmac_f32_e32 v184, v22, v180
	v_fmac_f32_e32 v185, v26, v180
	v_fmac_f32_e32 v184, v23, v181
	v_fmac_f32_e32 v185, v27, v181
	v_fmac_f32_e32 v184, v16, v182
	v_fmac_f32_e32 v185, v18, v182
	v_fmac_f32_e32 v184, v17, v183
	v_fmac_f32_e32 v185, v19, v183
	ds_read_b128 v[180:183], v152
	s_waitcnt lgkmcnt(1)
	v_fmac_f32_e32 v184, v12, v176
	v_fmac_f32_e32 v185, v14, v176
	v_fmac_f32_e32 v184, v13, v177
	v_fmac_f32_e32 v185, v15, v177
	v_fmac_f32_e32 v184, v2, v178
	v_fmac_f32_e32 v185, v6, v178
	v_fmac_f32_e32 v184, v3, v179
	v_fmac_f32_e32 v185, v7, v179
	s_waitcnt lgkmcnt(0)
	v_fmac_f32_e32 v184, v8, v180
	v_fmac_f32_e32 v185, v10, v180
	v_fmac_f32_e32 v184, v9, v181
	v_fmac_f32_e32 v185, v11, v181
	v_fmac_f32_e32 v184, v0, v182
	v_fmac_f32_e32 v185, v4, v182
	v_fmac_f32_e32 v184, v1, v183
	v_fmac_f32_e32 v185, v5, v183
	ds_read_b128 v[176:179], v153
	ds_read_b128 v[180:183], v154
	s_waitcnt lgkmcnt(1)
	v_fma_f32 v92, v92, v176, 0
	v_fmac_f32_e32 v92, v93, v177
	v_fma_f32 v94, v94, v176, 0
	v_fmac_f32_e32 v92, v84, v178
	v_fmac_f32_e32 v94, v95, v177
	v_fmac_f32_e32 v92, v85, v179
	v_fmac_f32_e32 v94, v88, v178
	s_waitcnt lgkmcnt(0)
	v_fmac_f32_e32 v92, v86, v180
	v_fmac_f32_e32 v94, v89, v179
	v_fmac_f32_e32 v92, v87, v181
	ds_read_b128 v[84:87], v155
	v_fmac_f32_e32 v94, v90, v180
	v_fmac_f32_e32 v94, v91, v181
	v_fmac_f32_e32 v92, v80, v182
	v_fmac_f32_e32 v94, v82, v182
	v_fmac_f32_e32 v92, v81, v183
	v_fmac_f32_e32 v94, v83, v183
	ds_read_b128 v[80:83], v156
	s_waitcnt lgkmcnt(1)
	v_fmac_f32_e32 v92, v60, v84
	v_fmac_f32_e32 v92, v61, v85
	v_fmac_f32_e32 v94, v62, v84
	v_fmac_f32_e32 v92, v46, v86
	v_fmac_f32_e32 v94, v63, v85
	v_fmac_f32_e32 v92, v47, v87
	v_fmac_f32_e32 v94, v58, v86
	s_waitcnt lgkmcnt(0)
	v_fmac_f32_e32 v92, v56, v80
	v_fmac_f32_e32 v94, v59, v87
	v_fmac_f32_e32 v92, v57, v81
	ds_read_b128 v[56:59], v157
	v_fmac_f32_e32 v94, v38, v80
	v_fmac_f32_e32 v94, v39, v81
	v_fmac_f32_e32 v92, v44, v82
	v_fmac_f32_e32 v94, v36, v82
	v_fmac_f32_e32 v92, v45, v83
	v_fmac_f32_e32 v94, v37, v83
	ds_read_b128 v[36:39], v158
	s_waitcnt lgkmcnt(1)
	v_fmac_f32_e32 v92, v28, v56
	v_fmac_f32_e32 v92, v29, v57
	v_fmac_f32_e32 v94, v30, v56
	v_fmac_f32_e32 v92, v20, v58
	v_fmac_f32_e32 v94, v31, v57
	v_fmac_f32_e32 v92, v21, v59
	v_fmac_f32_e32 v94, v24, v58
	s_waitcnt lgkmcnt(0)
	v_fmac_f32_e32 v92, v22, v36
	v_fmac_f32_e32 v94, v25, v59
	v_fmac_f32_e32 v92, v23, v37
	ds_read_b128 v[20:23], v159
	v_fmac_f32_e32 v94, v26, v36
	v_fmac_f32_e32 v94, v27, v37
	v_fmac_f32_e32 v92, v16, v38
	v_fmac_f32_e32 v94, v18, v38
	v_fmac_f32_e32 v92, v17, v39
	v_fmac_f32_e32 v94, v19, v39
	ds_read_b128 v[16:19], v160
	s_waitcnt lgkmcnt(1)
	v_fmac_f32_e32 v92, v12, v20
	v_fmac_f32_e32 v92, v13, v21
	v_fmac_f32_e32 v92, v2, v22
	v_fmac_f32_e32 v92, v3, v23
	s_waitcnt lgkmcnt(0)
	v_fmac_f32_e32 v92, v8, v16
	v_fmac_f32_e32 v92, v9, v17
	v_fmac_f32_e32 v94, v14, v20
	v_fmac_f32_e32 v92, v0, v18
	v_fmac_f32_e32 v94, v15, v21
	v_fmac_f32_e32 v92, v1, v19
	v_cndmask_b32_e64 v1, v33, v165, s[2:3]
	v_fmac_f32_e32 v94, v6, v22
	v_mov_b32_e32 v2, v1
	v_mov_b32_e32 v3, v1
	v_fmac_f32_e32 v94, v7, v23
	s_nop 0
	v_permlane32_swap_b32_e32 v2, v3
	v_fmac_f32_e32 v94, v10, v16
	v_cmp_eq_u32_e32 vcc, v2, v1
	v_fmac_f32_e32 v94, v11, v17
	v_fmac_f32_e32 v94, v4, v18
	v_cndmask_b32_e32 v1, v2, v3, vcc
	v_cndmask_b32_e64 v2, v35, v167, s[2:3]
	v_mov_b32_e32 v3, v2
	v_mov_b32_e32 v4, v2
	s_nop 1
	v_permlane32_swap_b32_e32 v3, v4
	v_cmp_eq_u32_e32 vcc, v3, v2
	v_fmac_f32_e32 v94, v5, v19
	v_cndmask_b32_e64 v0, v165, v33, s[2:3]
	v_cndmask_b32_e32 v2, v3, v4, vcc
	v_cndmask_b32_e64 v3, v41, v169, s[2:3]
	v_mov_b32_e32 v4, v3
	v_mov_b32_e32 v5, v3
	s_nop 1
	v_permlane32_swap_b32_e32 v4, v5
	v_cmp_eq_u32_e32 vcc, v4, v3
	v_add_f32_e32 v0, v0, v1
	v_cndmask_b32_e64 v1, v167, v35, s[2:3]
	v_cndmask_b32_e32 v3, v4, v5, vcc
	v_cndmask_b32_e64 v4, v43, v171, s[2:3]
	v_mov_b32_e32 v5, v4
	v_mov_b32_e32 v6, v4
	s_nop 1
	v_permlane32_swap_b32_e32 v5, v6
	v_cmp_eq_u32_e32 vcc, v5, v4
	v_add_f32_e32 v1, v1, v2
	v_cndmask_b32_e64 v2, v169, v41, s[2:3]
	v_cndmask_b32_e32 v4, v5, v6, vcc
	v_cndmask_b32_e64 v5, v49, v173, s[2:3]
	v_mov_b32_e32 v6, v5
	v_mov_b32_e32 v7, v5
	s_nop 1
	v_permlane32_swap_b32_e32 v6, v7
	v_cmp_eq_u32_e32 vcc, v6, v5
	v_add_f32_e32 v2, v2, v3
	v_cndmask_b32_e64 v3, v171, v43, s[2:3]
	v_cndmask_b32_e32 v5, v6, v7, vcc
	v_cndmask_b32_e64 v6, v51, v175, s[2:3]
	v_mov_b32_e32 v7, v6
	v_mov_b32_e32 v8, v6
	s_nop 1
	v_permlane32_swap_b32_e32 v7, v8
	v_cmp_eq_u32_e32 vcc, v7, v6
	v_add_f32_e32 v3, v3, v4
	v_cndmask_b32_e64 v4, v173, v49, s[2:3]
	v_cndmask_b32_e32 v6, v7, v8, vcc
	v_cndmask_b32_e64 v7, v53, v184, s[2:3]
	v_mov_b32_e32 v8, v7
	v_mov_b32_e32 v9, v7
	s_nop 1
	v_permlane32_swap_b32_e32 v8, v9
	v_cmp_eq_u32_e32 vcc, v8, v7
	v_add_f32_e32 v4, v4, v5
	v_cndmask_b32_e64 v5, v175, v51, s[2:3]
	v_cndmask_b32_e32 v7, v8, v9, vcc
	v_cndmask_b32_e64 v8, v55, v92, s[2:3]
	v_mov_b32_e32 v9, v8
	v_mov_b32_e32 v10, v8
	s_nop 1
	v_permlane32_swap_b32_e32 v9, v10
	v_add_f32_e32 v5, v5, v6
	v_cndmask_b32_e64 v6, v184, v53, s[2:3]
	v_cmp_eq_u32_e32 vcc, v9, v8
	v_add_f32_e32 v6, v6, v7
	v_cndmask_b32_e64 v7, v92, v55, s[2:3]
	v_cndmask_b32_e32 v8, v9, v10, vcc
	v_add_f32_e32 v7, v7, v8
	v_cndmask_b32_e64 v11, v0, v4, s[4:5]
	v_cndmask_b32_e64 v0, v4, v0, s[4:5]
	v_cndmask_b32_e64 v4, v5, v1, s[4:5]
	v_cndmask_b32_e64 v1, v1, v5, s[4:5]
	v_cndmask_b32_e64 v5, v2, v6, s[4:5]
	v_cndmask_b32_e64 v8, v3, v7, s[4:5]
	ds_swizzle_b32 v11, v11 offset:swizzle(SWAP,16)
	ds_swizzle_b32 v1, v1 offset:swizzle(SWAP,16)
	ds_swizzle_b32 v5, v5 offset:swizzle(SWAP,16)
	ds_swizzle_b32 v8, v8 offset:swizzle(SWAP,16)
	v_cndmask_b32_e64 v2, v6, v2, s[4:5]
	v_cndmask_b32_e64 v3, v7, v3, s[4:5]
	s_waitcnt lgkmcnt(3)
	v_add_f32_e32 v0, v0, v11
	s_waitcnt lgkmcnt(2)
	v_add_f32_e32 v1, v4, v1
	s_waitcnt lgkmcnt(1)
	v_add_f32_e32 v2, v2, v5
	s_waitcnt lgkmcnt(0)
	v_add_f32_e32 v3, v3, v8
	v_cndmask_b32_e64 v4, v0, v2, s[6:7]
	v_cndmask_b32_e64 v5, v1, v3, s[6:7]
	ds_swizzle_b32 v4, v4 offset:swizzle(SWAP,8)
	ds_swizzle_b32 v5, v5 offset:swizzle(SWAP,8)
	v_cndmask_b32_e64 v0, v2, v0, s[6:7]
	v_cndmask_b32_e64 v1, v3, v1, s[6:7]
	s_waitcnt lgkmcnt(1)
	v_add_f32_e32 v0, v0, v4
	s_waitcnt lgkmcnt(0)
	v_add_f32_e32 v1, v1, v5
	v_cndmask_b32_e64 v2, v0, v1, s[8:9]
	ds_swizzle_b32 v2, v2 offset:swizzle(SWAP,4)
	v_cndmask_b32_e64 v0, v1, v0, s[8:9]
	s_waitcnt lgkmcnt(0)
	v_add_f32_e32 v0, v0, v2
	v_cndmask_b32_e64 v2, v32, v164, s[2:3]
	v_mov_b32_e32 v3, v2
	v_mov_b32_e32 v4, v2
	s_nop 1
	v_permlane32_swap_b32_e32 v3, v4
	v_cmp_eq_u32_e32 vcc, v3, v2
	ds_swizzle_b32 v1, v0 offset:swizzle(SWAP,1)
	s_waitcnt lgkmcnt(0)
	v_add_f32_e32 v0, v0, v1
	v_cndmask_b32_e32 v2, v3, v4, vcc
	v_cndmask_b32_e64 v3, v34, v166, s[2:3]
	v_mov_b32_e32 v4, v3
	v_mov_b32_e32 v5, v3
	s_nop 1
	v_permlane32_swap_b32_e32 v4, v5
	v_cmp_eq_u32_e32 vcc, v4, v3
	ds_swizzle_b32 v1, v0 offset:swizzle(SWAP,2)
	s_waitcnt lgkmcnt(0)
	v_add_f32_e32 v0, v0, v1
	v_cndmask_b32_e32 v3, v4, v5, vcc
	v_cndmask_b32_e64 v4, v40, v168, s[2:3]
	v_mov_b32_e32 v5, v4
	v_mov_b32_e32 v6, v4
	s_nop 1
	v_permlane32_swap_b32_e32 v5, v6
	v_cmp_eq_u32_e32 vcc, v5, v4
	v_cndmask_b32_e64 v1, v164, v32, s[2:3]
	v_add_f32_e32 v1, v1, v2
	v_cndmask_b32_e32 v4, v5, v6, vcc
	v_cndmask_b32_e64 v5, v42, v170, s[2:3]
	v_mov_b32_e32 v6, v5
	v_mov_b32_e32 v7, v5
	s_nop 1
	v_permlane32_swap_b32_e32 v6, v7
	v_cmp_eq_u32_e32 vcc, v6, v5
	v_cndmask_b32_e64 v2, v166, v34, s[2:3]
	v_add_f32_e32 v2, v2, v3
	v_cndmask_b32_e32 v5, v6, v7, vcc
	v_cndmask_b32_e64 v6, v48, v172, s[2:3]
	v_mov_b32_e32 v7, v6
	v_mov_b32_e32 v8, v6
	s_nop 1
	v_permlane32_swap_b32_e32 v7, v8
	v_cmp_eq_u32_e32 vcc, v7, v6
	v_cndmask_b32_e64 v3, v168, v40, s[2:3]
	v_add_f32_e32 v3, v3, v4
	v_cndmask_b32_e32 v6, v7, v8, vcc
	v_cndmask_b32_e64 v7, v50, v174, s[2:3]
	v_mov_b32_e32 v8, v7
	v_mov_b32_e32 v9, v7
	s_nop 1
	v_permlane32_swap_b32_e32 v8, v9
	v_cmp_eq_u32_e32 vcc, v8, v7
	v_cndmask_b32_e64 v4, v170, v42, s[2:3]
	v_add_f32_e32 v4, v4, v5
	v_cndmask_b32_e32 v7, v8, v9, vcc
	v_cndmask_b32_e64 v8, v52, v185, s[2:3]
	v_mov_b32_e32 v9, v8
	v_mov_b32_e32 v10, v8
	s_nop 1
	v_permlane32_swap_b32_e32 v9, v10
	v_cmp_eq_u32_e32 vcc, v9, v8
	v_cndmask_b32_e64 v5, v172, v48, s[2:3]
	v_add_f32_e32 v5, v5, v6
	v_cndmask_b32_e32 v8, v9, v10, vcc
	v_cndmask_b32_e64 v9, v54, v94, s[2:3]
	v_mov_b32_e32 v10, v9
	v_mov_b32_e32 v11, v9
	v_cndmask_b32_e64 v6, v174, v50, s[2:3]
	s_nop 0
	v_permlane32_swap_b32_e32 v10, v11
	v_add_f32_e32 v6, v6, v7
	v_cndmask_b32_e64 v7, v185, v52, s[2:3]
	v_cmp_eq_u32_e32 vcc, v10, v9
	v_add_f32_e32 v7, v7, v8
	v_cndmask_b32_e64 v8, v94, v54, s[2:3]
	v_cndmask_b32_e32 v9, v10, v11, vcc
	v_cndmask_b32_e64 v10, v1, v5, s[4:5]
	v_cndmask_b32_e64 v1, v5, v1, s[4:5]
	ds_swizzle_b32 v5, v0 offset:swizzle(SWAP,4)
	v_add_f32_e32 v8, v8, v9
	v_cndmask_b32_e64 v9, v2, v6, s[4:5]
	ds_swizzle_b32 v9, v9 offset:swizzle(SWAP,16)
	v_cndmask_b32_e64 v2, v6, v2, s[4:5]
	s_waitcnt lgkmcnt(1)
	v_max_f32_e32 v5, v5, v5
	v_max_f32_e32 v5, v0, v5
	ds_swizzle_b32 v10, v10 offset:swizzle(SWAP,16)
	s_waitcnt lgkmcnt(1)
	v_add_f32_e32 v6, v2, v9
	v_cndmask_b32_e64 v2, v3, v7, s[4:5]
	v_cndmask_b32_e64 v3, v7, v3, s[4:5]
	ds_swizzle_b32 v7, v5 offset:swizzle(SWAP,8)
	ds_swizzle_b32 v2, v2 offset:swizzle(SWAP,16)
	s_waitcnt lgkmcnt(2)
	v_add_f32_e32 v1, v1, v10
	s_waitcnt lgkmcnt(1)
	v_max_f32_e32 v7, v7, v7
	s_waitcnt lgkmcnt(0)
	v_add_f32_e32 v2, v3, v2
	v_cndmask_b32_e64 v3, v4, v8, s[4:5]
	v_max_f32_e32 v5, v5, v7
	ds_swizzle_b32 v3, v3 offset:swizzle(SWAP,16)
	ds_swizzle_b32 v7, v5 offset:swizzle(SWAP,16)
	v_cndmask_b32_e64 v4, v8, v4, s[4:5]
	s_waitcnt lgkmcnt(1)
	v_add_f32_e32 v3, v4, v3
	v_cndmask_b32_e64 v4, v2, v1, s[6:7]
	v_cndmask_b32_e64 v1, v1, v2, s[6:7]
	s_waitcnt lgkmcnt(0)
	v_max_f32_e32 v2, v7, v7
	v_max_f32_e32 v2, v5, v2
	v_mov_b32_e32 v5, v2
	v_mov_b32_e32 v7, v2
	s_nop 1
	v_permlane32_swap_b32_e32 v5, v7
	v_cmp_eq_u32_e32 vcc, v5, v2
	ds_swizzle_b32 v1, v1 offset:swizzle(SWAP,8)
	s_waitcnt lgkmcnt(0)
	v_add_f32_e32 v1, v4, v1
	v_cndmask_b32_e32 v5, v5, v7, vcc
	v_max_f32_e32 v5, v5, v5
	v_max_f32_e32 v2, v2, v5
	v_sub_f32_e32 v0, v0, v2
	v_mul_f32_e32 v2, 0x3fb8aa3b, v0
	v_fma_f32 v5, v0, s31, -v2
	v_rndne_f32_e32 v7, v2
	v_fmac_f32_e32 v5, 0x32a5705f, v0
	v_sub_f32_e32 v2, v2, v7
	v_add_f32_e32 v2, v2, v5
	v_exp_f32_e32 v2, v2
	v_cvt_i32_f32_e32 v5, v7
	v_cndmask_b32_e64 v4, v6, v3, s[6:7]
	ds_swizzle_b32 v4, v4 offset:swizzle(SWAP,8)
	v_cmp_ngt_f32_e32 vcc, s34, v0
	v_ldexp_f32 v2, v2, v5
	v_cndmask_b32_e64 v3, v3, v6, s[6:7]
	v_cndmask_b32_e32 v2, 0, v2, vcc
	v_cmp_nlt_f32_e32 vcc, s35, v0
	s_waitcnt lgkmcnt(0)
	v_add_f32_e32 v3, v3, v4
	v_cndmask_b32_e64 v4, v1, v3, s[8:9]
	v_cndmask_b32_e32 v2, v163, v2, vcc
	ds_swizzle_b32 v0, v2 offset:swizzle(SWAP,4)
	ds_swizzle_b32 v4, v4 offset:swizzle(SWAP,4)
	v_cndmask_b32_e64 v1, v3, v1, s[8:9]
	s_waitcnt lgkmcnt(1)
	v_add_f32_e32 v0, v2, v0
	ds_swizzle_b32 v5, v0 offset:swizzle(SWAP,8)
	s_waitcnt lgkmcnt(1)
	v_add_f32_e32 v1, v1, v4
	ds_swizzle_b32 v3, v1 offset:swizzle(SWAP,1)
	s_waitcnt lgkmcnt(1)
	v_add_f32_e32 v0, v0, v5
	ds_swizzle_b32 v5, v0 offset:swizzle(SWAP,16)
	s_waitcnt lgkmcnt(1)
	v_add_f32_e32 v3, v1, v3
	ds_swizzle_b32 v4, v3 offset:swizzle(SWAP,2)
	s_waitcnt lgkmcnt(1)
	v_add_f32_e32 v5, v0, v5
	v_mov_b32_e32 v6, v5
	v_mov_b32_e32 v7, v5
	s_nop 1
	v_permlane32_swap_b32_e32 v6, v7
	v_lshl_add_u64 v[0:1], s[18:19], 0, v[74:75]
	s_and_saveexec_b64 s[12:13], s[10:11]
	s_cbranch_execz .LBB0_955
	v_cmp_eq_u32_e32 vcc, v6, v5
	s_nop 1
	v_cndmask_b32_e32 v6, v6, v7, vcc
	v_add_f32_e32 v5, v5, v6
	v_div_scale_f32 v6, s[14:15], v5, v5, v2
	v_rcp_f32_e32 v7, v6
	s_nop 0
	v_fma_f32 v8, -v6, v7, 1.0
	v_fmac_f32_e32 v7, v8, v7
	v_div_scale_f32 v8, vcc, v2, v5, v2
	v_mul_f32_e32 v9, v8, v7
	v_fma_f32 v10, -v6, v9, v8
	v_fmac_f32_e32 v9, v10, v7
	v_fma_f32 v6, -v6, v9, v8
	v_div_fmas_f32 v6, v6, v7, v9
	v_div_fixup_f32 v2, v6, v5, v2
	v_add_co_u32_e32 v6, vcc, 0x3c800000, v0
	s_nop 1
	v_addc_co_u32_e32 v7, vcc, 0, v1, vcc
	global_store_dword v[6:7], v2, off

.LBB0_1345:
	s_ashr_i32 s11, s10, 31
	s_lshl_b64 s[4:5], s[10:11], 13
	v_lshl_add_u64 v[148:149], v[64:65], 0, s[4:5]
	v_add_co_u32_e32 v0, vcc, 0x1000, v148
	global_load_dwordx4 v[60:63], v[148:149], off nt
	global_load_dwordx4 v[56:59], v[148:149], off offset:1024 nt
	global_load_dwordx4 v[52:55], v[148:149], off offset:2048 nt
	global_load_dwordx4 v[48:51], v[148:149], off offset:3072 nt
	v_addc_co_u32_e32 v1, vcc, 0, v149, vcc
	global_load_dwordx4 v[44:47], v[0:1], off nt
	global_load_dwordx4 v[40:43], v[0:1], off offset:1024 nt
	global_load_dwordx4 v[36:39], v[0:1], off offset:2048 nt
	global_load_dwordx4 v[32:35], v[0:1], off offset:3072 nt
	v_mov_b32_e32 v152, -1
	v_mov_b32_e32 v153, -1
	s_and_saveexec_b64 s[4:5], s[2:3]
	s_cbranch_execz .LBB0_1347
	s_lshl_b64 s[22:23], s[10:11], 6
	v_lshl_add_u64 v[0:1], v[66:67], 0, s[22:23]
	global_load_dword v153, v[0:1], off nt
.LBB0_1347:
	s_or_b64 exec, exec, s[4:5]
	s_or_b32 s22, s10, 1
	s_ashr_i32 s23, s22, 31
	s_lshl_b64 s[4:5], s[22:23], 13
	v_lshl_add_u64 v[150:151], v[64:65], 0, s[4:5]
	v_add_co_u32_e32 v0, vcc, 0x1000, v150
	global_load_dwordx4 v[28:31], v[150:151], off nt
	global_load_dwordx4 v[24:27], v[150:151], off offset:1024 nt
	global_load_dwordx4 v[20:23], v[150:151], off offset:2048 nt
	global_load_dwordx4 v[16:19], v[150:151], off offset:3072 nt
	v_addc_co_u32_e32 v1, vcc, 0, v151, vcc
	global_load_dwordx4 v[12:15], v[0:1], off nt
	global_load_dwordx4 v[8:11], v[0:1], off offset:1024 nt
	global_load_dwordx4 v[4:7], v[0:1], off offset:2048 nt
	s_nop 0
	global_load_dwordx4 v[0:3], v[0:1], off offset:3072 nt
	s_and_saveexec_b64 s[4:5], s[2:3]
	s_cbranch_execz .LBB0_1349
	s_lshl_b64 s[24:25], s[22:23], 6
	v_lshl_add_u64 v[154:155], v[66:67], 0, s[24:25]
	global_load_dword v152, v[154:155], off nt

.LBB0_1352:
	v_sub_co_u32_e64 v154, s[28:29], s5, 1
	s_nop 0
	v_readfirstlane_b32 s24, v154
	s_and_b64 vcc, exec, s[28:29]
	s_cbranch_vccnz .LBB0_1354
	s_ff1_i32_b32 s25, s5
	v_readlane_b32 s26, v153, s25
	s_add_i32 s25, s25, s34
	s_lshl_b32 s25, s25, 9
	s_add_i32 s26, s26, s25
	s_ashr_i32 s27, s26, 31
	s_lshl_b64 s[26:27], s[26:27], 12
	s_waitcnt vmcnt(0)
	v_lshl_add_u64 v[132:133], v[68:69], 0, s[26:27]
	global_load_dwordx2 v[146:147], v[132:133], off nt
	global_load_dwordx2 v[144:145], v[132:133], off offset:512 nt
	global_load_dwordx2 v[142:143], v[132:133], off offset:1024 nt
	global_load_dwordx2 v[140:141], v[132:133], off offset:1536 nt
	global_load_dwordx2 v[138:139], v[132:133], off offset:2048 nt
	global_load_dwordx2 v[136:137], v[132:133], off offset:2560 nt
	global_load_dwordx2 v[134:135], v[132:133], off offset:3072 nt
	s_nop 0
	global_load_dwordx2 v[132:133], v[132:133], off offset:3584 nt
.LBB0_1354:
	s_and_b32 s35, s24, s5
	v_sub_co_u32_e64 v154, s[26:27], s35, 1
	s_nop 0
	v_readfirstlane_b32 s36, v154
	s_and_b64 vcc, exec, s[26:27]
	s_cbranch_vccnz .LBB0_1356
	s_ff1_i32_b32 s5, s35
	v_readlane_b32 s24, v153, s5
	s_add_i32 s5, s5, s34
	s_lshl_b32 s5, s5, 9
	s_add_i32 s24, s24, s5
	s_ashr_i32 s25, s24, 31
	s_lshl_b64 s[24:25], s[24:25], 12
	s_waitcnt vmcnt(0)
	v_lshl_add_u64 v[116:117], v[68:69], 0, s[24:25]
	global_load_dwordx2 v[130:131], v[116:117], off nt
	global_load_dwordx2 v[128:129], v[116:117], off offset:512 nt
	global_load_dwordx2 v[126:127], v[116:117], off offset:1024 nt
	global_load_dwordx2 v[124:125], v[116:117], off offset:1536 nt
	global_load_dwordx2 v[122:123], v[116:117], off offset:2048 nt
	global_load_dwordx2 v[120:121], v[116:117], off offset:2560 nt
	global_load_dwordx2 v[118:119], v[116:117], off offset:3072 nt
	s_nop 0
	global_load_dwordx2 v[116:117], v[116:117], off offset:3584 nt
.LBB0_1356:
	v_sub_co_u32_e64 v154, s[24:25], s4, 1
	s_nop 0
	v_readfirstlane_b32 s5, v154
	s_and_b64 vcc, exec, s[24:25]
	s_cbranch_vccnz .LBB0_1358
	s_ff1_i32_b32 s37, s4
	v_readlane_b32 s38, v152, s37
	s_add_i32 s37, s37, s34
	s_lshl_b32 s37, s37, 9
	s_add_i32 s38, s38, s37
	s_ashr_i32 s39, s38, 31
	s_lshl_b64 s[38:39], s[38:39], 12
	s_waitcnt vmcnt(0)
	v_lshl_add_u64 v[100:101], v[68:69], 0, s[38:39]
	global_load_dwordx2 v[114:115], v[100:101], off nt
	global_load_dwordx2 v[112:113], v[100:101], off offset:512 nt
	global_load_dwordx2 v[110:111], v[100:101], off offset:1024 nt
	global_load_dwordx2 v[108:109], v[100:101], off offset:1536 nt
	global_load_dwordx2 v[106:107], v[100:101], off offset:2048 nt
	global_load_dwordx2 v[104:105], v[100:101], off offset:2560 nt
	global_load_dwordx2 v[102:103], v[100:101], off offset:3072 nt
	s_nop 0
	global_load_dwordx2 v[100:101], v[100:101], off offset:3584 nt

.LBB0_1363:
	s_ff1_i32_b32 s39, s37
	v_readlane_b32 s40, v152, s39
	s_add_i32 s39, s39, s34
	s_lshl_b32 s39, s39, 9
	s_add_i32 s40, s40, s39
	s_ashr_i32 s41, s40, 31
	s_lshl_b64 s[40:41], s[40:41], 12
	s_waitcnt vmcnt(0)
	v_lshl_add_u64 v[84:85], v[68:69], 0, s[40:41]
	global_load_dwordx2 v[98:99], v[84:85], off nt
	global_load_dwordx2 v[96:97], v[84:85], off offset:512 nt
	global_load_dwordx2 v[94:95], v[84:85], off offset:1024 nt
	global_load_dwordx2 v[92:93], v[84:85], off offset:1536 nt
	global_load_dwordx2 v[90:91], v[84:85], off offset:2048 nt
	global_load_dwordx2 v[88:89], v[84:85], off offset:2560 nt
	global_load_dwordx2 v[86:87], v[84:85], off offset:3072 nt
	s_nop 0
	global_load_dwordx2 v[84:85], v[84:85], off offset:3584 nt
	s_xor_b64 s[28:29], s[28:29], -1
	s_andn2_b64 vcc, exec, s[28:29]
	s_cbranch_vccnz .LBB0_1360

.LBB0_1368:
	s_and_b64 vcc, exec, s[12:13]
	v_lshl_add_u64 v[160:161], v[148:149], 0, s[14:15]
	v_lshl_add_u64 v[162:163], v[148:149], 0, s[16:17]
	v_lshl_add_u64 v[164:165], v[148:149], 0, s[18:19]
	v_lshl_add_u64 v[166:167], v[148:149], 0, s[20:21]
	v_lshl_add_u64 v[152:153], v[150:151], 0, s[14:15]
	v_lshl_add_u64 v[154:155], v[150:151], 0, s[16:17]
	v_lshl_add_u64 v[156:157], v[150:151], 0, s[18:19]
	v_lshl_add_u64 v[158:159], v[150:151], 0, s[20:21]
	global_store_dwordx4 v[148:149], v[60:63], off
	global_store_dwordx4 v[148:149], v[56:59], off offset:1024
	global_store_dwordx4 v[148:149], v[52:55], off offset:2048
	global_store_dwordx4 v[148:149], v[48:51], off offset:3072
	global_store_dwordx4 v[160:161], v[44:47], off
	global_store_dwordx4 v[162:163], v[40:43], off
	global_store_dwordx4 v[164:165], v[36:39], off
	global_store_dwordx4 v[166:167], v[32:35], off
	global_store_dwordx4 v[150:151], v[28:31], off
	global_store_dwordx4 v[150:151], v[24:27], off offset:1024
	global_store_dwordx4 v[150:151], v[20:23], off offset:2048
	global_store_dwordx4 v[150:151], v[16:19], off offset:3072
	global_store_dwordx4 v[152:153], v[12:15], off
	global_store_dwordx4 v[154:155], v[8:11], off
	global_store_dwordx4 v[156:157], v[4:7], off
	global_store_dwordx4 v[158:159], v[0:3], off
	s_cbranch_vccz .LBB0_1344
	v_mul_f32_e32 v148, v61, v61
	v_mul_f32_e32 v149, v63, v63
	v_fmac_f32_e32 v148, v60, v60
	v_fmac_f32_e32 v149, v62, v62
	v_add_f32_e32 v148, v148, v149
	v_mul_f32_e32 v149, v57, v57
	v_mul_f32_e32 v150, v59, v59
	v_fmac_f32_e32 v149, v56, v56
	v_fmac_f32_e32 v150, v58, v58
	v_add_f32_e32 v149, v149, v150
	v_add_f32_e32 v148, v149, v148
	v_mul_f32_e32 v149, v53, v53
	v_mul_f32_e32 v150, v55, v55
	v_fmac_f32_e32 v149, v52, v52
	v_fmac_f32_e32 v150, v54, v54
	v_add_f32_e32 v149, v149, v150
	v_add_f32_e32 v148, v149, v148
	v_mul_f32_e32 v149, v49, v49
	v_mul_f32_e32 v150, v51, v51
	v_fmac_f32_e32 v149, v48, v48
	v_fmac_f32_e32 v150, v50, v50
	v_add_f32_e32 v149, v149, v150
	v_add_f32_e32 v148, v149, v148
	v_mul_f32_e32 v149, v45, v45
	v_mul_f32_e32 v150, v47, v47
	v_fmac_f32_e32 v149, v44, v44
	v_fmac_f32_e32 v150, v46, v46
	v_add_f32_e32 v149, v149, v150
	v_add_f32_e32 v148, v149, v148
	v_mul_f32_e32 v149, v41, v41
	v_mul_f32_e32 v150, v43, v43
	v_fmac_f32_e32 v149, v40, v40
	v_fmac_f32_e32 v150, v42, v42
	v_add_f32_e32 v149, v149, v150
	v_add_f32_e32 v148, v149, v148
	v_mul_f32_e32 v149, v37, v37
	v_mul_f32_e32 v150, v39, v39
	v_fmac_f32_e32 v149, v36, v36
	v_fmac_f32_e32 v150, v38, v38
	v_add_f32_e32 v149, v149, v150
	v_add_f32_e32 v152, v149, v148
	global_load_dwordx4 v[148:151], v[70:71], off nt
	v_mul_f32_e32 v153, v33, v33
	v_mul_f32_e32 v154, v35, v35
	v_fmac_f32_e32 v153, v32, v32
	v_fmac_f32_e32 v154, v34, v34
	v_add_f32_e32 v153, v153, v154
	v_add_f32_e32 v152, v153, v152
	ds_swizzle_b32 v153, v152 offset:swizzle(SWAP,1)
	s_lshl_b64 s[22:23], s[22:23], 12
	s_waitcnt lgkmcnt(0)
	v_add_f32_e32 v152, v152, v153
	ds_swizzle_b32 v153, v152 offset:swizzle(SWAP,2)
	s_waitcnt lgkmcnt(0)
	v_add_f32_e32 v152, v152, v153
	ds_swizzle_b32 v153, v152 offset:swizzle(SWAP,4)
	s_waitcnt lgkmcnt(0)
	v_add_f32_e32 v152, v152, v153
	ds_swizzle_b32 v153, v152 offset:swizzle(SWAP,8)
	s_waitcnt lgkmcnt(0)
	v_add_f32_e32 v152, v152, v153
	ds_swizzle_b32 v153, v152 offset:swizzle(SWAP,16)
	s_waitcnt lgkmcnt(0)
	v_add_f32_e32 v152, v152, v153
	v_mov_b32_e32 v153, v152
	s_nop 1
	v_permlane32_swap_b32_e32 v152, v153
	v_add_f32_e32 v152, v152, v153
	v_fmamk_f32 v152, v152, 0x3a000000, v73
	v_mul_f32_e32 v153, 0x4f800000, v152
	v_cmp_gt_f32_e32 vcc, s31, v152
	s_nop 1
	v_cndmask_b32_e32 v152, v152, v153, vcc
	v_sqrt_f32_e32 v153, v152
	s_nop 0
	v_add_u32_e32 v154, -1, v153
	v_fma_f32 v155, -v154, v153, v152
	v_cmp_ge_f32_e64 s[4:5], 0, v155
	v_add_u32_e32 v155, 1, v153
	s_nop 0
	v_cndmask_b32_e64 v154, v153, v154, s[4:5]
	v_fma_f32 v153, -v155, v153, v152
	v_cmp_lt_f32_e64 s[4:5], 0, v153
	s_nop 1
	v_cndmask_b32_e64 v153, v154, v155, s[4:5]
	v_mul_f32_e32 v154, 0x37800000, v153
	v_cndmask_b32_e32 v153, v153, v154, vcc
	v_cmp_class_f32_e32 vcc, v152, v168
	s_nop 1
	v_cndmask_b32_e32 v152, v153, v152, vcc
	v_div_scale_f32 v153, s[4:5], v152, v152, 1.0
	v_rcp_f32_e32 v154, v153
	s_lshl_b64 s[4:5], s[10:11], 12
	v_fma_f32 v155, -v153, v154, 1.0
	v_fmac_f32_e32 v154, v155, v154
	v_div_scale_f32 v155, vcc, 1.0, v152, 1.0
	v_mul_f32_e32 v156, v155, v154
	v_fma_f32 v157, -v153, v156, v155
	v_fmac_f32_e32 v156, v157, v154
	v_fma_f32 v153, -v153, v156, v155
	v_div_fmas_f32 v153, v153, v154, v156
	v_div_fixup_f32 v152, v153, v152, 1.0
	v_pk_mul_f32 v[60:61], v[60:61], v[152:153] op_sel_hi:[1,0]
	v_pk_mul_f32 v[62:63], v[62:63], v[152:153] op_sel_hi:[1,0]
	s_waitcnt vmcnt(0)
	v_pk_mul_f32 v[60:61], v[148:149], v[60:61]
	v_pk_mul_f32 v[62:63], v[150:151], v[62:63]
	v_lshl_add_u64 v[154:155], v[82:83], 0, s[4:5]
	v_cvt_pk_bf16_f32 v60, v60, v61
	v_cvt_pk_bf16_f32 v61, v62, v63
	global_store_dwordx2 v[154:155], v[60:61], off
	global_load_dwordx4 v[60:63], v[70:71], off offset:1024 nt
	v_pk_mul_f32 v[56:57], v[56:57], v[152:153] op_sel_hi:[1,0]
	v_pk_mul_f32 v[58:59], v[58:59], v[152:153] op_sel_hi:[1,0]
	v_pk_mul_f32 v[52:53], v[52:53], v[152:153] op_sel_hi:[1,0]
	v_pk_mul_f32 v[54:55], v[54:55], v[152:153] op_sel_hi:[1,0]
	v_pk_mul_f32 v[48:49], v[48:49], v[152:153] op_sel_hi:[1,0]
	v_pk_mul_f32 v[50:51], v[50:51], v[152:153] op_sel_hi:[1,0]
	v_pk_mul_f32 v[44:45], v[44:45], v[152:153] op_sel_hi:[1,0]
	v_pk_mul_f32 v[46:47], v[46:47], v[152:153] op_sel_hi:[1,0]
	v_pk_mul_f32 v[40:41], v[40:41], v[152:153] op_sel_hi:[1,0]
	v_pk_mul_f32 v[42:43], v[42:43], v[152:153] op_sel_hi:[1,0]
	v_pk_mul_f32 v[36:37], v[36:37], v[152:153] op_sel_hi:[1,0]
	v_pk_mul_f32 v[38:39], v[38:39], v[152:153] op_sel_hi:[1,0]
	v_pk_mul_f32 v[32:33], v[32:33], v[152:153] op_sel_hi:[1,0]
	v_pk_mul_f32 v[34:35], v[34:35], v[152:153] op_sel_hi:[1,0]
	s_waitcnt vmcnt(0)
	v_pk_mul_f32 v[56:57], v[60:61], v[56:57]
	v_pk_mul_f32 v[58:59], v[62:63], v[58:59]
	v_cvt_pk_bf16_f32 v56, v56, v57
	v_cvt_pk_bf16_f32 v57, v58, v59
	global_store_dwordx2 v[154:155], v[56:57], off offset:512
	global_load_dwordx4 v[56:59], v[70:71], off offset:2048 nt
	s_waitcnt vmcnt(0)
	v_pk_mul_f32 v[52:53], v[56:57], v[52:53]
	v_pk_mul_f32 v[54:55], v[58:59], v[54:55]
	v_cvt_pk_bf16_f32 v52, v52, v53
	v_cvt_pk_bf16_f32 v53, v54, v55
	global_store_dwordx2 v[154:155], v[52:53], off offset:1024
	global_load_dwordx4 v[52:55], v[70:71], off offset:3072 nt
	s_waitcnt vmcnt(0)
	v_pk_mul_f32 v[48:49], v[48:49], v[52:53]
	v_pk_mul_f32 v[50:51], v[50:51], v[54:55]
	v_cvt_pk_bf16_f32 v48, v48, v49
	v_cvt_pk_bf16_f32 v49, v50, v51
	global_store_dwordx2 v[154:155], v[48:49], off offset:1536
	global_load_dwordx4 v[48:51], v[74:75], off nt
	v_mul_f32_e32 v52, v5, v5
	v_mul_f32_e32 v53, v7, v7
	v_mul_f32_e32 v54, v1, v1
	v_mul_f32_e32 v55, v3, v3
	v_fmac_f32_e32 v52, v4, v4
	v_fmac_f32_e32 v53, v6, v6
	v_fmac_f32_e32 v54, v0, v0
	v_fmac_f32_e32 v55, v2, v2
	s_waitcnt vmcnt(0)
	v_pk_mul_f32 v[44:45], v[44:45], v[48:49]
	v_pk_mul_f32 v[46:47], v[46:47], v[50:51]
	v_cvt_pk_bf16_f32 v44, v44, v45
	v_cvt_pk_bf16_f32 v45, v46, v47
	global_store_dwordx2 v[154:155], v[44:45], off offset:2048
	global_load_dwordx4 v[44:47], v[76:77], off nt
	v_mul_f32_e32 v48, v13, v13
	v_mul_f32_e32 v49, v15, v15
	v_mul_f32_e32 v50, v9, v9
	v_mul_f32_e32 v51, v11, v11
	v_fmac_f32_e32 v48, v12, v12
	v_fmac_f32_e32 v49, v14, v14
	v_fmac_f32_e32 v50, v8, v8
	v_fmac_f32_e32 v51, v10, v10
	s_waitcnt vmcnt(0)
	v_pk_mul_f32 v[40:41], v[40:41], v[44:45]
	v_pk_mul_f32 v[42:43], v[42:43], v[46:47]
	v_cvt_pk_bf16_f32 v40, v40, v41
	v_cvt_pk_bf16_f32 v41, v42, v43
	global_store_dwordx2 v[154:155], v[40:41], off offset:2560
	global_load_dwordx4 v[40:43], v[78:79], off nt
	v_mul_f32_e32 v44, v21, v21
	v_mul_f32_e32 v45, v23, v23
	v_mul_f32_e32 v46, v17, v17
	v_mul_f32_e32 v47, v19, v19
	v_fmac_f32_e32 v44, v20, v20
	v_fmac_f32_e32 v45, v22, v22
	v_fmac_f32_e32 v46, v16, v16
	v_fmac_f32_e32 v47, v18, v18
	s_waitcnt vmcnt(0)
	v_pk_mul_f32 v[36:37], v[36:37], v[40:41]
	v_pk_mul_f32 v[38:39], v[38:39], v[42:43]
	v_cvt_pk_bf16_f32 v36, v36, v37
	v_cvt_pk_bf16_f32 v37, v38, v39
	global_store_dwordx2 v[154:155], v[36:37], off offset:3072
	global_load_dwordx4 v[36:39], v[80:81], off nt
	v_mul_f32_e32 v40, v29, v29
	v_mul_f32_e32 v41, v31, v31
	v_mul_f32_e32 v42, v25, v25
	v_mul_f32_e32 v43, v27, v27
	v_fmac_f32_e32 v40, v28, v28
	v_fmac_f32_e32 v41, v30, v30
	v_fmac_f32_e32 v42, v24, v24
	v_fmac_f32_e32 v43, v26, v26
	v_add_f32_e32 v40, v40, v41
	v_add_f32_e32 v41, v42, v43
	v_add_f32_e32 v42, v44, v45
	v_add_f32_e32 v43, v46, v47
	v_add_f32_e32 v44, v48, v49
	v_add_f32_e32 v45, v50, v51
	v_add_f32_e32 v46, v52, v53
	s_waitcnt vmcnt(0)
	v_pk_mul_f32 v[32:33], v[32:33], v[36:37]
	v_pk_mul_f32 v[34:35], v[34:35], v[38:39]
	v_cvt_pk_bf16_f32 v32, v32, v33
	v_cvt_pk_bf16_f32 v33, v34, v35
	global_store_dwordx2 v[154:155], v[32:33], off offset:3584
	global_load_dwordx4 v[32:35], v[70:71], off nt
	v_add_f32_e32 v37, v41, v40
	v_add_f32_e32 v37, v37, v42
	v_add_f32_e32 v37, v37, v43
	v_add_f32_e32 v37, v37, v44
	v_add_f32_e32 v37, v37, v45
	v_add_f32_e32 v36, v54, v55
	v_add_f32_e32 v37, v37, v46
	v_add_f32_e32 v36, v37, v36
	ds_swizzle_b32 v37, v36 offset:swizzle(SWAP,1)
	s_waitcnt lgkmcnt(0)
	v_add_f32_e32 v36, v36, v37
	ds_swizzle_b32 v37, v36 offset:swizzle(SWAP,2)
	s_waitcnt lgkmcnt(0)
	v_add_f32_e32 v36, v36, v37
	ds_swizzle_b32 v37, v36 offset:swizzle(SWAP,4)
	s_waitcnt lgkmcnt(0)
	v_add_f32_e32 v36, v36, v37
	ds_swizzle_b32 v37, v36 offset:swizzle(SWAP,8)
	s_waitcnt lgkmcnt(0)
	v_add_f32_e32 v36, v36, v37
	ds_swizzle_b32 v37, v36 offset:swizzle(SWAP,16)
	s_waitcnt lgkmcnt(0)
	v_add_f32_e32 v36, v36, v37
	v_mov_b32_e32 v37, v36
	s_nop 1
	v_permlane32_swap_b32_e32 v36, v37
	v_add_f32_e32 v36, v36, v37
	v_fmamk_f32 v36, v36, 0x3a000000, v73
	v_mul_f32_e32 v37, 0x4f800000, v36
	v_cmp_gt_f32_e32 vcc, s31, v36
	s_nop 1
	v_cndmask_b32_e32 v36, v36, v37, vcc
	v_sqrt_f32_e32 v37, v36
	s_nop 0
	v_add_u32_e32 v38, -1, v37
	v_add_u32_e32 v39, 1, v37
	v_fma_f32 v40, -v38, v37, v36
	v_fma_f32 v41, -v39, v37, v36
	v_cmp_ge_f32_e64 s[4:5], 0, v40
	s_nop 1
	v_cndmask_b32_e64 v37, v37, v38, s[4:5]
	v_cmp_lt_f32_e64 s[4:5], 0, v41
	s_nop 1
	v_cndmask_b32_e64 v37, v37, v39, s[4:5]
	v_mul_f32_e32 v38, 0x37800000, v37
	v_cndmask_b32_e32 v37, v37, v38, vcc
	v_cmp_class_f32_e32 vcc, v36, v168
	s_nop 1
	v_cndmask_b32_e32 v38, v37, v36, vcc
	v_div_scale_f32 v39, s[4:5], v38, v38, 1.0
	v_rcp_f32_e32 v40, v39
	v_div_scale_f32 v41, vcc, 1.0, v38, 1.0
	v_lshl_add_u64 v[36:37], v[82:83], 0, s[22:23]
	v_fma_f32 v42, -v39, v40, 1.0
	v_fmac_f32_e32 v40, v42, v40
	v_mul_f32_e32 v42, v41, v40
	v_fma_f32 v43, -v39, v42, v41
	v_fmac_f32_e32 v42, v43, v40
	v_fma_f32 v39, -v39, v42, v41
	v_div_fmas_f32 v39, v39, v40, v42
	v_div_fixup_f32 v38, v39, v38, 1.0
	v_pk_mul_f32 v[28:29], v[28:29], v[38:39] op_sel_hi:[1,0]
	v_pk_mul_f32 v[30:31], v[30:31], v[38:39] op_sel_hi:[1,0]
	s_waitcnt vmcnt(0)
	v_pk_mul_f32 v[28:29], v[32:33], v[28:29]
	v_pk_mul_f32 v[30:31], v[34:35], v[30:31]
	v_cvt_pk_bf16_f32 v28, v28, v29
	v_cvt_pk_bf16_f32 v29, v30, v31
	global_store_dwordx2 v[36:37], v[28:29], off
	global_load_dwordx4 v[28:31], v[70:71], off offset:1024 nt
	v_pk_mul_f32 v[24:25], v[24:25], v[38:39] op_sel_hi:[1,0]
	v_pk_mul_f32 v[26:27], v[26:27], v[38:39] op_sel_hi:[1,0]
	v_pk_mul_f32 v[20:21], v[20:21], v[38:39] op_sel_hi:[1,0]
	v_pk_mul_f32 v[22:23], v[22:23], v[38:39] op_sel_hi:[1,0]
	v_pk_mul_f32 v[16:17], v[16:17], v[38:39] op_sel_hi:[1,0]
	v_pk_mul_f32 v[18:19], v[18:19], v[38:39] op_sel_hi:[1,0]
	v_pk_mul_f32 v[12:13], v[12:13], v[38:39] op_sel_hi:[1,0]
	v_pk_mul_f32 v[14:15], v[14:15], v[38:39] op_sel_hi:[1,0]
	v_pk_mul_f32 v[8:9], v[8:9], v[38:39] op_sel_hi:[1,0]
	v_pk_mul_f32 v[10:11], v[10:11], v[38:39] op_sel_hi:[1,0]
	v_pk_mul_f32 v[4:5], v[4:5], v[38:39] op_sel_hi:[1,0]
	v_pk_mul_f32 v[6:7], v[6:7], v[38:39] op_sel_hi:[1,0]
	v_pk_mul_f32 v[0:1], v[0:1], v[38:39] op_sel_hi:[1,0]
	v_pk_mul_f32 v[2:3], v[2:3], v[38:39] op_sel_hi:[1,0]
	s_waitcnt vmcnt(0)
	v_pk_mul_f32 v[24:25], v[28:29], v[24:25]
	v_pk_mul_f32 v[26:27], v[30:31], v[26:27]
	v_cvt_pk_bf16_f32 v24, v24, v25
	v_cvt_pk_bf16_f32 v25, v26, v27
	global_store_dwordx2 v[36:37], v[24:25], off offset:512
	global_load_dwordx4 v[24:27], v[70:71], off offset:2048 nt
	s_waitcnt vmcnt(0)
	v_pk_mul_f32 v[20:21], v[24:25], v[20:21]
	v_pk_mul_f32 v[22:23], v[26:27], v[22:23]
	v_cvt_pk_bf16_f32 v20, v20, v21
	v_cvt_pk_bf16_f32 v21, v22, v23
	global_store_dwordx2 v[36:37], v[20:21], off offset:1024
	global_load_dwordx4 v[20:23], v[70:71], off offset:3072 nt
	s_waitcnt vmcnt(0)
	v_pk_mul_f32 v[16:17], v[16:17], v[20:21]
	v_pk_mul_f32 v[18:19], v[18:19], v[22:23]
	v_cvt_pk_bf16_f32 v16, v16, v17
	v_cvt_pk_bf16_f32 v17, v18, v19
	global_store_dwordx2 v[36:37], v[16:17], off offset:1536
	global_load_dwordx4 v[16:19], v[74:75], off nt
	s_waitcnt vmcnt(0)
	v_pk_mul_f32 v[12:13], v[12:13], v[16:17]
	v_pk_mul_f32 v[14:15], v[14:15], v[18:19]
	v_cvt_pk_bf16_f32 v12, v12, v13
	v_cvt_pk_bf16_f32 v13, v14, v15
	global_store_dwordx2 v[36:37], v[12:13], off offset:2048
	global_load_dwordx4 v[12:15], v[76:77], off nt
	s_waitcnt vmcnt(0)
	v_pk_mul_f32 v[8:9], v[8:9], v[12:13]
	v_pk_mul_f32 v[10:11], v[10:11], v[14:15]
	v_cvt_pk_bf16_f32 v8, v8, v9
	v_cvt_pk_bf16_f32 v9, v10, v11
	global_store_dwordx2 v[36:37], v[8:9], off offset:2560
	global_load_dwordx4 v[8:11], v[78:79], off nt
	s_waitcnt vmcnt(0)
	v_pk_mul_f32 v[4:5], v[4:5], v[8:9]
	v_pk_mul_f32 v[6:7], v[6:7], v[10:11]
	v_cvt_pk_bf16_f32 v4, v4, v5
	v_cvt_pk_bf16_f32 v5, v6, v7
	global_store_dwordx2 v[36:37], v[4:5], off offset:3072
	global_load_dwordx4 v[4:7], v[80:81], off nt
	s_waitcnt vmcnt(0)
	v_pk_mul_f32 v[0:1], v[0:1], v[4:5]
	v_pk_mul_f32 v[2:3], v[2:3], v[6:7]
	v_cvt_pk_bf16_f32 v0, v0, v1
	v_cvt_pk_bf16_f32 v1, v2, v3
	global_store_dwordx2 v[36:37], v[0:1], off offset:3584
	s_branch .LBB0_1344

.LBB0_1393:
	v_lshlrev_b32_e32 v0, 2, v72
	v_and_b32_e32 v73, 28, v0
	v_mov_b32_e32 v4, 0
	v_or_b32_e32 v0, s12, v73
	v_mov_b32_e32 v6, v4
	v_mov_b32_e32 v7, v4
	v_ashrrev_i32_e32 v74, 3, v72
	v_ashrrev_i32_e32 v1, 31, v0
	v_mov_b32_e32 v5, v4
	v_mov_b64_e32 v[14:15], v[6:7]
	v_mov_b64_e32 v[10:11], v[6:7]
	v_cmp_gt_i32_e32 vcc, s13, v0
	v_add_u32_e32 v30, s4, v74
	v_lshl_add_u64 v[28:29], v[0:1], 2, s[10:11]
	v_mov_b64_e32 v[12:13], v[4:5]
	v_mov_b64_e32 v[8:9], v[4:5]
	s_and_saveexec_b64 s[4:5], vcc
	s_cbranch_execz .LBB0_1395
	v_mad_u64_u32 v[0:1], s[10:11], v30, s13, 0
	v_ashrrev_i32_e32 v3, 31, v30
	v_mov_b32_e32 v2, v1
	v_mad_u64_u32 v[2:3], s[10:11], v3, s13, v[2:3]
	v_mov_b32_e32 v1, v2
	v_add_u32_e32 v2, 8, v30
	v_ashrrev_i32_e32 v9, 31, v2
	v_mad_u64_u32 v[2:3], s[10:11], v2, s13, 0
	v_mov_b32_e32 v8, v3
	v_mad_u64_u32 v[8:9], s[10:11], v9, s13, v[8:9]
	v_lshl_add_u64 v[0:1], v[0:1], 2, v[28:29]
	v_mov_b32_e32 v3, v8
	v_lshl_add_u64 v[2:3], v[2:3], 2, v[28:29]
	global_load_dwordx4 v[12:15], v[0:1], off nt
	global_load_dwordx4 v[8:11], v[2:3], off nt
.LBB0_1395:
	s_or_b64 exec, exec, s[4:5]
	v_mov_b64_e32 v[18:19], v[6:7]
	v_mov_b64_e32 v[16:17], v[4:5]
	s_and_saveexec_b64 s[4:5], vcc
	s_cbranch_execz .LBB0_1397
	v_add_u32_e32 v0, 16, v30
	v_ashrrev_i32_e32 v3, 31, v0
	v_mad_u64_u32 v[0:1], s[10:11], v0, s13, 0
	v_mov_b32_e32 v2, v1
	v_mad_u64_u32 v[2:3], s[10:11], v3, s13, v[2:3]
	v_mov_b32_e32 v1, v2
	v_add_u32_e32 v2, 24, v30
	v_ashrrev_i32_e32 v5, 31, v2
	v_mad_u64_u32 v[2:3], s[10:11], v2, s13, 0
	v_mov_b32_e32 v4, v3
	v_mad_u64_u32 v[4:5], s[10:11], v5, s13, v[4:5]
	v_lshl_add_u64 v[0:1], v[0:1], 2, v[28:29]
	v_mov_b32_e32 v3, v4
	v_lshl_add_u64 v[2:3], v[2:3], 2, v[28:29]
	global_load_dwordx4 v[4:7], v[0:1], off nt
	global_load_dwordx4 v[16:19], v[2:3], off nt
.LBB0_1397:
	s_or_b64 exec, exec, s[4:5]
	v_mov_b32_e32 v1, 0
	v_mov_b32_e32 v2, v1
	v_mov_b32_e32 v3, v1
	v_mov_b32_e32 v0, v1
	v_mov_b64_e32 v[26:27], v[2:3]
	v_mov_b64_e32 v[22:23], v[2:3]
	v_mov_b64_e32 v[24:25], v[0:1]
	v_mov_b64_e32 v[20:21], v[0:1]
	s_and_saveexec_b64 s[4:5], vcc
	s_cbranch_execz .LBB0_1399
	v_add_u32_e32 v0, 32, v30
	v_mad_u64_u32 v[2:3], s[10:11], v0, s13, 0
	v_ashrrev_i32_e32 v20, 31, v0
	v_mov_b32_e32 v0, v3
	v_mad_u64_u32 v[20:21], s[10:11], v20, s13, v[0:1]
	v_add_u32_e32 v0, 40, v30
	v_mov_b32_e32 v3, v20
	v_mad_u64_u32 v[20:21], s[10:11], v0, s13, 0
	v_ashrrev_i32_e32 v22, 31, v0
	v_mov_b32_e32 v0, v21
	v_mad_u64_u32 v[22:23], s[10:11], v22, s13, v[0:1]
	v_lshl_add_u64 v[2:3], v[2:3], 2, v[28:29]
	v_mov_b32_e32 v21, v22
	v_lshl_add_u64 v[32:33], v[20:21], 2, v[28:29]
	global_load_dwordx4 v[24:27], v[2:3], off nt
	global_load_dwordx4 v[20:23], v[32:33], off nt
.LBB0_1399:
	s_or_b64 exec, exec, s[4:5]
	v_mov_b32_e32 v32, 0
	v_mov_b32_e32 v33, 0
	v_mov_b32_e32 v34, 0
	v_mov_b32_e32 v35, 0
	v_mov_b32_e32 v36, 0
	v_mov_b32_e32 v37, 0
	v_mov_b32_e32 v38, 0
	v_mov_b32_e32 v39, 0
	s_and_saveexec_b64 s[4:5], vcc
	s_cbranch_execz .LBB0_1401
	v_add_u32_e32 v0, 48, v30
	v_mad_u64_u32 v[2:3], s[10:11], v0, s13, 0
	v_ashrrev_i32_e32 v31, 31, v0
	v_mov_b32_e32 v0, v3
	v_mad_u64_u32 v[32:33], s[10:11], v31, s13, v[0:1]
	v_add_u32_e32 v0, 56, v30
	v_mad_u64_u32 v[30:31], s[10:11], v0, s13, 0
	v_mov_b32_e32 v3, v32
	v_ashrrev_i32_e32 v32, 31, v0
	v_mov_b32_e32 v0, v31
	v_mad_u64_u32 v[32:33], s[10:11], v32, s13, v[0:1]
	v_lshl_add_u64 v[2:3], v[2:3], 2, v[28:29]
	v_mov_b32_e32 v31, v32
	v_lshl_add_u64 v[28:29], v[30:31], 2, v[28:29]
	global_load_dwordx4 v[36:39], v[2:3], off nt
	global_load_dwordx4 v[32:35], v[28:29], off nt

.LBB0_1425:
	v_or_b32_e32 v30, s14, v73
	v_ashrrev_i32_e32 v31, 31, v30
	v_cmp_gt_i32_e32 vcc, s4, v30
	v_lshl_add_u64 v[82:83], v[30:31], 2, s[16:17]
	v_mov_b32_e32 v30, v28
	v_mov_b32_e32 v31, v28
	v_mov_b32_e32 v29, v28
	v_mov_b64_e32 v[42:43], v[30:31]
	v_mov_b64_e32 v[46:47], v[30:31]
	v_add_u32_e32 v85, s18, v74
	v_mov_b64_e32 v[40:41], v[28:29]
	v_mov_b64_e32 v[44:45], v[28:29]
	s_and_saveexec_b64 s[14:15], vcc
	s_cbranch_execz .LBB0_1427
	v_mad_u64_u32 v[40:41], s[16:17], v85, s4, 0
	v_ashrrev_i32_e32 v43, 31, v85
	v_mov_b32_e32 v42, v41
	v_mad_u64_u32 v[42:43], s[16:17], v43, s4, v[42:43]
	v_mov_b32_e32 v41, v42
	v_lshl_add_u64 v[48:49], v[40:41], 2, v[82:83]
	v_add_u32_e32 v40, 8, v85
	v_ashrrev_i32_e32 v43, 31, v40
	v_mad_u64_u32 v[40:41], s[16:17], v40, s4, 0
	v_mov_b32_e32 v42, v41
	v_mad_u64_u32 v[42:43], s[16:17], v43, s4, v[42:43]
	v_mov_b32_e32 v41, v42
	v_lshl_add_u64 v[50:51], v[40:41], 2, v[82:83]
	global_load_dwordx4 v[40:43], v[48:49], off nt
	global_load_dwordx4 v[44:47], v[50:51], off nt
.LBB0_1427:
	s_or_b64 exec, exec, s[14:15]
	v_mov_b64_e32 v[50:51], v[30:31]
	v_mov_b64_e32 v[54:55], v[30:31]
	v_mov_b64_e32 v[48:49], v[28:29]
	v_mov_b64_e32 v[52:53], v[28:29]
	s_and_saveexec_b64 s[14:15], vcc
	s_cbranch_execz .LBB0_1429
	v_add_u32_e32 v29, 16, v85
	v_mad_u64_u32 v[30:31], s[16:17], v29, s4, 0
	v_ashrrev_i32_e32 v49, 31, v29
	v_mov_b32_e32 v48, v31
	v_mad_u64_u32 v[48:49], s[16:17], v49, s4, v[48:49]
	v_add_u32_e32 v29, 24, v85
	v_mov_b32_e32 v31, v48
	v_mad_u64_u32 v[48:49], s[16:17], v29, s4, 0
	v_ashrrev_i32_e32 v51, 31, v29
	v_mov_b32_e32 v50, v49
	v_mad_u64_u32 v[50:51], s[16:17], v51, s4, v[50:51]
	v_lshl_add_u64 v[30:31], v[30:31], 2, v[82:83]
	v_mov_b32_e32 v49, v50
	v_lshl_add_u64 v[56:57], v[48:49], 2, v[82:83]
	global_load_dwordx4 v[48:51], v[30:31], off nt
	global_load_dwordx4 v[52:55], v[56:57], off nt
.LBB0_1429:
	s_or_b64 exec, exec, s[14:15]
	v_mov_b32_e32 v30, v28
	v_mov_b32_e32 v31, v28
	v_mov_b32_e32 v29, v28
	v_mov_b64_e32 v[58:59], v[30:31]
	v_mov_b64_e32 v[62:63], v[30:31]
	v_mov_b64_e32 v[56:57], v[28:29]
	v_mov_b64_e32 v[60:61], v[28:29]
	s_and_saveexec_b64 s[14:15], vcc
	s_cbranch_execz .LBB0_1431
	v_add_u32_e32 v29, 32, v85
	v_mad_u64_u32 v[30:31], s[16:17], v29, s4, 0
	v_ashrrev_i32_e32 v57, 31, v29
	v_mov_b32_e32 v56, v31
	v_mad_u64_u32 v[56:57], s[16:17], v57, s4, v[56:57]
	v_add_u32_e32 v29, 40, v85
	v_mov_b32_e32 v31, v56
	v_mad_u64_u32 v[56:57], s[16:17], v29, s4, 0
	v_ashrrev_i32_e32 v59, 31, v29
	v_mov_b32_e32 v58, v57
	v_mad_u64_u32 v[58:59], s[16:17], v59, s4, v[58:59]
	v_lshl_add_u64 v[30:31], v[30:31], 2, v[82:83]
	v_mov_b32_e32 v57, v58
	v_lshl_add_u64 v[64:65], v[56:57], 2, v[82:83]
	global_load_dwordx4 v[56:59], v[30:31], off nt
	global_load_dwordx4 v[60:63], v[64:65], off nt
.LBB0_1431:
	s_or_b64 exec, exec, s[14:15]
	v_mov_b32_e32 v67, 0
	v_mov_b32_e32 v66, 0
	v_mov_b32_e32 v65, 0
	v_mov_b32_e32 v64, 0
	v_mov_b32_e32 v71, 0
	v_mov_b32_e32 v70, 0
	v_mov_b32_e32 v69, 0
	v_mov_b32_e32 v68, 0
	s_and_saveexec_b64 s[14:15], vcc
	s_cbranch_execz .LBB0_1402
	v_add_u32_e32 v29, 48, v85
	v_mad_u64_u32 v[30:31], s[16:17], v29, s4, 0
	v_ashrrev_i32_e32 v65, 31, v29
	v_mov_b32_e32 v64, v31
	v_mad_u64_u32 v[64:65], s[16:17], v65, s4, v[64:65]
	v_add_u32_e32 v29, 56, v85
	v_mov_b32_e32 v31, v64
	v_mad_u64_u32 v[64:65], s[16:17], v29, s4, 0
	v_ashrrev_i32_e32 v67, 31, v29
	v_mov_b32_e32 v66, v65
	v_mad_u64_u32 v[66:67], s[16:17], v67, s4, v[66:67]
	v_lshl_add_u64 v[30:31], v[30:31], 2, v[82:83]
	v_mov_b32_e32 v65, v66
	v_lshl_add_u64 v[82:83], v[64:65], 2, v[82:83]
	global_load_dwordx4 v[64:67], v[30:31], off nt
	global_load_dwordx4 v[68:71], v[82:83], off nt
	s_branch .LBB0_1402

.LBB0_1435:
	v_ashrrev_i32_e32 v4, 11, v0
	v_and_b32_e32 v5, 0x7ff0, v1
	v_add_u32_e32 v4, v5, v4
	v_ashrrev_i32_e32 v5, 31, v4
	v_lshl_add_u64 v[4:5], v[4:5], 2, s[4:5]
	global_load_dword v4, v[4:5], off nt
	v_add_u32_e32 v0, s6, v0
	v_cmp_lt_i32_e32 vcc, s12, v0
	v_add_u32_e32 v1, s7, v1
	s_or_b64 s[10:11], vcc, s[10:11]
	s_waitcnt vmcnt(0)
	global_store_dword v[2:3], v4, off
	v_lshl_add_u64 v[2:3], v[2:3], 0, s[8:9]
	s_andn2_b64 exec, exec, s[10:11]
	s_cbranch_execnz .LBB0_1435

.LBB0_2005:
	s_or_b64 exec, exec, s[4:5]
	s_mov_b64 s[2:3], s[0:1]
	v_mbcnt_lo_u32_b32 v0, -1, 0
	v_mbcnt_hi_u32_b32 v0, -1, v0
	s_lshl_b32 s4, s33, 4
	s_lshl_b32 s5, s63, 1
	s_add_i32 s42, s4, s5
	s_cmpk_gt_i32 s42, 0x3fff
	s_cbranch_scc1 .LBB0_2008
	s_load_dwordx2 s[4:5], s[2:3], 0x88
	s_load_dwordx2 s[44:45], s[2:3], 0xf0
	v_lshlrev_b32_e32 v2, 1, v0
	v_ashrrev_i32_e32 v3, 31, v2
	v_lshlrev_b64 v[6:7], 2, v[2:3]
	s_waitcnt lgkmcnt(0)
	v_lshl_add_u64 v[0:1], s[4:5], 0, v[6:7]
	global_load_dwordx2 v[0:1], v[0:1], off offset:512 nt
	s_ashr_i32 s43, s42, 31
	s_lshl_b32 s46, s62, 4
	s_lshl_b64 s[2:3], s[42:43], 12
	v_lshlrev_b64 v[4:5], 1, v[2:3]
	v_mov_b32_e32 v8, 0x3600
	v_lshl_add_u64 v[2:3], s[2:3], 0, v[4:5]
	s_ashr_i32 s47, s46, 31
	v_mad_i64_i32 v[4:5], s[2:3], s42, v8, v[4:5]
	v_mov_b32_e32 v8, 0xc00
	s_lshl_b64 s[48:49], s[46:47], 12
	s_mul_i32 s50, s62, 0x36000
	s_mul_hi_i32 s51, s46, 0x3600
	v_mad_i64_i32 v[6:7], s[2:3], s42, v8, v[6:7]
	s_mul_i32 s52, s62, 0xc000
	s_mul_hi_i32 s53, s46, 0xc00
	s_mov_b32 s43, 0x14606000
	s_mov_b32 s47, 0x36801000
	s_mov_b32 s54, 0x39801000
	v_mov_b32_e32 v60, 0x358637bd
	s_mov_b32 s55, 0xf800000
	v_mov_b32_e32 v61, 0x260
	s_mov_b32 s56, 0x22000000
	s_mov_b32 s57, 0x22001000

.LBB0_2703:
	s_ashr_i32 s3, s2, 31
	s_lshl_b64 s[12:13], s[2:3], 13
	v_lshl_add_u64 v[134:135], v[64:65], 0, s[12:13]
	v_add_co_u32_e32 v32, vcc, 0x1000, v134
	global_load_dwordx4 v[12:15], v[134:135], off nt
	global_load_dwordx4 v[8:11], v[134:135], off offset:1024 nt
	global_load_dwordx4 v[4:7], v[134:135], off offset:2048 nt
	global_load_dwordx4 v[0:3], v[134:135], off offset:3072 nt
	v_addc_co_u32_e32 v33, vcc, 0, v135, vcc
	global_load_dwordx4 v[28:31], v[32:33], off nt
	global_load_dwordx4 v[24:27], v[32:33], off offset:1024 nt
	global_load_dwordx4 v[20:23], v[32:33], off offset:2048 nt
	global_load_dwordx4 v[16:19], v[32:33], off offset:3072 nt
	v_mov_b32_e32 v138, -1
	v_mov_b32_e32 v139, -1
	s_and_saveexec_b64 s[12:13], s[0:1]
	s_cbranch_execz .LBB0_2705
	s_lshl_b64 s[14:15], s[2:3], 6
	v_lshl_add_u64 v[32:33], v[66:67], 0, s[14:15]
	global_load_dword v139, v[32:33], off nt
.LBB0_2705:
	s_or_b64 exec, exec, s[12:13]
	s_or_b32 s12, s2, 1
	s_ashr_i32 s13, s12, 31
	s_lshl_b64 s[14:15], s[12:13], 13
	v_lshl_add_u64 v[136:137], v[64:65], 0, s[14:15]
	v_add_co_u32_e32 v48, vcc, 0x1000, v136
	global_load_dwordx4 v[36:39], v[136:137], off nt
	global_load_dwordx4 v[32:35], v[136:137], off offset:1024 nt
	global_load_dwordx4 v[40:43], v[136:137], off offset:2048 nt
	global_load_dwordx4 v[44:47], v[136:137], off offset:3072 nt
	v_addc_co_u32_e32 v49, vcc, 0, v137, vcc
	global_load_dwordx4 v[52:55], v[48:49], off nt
	global_load_dwordx4 v[56:59], v[48:49], off offset:1024 nt
	global_load_dwordx4 v[60:63], v[48:49], off offset:2048 nt
	s_nop 0
	global_load_dwordx4 v[48:51], v[48:49], off offset:3072 nt
	s_and_saveexec_b64 s[14:15], s[0:1]
	s_cbranch_execz .LBB0_2707
	s_lshl_b64 s[12:13], s[12:13], 6
	v_lshl_add_u64 v[140:141], v[66:67], 0, s[12:13]
	global_load_dword v138, v[140:141], off nt

.LBB0_2710:
	v_sub_co_u32_e64 v140, s[18:19], s13, 1
	s_nop 0
	v_readfirstlane_b32 s14, v140
	s_and_b64 vcc, exec, s[18:19]
	s_cbranch_vccnz .LBB0_2712
	s_ff1_i32_b32 s15, s13
	v_readlane_b32 s16, v139, s15
	s_add_i32 s15, s15, s3
	s_lshl_b32 s15, s15, 9
	s_add_i32 s16, s16, s15
	s_ashr_i32 s17, s16, 31
	s_lshl_b64 s[16:17], s[16:17], 12
	s_waitcnt vmcnt(0)
	v_lshl_add_u64 v[118:119], v[68:69], 0, s[16:17]
	global_load_dwordx2 v[132:133], v[118:119], off nt
	global_load_dwordx2 v[130:131], v[118:119], off offset:512 nt
	global_load_dwordx2 v[128:129], v[118:119], off offset:1024 nt
	global_load_dwordx2 v[126:127], v[118:119], off offset:1536 nt
	global_load_dwordx2 v[124:125], v[118:119], off offset:2048 nt
	global_load_dwordx2 v[122:123], v[118:119], off offset:2560 nt
	global_load_dwordx2 v[120:121], v[118:119], off offset:3072 nt
	s_nop 0
	global_load_dwordx2 v[118:119], v[118:119], off offset:3584 nt
.LBB0_2712:
	s_and_b32 s21, s14, s13
	v_sub_co_u32_e64 v140, s[16:17], s21, 1
	s_nop 0
	v_readfirstlane_b32 s22, v140
	s_and_b64 vcc, exec, s[16:17]
	s_cbranch_vccnz .LBB0_2714
	s_ff1_i32_b32 s13, s21
	v_readlane_b32 s14, v139, s13
	s_add_i32 s13, s13, s3
	s_lshl_b32 s13, s13, 9
	s_add_i32 s14, s14, s13
	s_ashr_i32 s15, s14, 31
	s_lshl_b64 s[14:15], s[14:15], 12
	s_waitcnt vmcnt(0)
	v_lshl_add_u64 v[102:103], v[68:69], 0, s[14:15]
	global_load_dwordx2 v[116:117], v[102:103], off nt
	global_load_dwordx2 v[114:115], v[102:103], off offset:512 nt
	global_load_dwordx2 v[112:113], v[102:103], off offset:1024 nt
	global_load_dwordx2 v[110:111], v[102:103], off offset:1536 nt
	global_load_dwordx2 v[108:109], v[102:103], off offset:2048 nt
	global_load_dwordx2 v[106:107], v[102:103], off offset:2560 nt
	global_load_dwordx2 v[104:105], v[102:103], off offset:3072 nt
	s_nop 0
	global_load_dwordx2 v[102:103], v[102:103], off offset:3584 nt
.LBB0_2714:
	v_sub_co_u32_e64 v140, s[14:15], s12, 1
	s_nop 0
	v_readfirstlane_b32 s13, v140
	s_and_b64 vcc, exec, s[14:15]
	s_cbranch_vccnz .LBB0_2716
	s_ff1_i32_b32 s23, s12
	v_readlane_b32 s24, v138, s23
	s_add_i32 s23, s23, s3
	s_lshl_b32 s23, s23, 9
	s_add_i32 s24, s24, s23
	s_ashr_i32 s25, s24, 31
	s_lshl_b64 s[24:25], s[24:25], 12
	s_waitcnt vmcnt(0)
	v_lshl_add_u64 v[86:87], v[68:69], 0, s[24:25]
	global_load_dwordx2 v[100:101], v[86:87], off nt
	global_load_dwordx2 v[98:99], v[86:87], off offset:512 nt
	global_load_dwordx2 v[96:97], v[86:87], off offset:1024 nt
	global_load_dwordx2 v[94:95], v[86:87], off offset:1536 nt
	global_load_dwordx2 v[92:93], v[86:87], off offset:2048 nt
	global_load_dwordx2 v[90:91], v[86:87], off offset:2560 nt
	global_load_dwordx2 v[88:89], v[86:87], off offset:3072 nt
	s_nop 0
	global_load_dwordx2 v[86:87], v[86:87], off offset:3584 nt

.LBB0_2721:
	s_ff1_i32_b32 s25, s23
	v_readlane_b32 s26, v138, s25
	s_add_i32 s25, s25, s3
	s_lshl_b32 s25, s25, 9
	s_add_i32 s26, s26, s25
	s_ashr_i32 s27, s26, 31
	s_lshl_b64 s[26:27], s[26:27], 12
	s_waitcnt vmcnt(0)
	v_lshl_add_u64 v[70:71], v[68:69], 0, s[26:27]
	global_load_dwordx2 v[84:85], v[70:71], off nt
	global_load_dwordx2 v[82:83], v[70:71], off offset:512 nt
	global_load_dwordx2 v[80:81], v[70:71], off offset:1024 nt
	global_load_dwordx2 v[78:79], v[70:71], off offset:1536 nt
	global_load_dwordx2 v[76:77], v[70:71], off offset:2048 nt
	global_load_dwordx2 v[74:75], v[70:71], off offset:2560 nt
	global_load_dwordx2 v[72:73], v[70:71], off offset:3072 nt
	s_nop 0
	global_load_dwordx2 v[70:71], v[70:71], off offset:3584 nt
	s_xor_b64 s[18:19], s[18:19], -1
	s_andn2_b64 vcc, exec, s[18:19]
	s_cbranch_vccnz .LBB0_2718
